# v7 + GEMM units: first two counted waits after an epilogue tolerate its output stores (vmcnt 8 -> 8+NS under a flag)
# speedup vs baseline: 1.0037x; 1.0037x over previous
; #define PH_END   if (ph + 1 < hi) { for (int br_ = 0; br_ < BAR_REP; ++br_) xcd_barrier(bar); } } ++ph;
; __global__ void __launch_bounds__(NTHREADS, 2) fwd_kernel(Args args) {
;     ...
;         const int kind = layer % 3, jl = layer / 3;
;         const bool last = layer == DEPTH - 1, ctx_out = !last;
;         const int rows_out = ctx_out ? MROWS : NLAT;
;         PH_BEGIN for (int rep_ = 0; rep_ < REPN(1); ++rep_) if (EN(1)) { if (layer == 0 && rep_ == 0) norm_phase<false, true>(F, A, layer, false, MROWS); else norm_phase<false, false>(F, A, layer, layer > 0, MROWS, rep_ == 0 ? 1.0f : 0.0f); } PH_END
;         if (kind == 0) {
;     ...
;         } else {
;             PH_BEGIN for (int rep_ = 0; rep_ < REPN(13); ++rep_) if (EN(13)) { pg8::Gemm g{H, (const bf16*)(F.ws + WS_SG_WIN), MROWS, 4096, 1024}; pg8::StaticOrder S; S.init(MROWS, 4096, F.G, (int)blockIdx.x);
.LBB0_376:
	v_readlane_b32 s0, v252, 32
	v_readlane_b32 s1, v252, 33
	s_cmp_eq_u32 s0, 3
	s_mov_b32 s2, s0
	s_cselect_b64 s[0:1], -1, 0
	v_writelane_b32 v252, s0, 34
	s_nop 1
	v_writelane_b32 v252, s1, 35
	s_and_b64 s[0:1], s[0:1], exec
	s_cselect_b32 s1, 0, s2
	s_mov_b32 s0, 0x8000
	s_cselect_b32 s46, s0, 0x8800
	v_writelane_b32 v252, s1, 36
	s_cmp_lt_i32 s1, 1
	s_mov_b64 s[0:1], -1
	s_cbranch_scc1 .LBB0_1114
	v_readlane_b32 s0, v252, 36
	s_cmp_lg_u32 s0, 1
	s_mov_b64 s[0:1], -1
	s_cbranch_scc0 .LBB0_679
	s_mov_b32 s97, 0
	v_readlane_b32 s4, v251, 10
	v_readlane_b32 s5, v251, 11
	s_cmp_ge_i32 s40, s4
	s_cselect_b64 s[0:1], -1, 0
	s_cmp_lt_i32 s40, s5
	s_cselect_b64 s[4:5], -1, 0
	s_and_b64 s[4:5], s[0:1], s[4:5]
	s_mov_b64 s[0:1], -1
	s_and_b64 vcc, exec, s[4:5]
	s_cbranch_vccnz .LBB0_380
	s_add_i32 s2, s44, 2
	s_mov_b64 s[0:1], 0

; #define PG8_STAGE(bufoff, gbase, voff) do { _Pragma("unroll") for (int _i = 0; _i < 2; ++_i) \
;         __builtin_amdgcn_global_load_lds((const unsigned*)((const char*)(gbase) + (voff)[_i]), (PG8_LAS unsigned*)(lds + (bufoff) + ldsw + _i * 8192), 16, 0, 0); } while (0)
; #define PG8_LDA(dst, b, h) do { _Pragma("unroll") for (int m = 0; m < 4; ++m) _Pragma("unroll") for (int k = 0; k < 2; ++k) dst[m][k] = *(const PG8_LAS bf16x8*)(lds + PG8_SA(b, h) + aoff + m * 2048 + k * 1024); } while (0)
; #define PG8_LDB(dst, b, h) do { _Pragma("unroll") for (int n = 0; n < 2; ++n) _Pragma("unroll") for (int k = 0; k < 2; ++k) dst[n][k] = *(const PG8_LAS bf16x8*)(lds + PG8_SB(b, h) + boff + n * 2048 + k * 1024); } while (0)
; #define PG8_MMA(ai, bj, At, Bt) do { __builtin_amdgcn_s_setprio(1); _Pragma("unroll") for (int m = 0; m < 4; ++m) _Pragma("unroll") for (int n = 0; n < 2; ++n) _Pragma("unroll") for (int k = 0; k < 2; ++k) \
;         acc[ai][bj][m][n] = __builtin_amdgcn_mfma_f32_16x16x32_bf16(Bt[n][k], At[m][k], acc[ai][bj][m][n], 0, 0, 0); __builtin_amdgcn_s_setprio(0); } while (0)
; #define PG8_WAIT_V(n) asm volatile("s_waitcnt vmcnt(" #n ")" ::: "memory")
; #define PG8_BAR __builtin_amdgcn_s_barrier()
; template <class Epi, class Sched, bool ALIGN_EPI = false, bool SP2 = false, bool GATHER = false>
; __device__ __forceinline__ void gemm_phase(PG8_LAS unsigned char* lds, const Gemm g, const Sched& S, const Epi& E, int tid_in, const int* rowsrc = nullptr, PG8_LAS int* idx_lds = nullptr) {
;     ...
;         for (int t = 0; t < nt; t += 2) {
;             const bool last = (t == nt - 2);
;             if constexpr (GATHER) {
; #pragma unroll
;                 for (int h_ = 0; h_ < 2; ++h_) { gS[h_][0] = last ? gN[h_][0] : gA[h_][0]; gS[h_][1] = last ? gN[h_][1] : gA[h_][1]; } }
;             const char* a1 = cA + (size_t)(t + 1) * kstep;
;             const char* a2 = last ? nA : cA + (size_t)(t + 2) * kstep; const char* b2 = last ? nB : cB + (size_t)(t + 2) * kstep;
;             const char* a3 = a2 + kstep; const char* b3 = b2 + kstep;
;             if (last && has_next) S.a_ready(nxt);
;             if constexpr (SP2) {
;             PG8_LDB(B0, 0, 0); PG8_LDB(B1, 0, 1); PG8_SCHED; PG8_LDA(At, 0, 0); PG8_STAGE(PG8_SA(1, 1), a1 + hstepA, PG8_OA(1));
;             PG8_WAIT_V(8); PG8_WAIT_L(0); PG8_BAR; PG8_MMA(0, 0, At, B0); PG8_MMA(0, 1, At, B1); PG8_BAR; PG8_SCHED;
.LBB0_390:
	s_add_u32 s20, s18, 0xfffc0080
	s_addc_u32 s21, s19, -1
	s_add_i32 s52, 0, 0x10000
	s_cmp_eq_u32 s51, 12
	s_cselect_b32 s23, s13, s21
	s_cselect_b32 s22, s47, s20
	v_add_u32_e32 v144, s52, v149
	s_cselect_b32 s21, s9, s50
	s_cselect_b32 s20, s48, s49
	s_add_i32 s54, 0, 0x14000
	ds_read_b128 v[140:143], v144
	ds_read_b128 v[152:155], v144 offset:1024
	ds_read_b128 v[156:159], v144 offset:2048
	ds_read_b128 v[160:163], v144 offset:3072
	v_add_u32_e32 v144, s54, v149
	ds_read_b128 v[164:167], v144
	ds_read_b128 v[168:171], v144 offset:1024
	ds_read_b128 v[172:175], v144 offset:2048
	ds_read_b128 v[176:179], v144 offset:3072
	v_lshl_add_u64 v[144:145], s[18:19], 0, v[136:137]
	s_add_i32 m0, s29, 0xc000
	ds_read_b128 v[180:183], v151
	ds_read_b128 v[184:187], v151 offset:1024
	ds_read_b128 v[188:191], v151 offset:2048
	ds_read_b128 v[192:195], v151 offset:3072
	ds_read_b128 v[196:199], v151 offset:4096
	ds_read_b128 v[200:203], v151 offset:5120
	ds_read_b128 v[204:207], v151 offset:6144
	ds_read_b128 v[208:211], v151 offset:7168
	global_load_lds_dwordx4 v[144:145], off
	v_lshl_add_u64 v[144:145], s[18:19], 0, v[138:139]
	s_add_i32 m0, s29, 0xe000
	s_nop 0
	global_load_lds_dwordx4 v[144:145], off
	s_cmp_eq_u32 s97, 0
	s_cbranch_scc1 .Lew1_a
	s_waitcnt vmcnt(24)
	s_branch .Lew1_b

; #define PG8_STAGE(bufoff, gbase, voff) do { _Pragma("unroll") for (int _i = 0; _i < 2; ++_i) \
;         __builtin_amdgcn_global_load_lds((const unsigned*)((const char*)(gbase) + (voff)[_i]), (PG8_LAS unsigned*)(lds + (bufoff) + ldsw + _i * 8192), 16, 0, 0); } while (0)
; #define PG8_LDA(dst, b, h) do { _Pragma("unroll") for (int m = 0; m < 4; ++m) _Pragma("unroll") for (int k = 0; k < 2; ++k) dst[m][k] = *(const PG8_LAS bf16x8*)(lds + PG8_SA(b, h) + aoff + m * 2048 + k * 1024); } while (0)
; #define PG8_LDB(dst, b, h) do { _Pragma("unroll") for (int n = 0; n < 2; ++n) _Pragma("unroll") for (int k = 0; k < 2; ++k) dst[n][k] = *(const PG8_LAS bf16x8*)(lds + PG8_SB(b, h) + boff + n * 2048 + k * 1024); } while (0)
; #define PG8_MMA(ai, bj, At, Bt) do { __builtin_amdgcn_s_setprio(1); _Pragma("unroll") for (int m = 0; m < 4; ++m) _Pragma("unroll") for (int n = 0; n < 2; ++n) _Pragma("unroll") for (int k = 0; k < 2; ++k) \
;         acc[ai][bj][m][n] = __builtin_amdgcn_mfma_f32_16x16x32_bf16(Bt[n][k], At[m][k], acc[ai][bj][m][n], 0, 0, 0); __builtin_amdgcn_s_setprio(0); } while (0)
; #define PG8_WAIT_V(n) asm volatile("s_waitcnt vmcnt(" #n ")" ::: "memory")
; #define PG8_WAIT_L(n) asm volatile("s_waitcnt lgkmcnt(" #n ")" ::: "memory")
; #define PG8_BAR __builtin_amdgcn_s_barrier()
; #define PG8_SCHED __builtin_amdgcn_sched_barrier(0)
; template <class Epi, class Sched, bool ALIGN_EPI = false, bool SP2 = false, bool GATHER = false>
; __device__ __forceinline__ void gemm_phase(PG8_LAS unsigned char* lds, const Gemm g, const Sched& S, const Epi& E, int tid_in, const int* rowsrc = nullptr, PG8_LAS int* idx_lds = nullptr) {
;     ...
;             PG8_LDB(B0, 0, 0); PG8_LDB(B1, 0, 1); PG8_SCHED; PG8_LDA(At, 0, 0); PG8_STAGE(PG8_SA(1, 1), a1 + hstepA, PG8_OA(1));
;             PG8_WAIT_V(8); PG8_WAIT_L(0); PG8_BAR; PG8_MMA(0, 0, At, B0); PG8_MMA(0, 1, At, B1); PG8_BAR; PG8_SCHED;
;             PG8_LDA(At, 0, 1); PG8_STAGE(PG8_SB(0, 0), b2, voffB); PG8_STAGE(PG8_SB(0, 1), b2 + hstep, voffB); PG8_STAGE(PG8_SA(0, 0), a2, PG8_OS(0));
.Lew1_b:
	s_waitcnt lgkmcnt(0)
	v_mfma_f32_16x16x32_bf16 v[126:129], v[140:143], v[180:183], v[126:129]
	v_mfma_f32_16x16x32_bf16 v[122:125], v[156:159], v[180:183], v[122:125]
	v_mfma_f32_16x16x32_bf16 v[110:113], v[140:143], v[188:191], v[110:113]
	s_barrier
	s_setprio 1
	s_waitcnt lgkmcnt(0)
	v_mfma_f32_16x16x32_bf16 v[106:109], v[156:159], v[188:191], v[106:109]
	v_mfma_f32_16x16x32_bf16 v[94:97], v[140:143], v[196:199], v[94:97]
	v_mfma_f32_16x16x32_bf16 v[90:93], v[156:159], v[196:199], v[90:93]
	v_mfma_f32_16x16x32_bf16 v[78:81], v[140:143], v[204:207], v[78:81]
	v_mfma_f32_16x16x32_bf16 v[74:77], v[156:159], v[204:207], v[74:77]
	v_mfma_f32_16x16x32_bf16 v[126:129], v[152:155], v[184:187], v[126:129]
	v_mfma_f32_16x16x32_bf16 v[122:125], v[160:163], v[184:187], v[122:125]
	v_mfma_f32_16x16x32_bf16 v[110:113], v[152:155], v[192:195], v[110:113]
	v_mfma_f32_16x16x32_bf16 v[106:109], v[160:163], v[192:195], v[106:109]
	v_mfma_f32_16x16x32_bf16 v[94:97], v[152:155], v[200:203], v[94:97]
	v_mfma_f32_16x16x32_bf16 v[90:93], v[160:163], v[200:203], v[90:93]
	v_mfma_f32_16x16x32_bf16 v[78:81], v[152:155], v[208:211], v[78:81]
	v_mfma_f32_16x16x32_bf16 v[74:77], v[160:163], v[208:211], v[74:77]
	s_setprio 0
	s_setprio 1
	v_mfma_f32_16x16x32_bf16 v[118:121], v[164:167], v[180:183], v[118:121]
	v_mfma_f32_16x16x32_bf16 v[114:117], v[172:175], v[180:183], v[114:117]
	v_mfma_f32_16x16x32_bf16 v[102:105], v[164:167], v[188:191], v[102:105]
	v_mfma_f32_16x16x32_bf16 v[98:101], v[172:175], v[188:191], v[98:101]
	v_mfma_f32_16x16x32_bf16 v[86:89], v[164:167], v[196:199], v[86:89]
	v_mfma_f32_16x16x32_bf16 v[82:85], v[172:175], v[196:199], v[82:85]
	v_mfma_f32_16x16x32_bf16 v[70:73], v[164:167], v[204:207], v[70:73]
	v_mfma_f32_16x16x32_bf16 v[66:69], v[172:175], v[204:207], v[66:69]
	v_mfma_f32_16x16x32_bf16 v[118:121], v[168:171], v[184:187], v[118:121]
	v_mfma_f32_16x16x32_bf16 v[114:117], v[176:179], v[184:187], v[114:117]
	v_mfma_f32_16x16x32_bf16 v[102:105], v[168:171], v[192:195], v[102:105]
	v_mfma_f32_16x16x32_bf16 v[98:101], v[176:179], v[192:195], v[98:101]
	v_mfma_f32_16x16x32_bf16 v[86:89], v[168:171], v[200:203], v[86:89]
	v_mfma_f32_16x16x32_bf16 v[82:85], v[176:179], v[200:203], v[82:85]
	v_mfma_f32_16x16x32_bf16 v[70:73], v[168:171], v[208:211], v[70:73]
	v_mfma_f32_16x16x32_bf16 v[66:69], v[176:179], v[208:211], v[66:69]
	s_setprio 0
	s_barrier
	s_add_i32 s52, s52, s28
	v_lshl_add_u64 v[144:145], s[20:21], 0, v[0:1]
	s_mov_b32 m0, s52
	ds_read_b128 v[180:183], v151 offset:16384
	ds_read_b128 v[184:187], v151 offset:17408
	ds_read_b128 v[188:191], v151 offset:18432
	ds_read_b128 v[192:195], v151 offset:19456
	ds_read_b128 v[196:199], v151 offset:20480
	ds_read_b128 v[200:203], v151 offset:21504
	ds_read_b128 v[204:207], v151 offset:22528
	ds_read_b128 v[208:211], v151 offset:23552
	global_load_lds_dwordx4 v[144:145], off
	s_add_i32 m0, s52, 0x2000
	s_add_u32 s52, s20, 0x40000
	v_lshl_add_u64 v[212:213], s[20:21], 0, v[130:131]
	s_addc_u32 s53, s21, 0
	s_add_i32 s54, s54, s28
	global_load_lds_dwordx4 v[212:213], off
	v_lshl_add_u64 v[214:215], s[52:53], 0, v[0:1]
	s_mov_b32 m0, s54
	v_lshl_add_u64 v[216:217], s[22:23], 0, v[132:133]
	global_load_lds_dwordx4 v[214:215], off
	v_lshl_add_u64 v[214:215], s[52:53], 0, v[130:131]
	s_add_i32 m0, s54, 0x2000
	s_nop 0
	global_load_lds_dwordx4 v[214:215], off
	v_lshl_add_u64 v[214:215], s[22:23], 0, v[134:135]
	s_mov_b32 m0, s29
	s_nop 0
	global_load_lds_dwordx4 v[214:215], off
	s_mov_b32 m0, s30
	s_nop 0
	global_load_lds_dwordx4 v[216:217], off
	s_cmp_eq_u32 s97, 0
	s_cbranch_scc1 .Lew2_a
	s_waitcnt vmcnt(24)
	s_branch .Lew2_b

; #define PG8_STAGE(bufoff, gbase, voff) do { _Pragma("unroll") for (int _i = 0; _i < 2; ++_i) \
;         __builtin_amdgcn_global_load_lds((const unsigned*)((const char*)(gbase) + (voff)[_i]), (PG8_LAS unsigned*)(lds + (bufoff) + ldsw + _i * 8192), 16, 0, 0); } while (0)
; #define PG8_LDA(dst, b, h) do { _Pragma("unroll") for (int m = 0; m < 4; ++m) _Pragma("unroll") for (int k = 0; k < 2; ++k) dst[m][k] = *(const PG8_LAS bf16x8*)(lds + PG8_SA(b, h) + aoff + m * 2048 + k * 1024); } while (0)
; #define PG8_LDB(dst, b, h) do { _Pragma("unroll") for (int n = 0; n < 2; ++n) _Pragma("unroll") for (int k = 0; k < 2; ++k) dst[n][k] = *(const PG8_LAS bf16x8*)(lds + PG8_SB(b, h) + boff + n * 2048 + k * 1024); } while (0)
; #define PG8_MMA(ai, bj, At, Bt) do { __builtin_amdgcn_s_setprio(1); _Pragma("unroll") for (int m = 0; m < 4; ++m) _Pragma("unroll") for (int n = 0; n < 2; ++n) _Pragma("unroll") for (int k = 0; k < 2; ++k) \
;         acc[ai][bj][m][n] = __builtin_amdgcn_mfma_f32_16x16x32_bf16(Bt[n][k], At[m][k], acc[ai][bj][m][n], 0, 0, 0); __builtin_amdgcn_s_setprio(0); } while (0)
; #define PG8_WAIT_V(n) asm volatile("s_waitcnt vmcnt(" #n ")" ::: "memory")
; #define PG8_WAIT_L(n) asm volatile("s_waitcnt lgkmcnt(" #n ")" ::: "memory")
; #define PG8_BAR __builtin_amdgcn_s_barrier()
; #define PG8_SCHED __builtin_amdgcn_sched_barrier(0)
; template <class Epi, class Sched, bool ALIGN_EPI = false, bool SP2 = false, bool GATHER = false>
; __device__ __forceinline__ void gemm_phase(PG8_LAS unsigned char* lds, const Gemm g, const Sched& S, const Epi& E, int tid_in, const int* rowsrc = nullptr, PG8_LAS int* idx_lds = nullptr) {
;     ...
;             PG8_WAIT_V(8); PG8_WAIT_L(0); PG8_BAR; PG8_MMA(1, 0, At, B0); PG8_MMA(1, 1, At, B1); PG8_BAR; PG8_SCHED;
;             PG8_LDB(B0, 1, 0); PG8_LDB(B1, 1, 1); PG8_SCHED; PG8_LDA(At, 1, 0); PG8_STAGE(PG8_SA(0, 1), a2 + hstepA, PG8_OS(1));
;             PG8_WAIT_V(8); PG8_WAIT_L(0); PG8_BAR; PG8_MMA(0, 0, At, B0); PG8_MMA(0, 1, At, B1); PG8_BAR; PG8_SCHED;
.Lew2_b:
	s_mov_b32 s97, 0
	s_waitcnt lgkmcnt(0)
	v_mfma_f32_16x16x32_bf16 v[62:65], v[140:143], v[180:183], v[62:65]
	v_mfma_f32_16x16x32_bf16 v[58:61], v[156:159], v[180:183], v[58:61]
	v_mfma_f32_16x16x32_bf16 v[46:49], v[140:143], v[188:191], v[46:49]
	s_barrier
	s_setprio 1
	s_waitcnt lgkmcnt(0)
	v_mfma_f32_16x16x32_bf16 v[42:45], v[156:159], v[188:191], v[42:45]
	v_mfma_f32_16x16x32_bf16 v[30:33], v[140:143], v[196:199], v[30:33]
	v_mfma_f32_16x16x32_bf16 v[26:29], v[156:159], v[196:199], v[26:29]
	v_mfma_f32_16x16x32_bf16 v[14:17], v[140:143], v[204:207], v[14:17]
	v_mfma_f32_16x16x32_bf16 v[10:13], v[156:159], v[204:207], v[10:13]
	v_mfma_f32_16x16x32_bf16 v[62:65], v[152:155], v[184:187], v[62:65]
	v_mfma_f32_16x16x32_bf16 v[58:61], v[160:163], v[184:187], v[58:61]
	v_mfma_f32_16x16x32_bf16 v[46:49], v[152:155], v[192:195], v[46:49]
	v_mfma_f32_16x16x32_bf16 v[42:45], v[160:163], v[192:195], v[42:45]
	v_mfma_f32_16x16x32_bf16 v[30:33], v[152:155], v[200:203], v[30:33]
	v_mfma_f32_16x16x32_bf16 v[26:29], v[160:163], v[200:203], v[26:29]
	v_mfma_f32_16x16x32_bf16 v[14:17], v[152:155], v[208:211], v[14:17]
	v_mfma_f32_16x16x32_bf16 v[10:13], v[160:163], v[208:211], v[10:13]
	s_setprio 0
	s_setprio 1
	v_mfma_f32_16x16x32_bf16 v[54:57], v[164:167], v[180:183], v[54:57]
	v_mfma_f32_16x16x32_bf16 v[50:53], v[172:175], v[180:183], v[50:53]
	v_mfma_f32_16x16x32_bf16 v[38:41], v[164:167], v[188:191], v[38:41]
	v_mfma_f32_16x16x32_bf16 v[34:37], v[172:175], v[188:191], v[34:37]
	v_mfma_f32_16x16x32_bf16 v[22:25], v[164:167], v[196:199], v[22:25]
	v_mfma_f32_16x16x32_bf16 v[18:21], v[172:175], v[196:199], v[18:21]
	v_mfma_f32_16x16x32_bf16 v[6:9], v[164:167], v[204:207], v[6:9]
	v_mfma_f32_16x16x32_bf16 v[2:5], v[172:175], v[204:207], v[2:5]
	v_mfma_f32_16x16x32_bf16 v[54:57], v[168:171], v[184:187], v[54:57]
	v_mfma_f32_16x16x32_bf16 v[50:53], v[176:179], v[184:187], v[50:53]
	v_mfma_f32_16x16x32_bf16 v[38:41], v[168:171], v[192:195], v[38:41]
	v_mfma_f32_16x16x32_bf16 v[34:37], v[176:179], v[192:195], v[34:37]
	v_mfma_f32_16x16x32_bf16 v[22:25], v[168:171], v[200:203], v[22:25]
	v_mfma_f32_16x16x32_bf16 v[18:21], v[176:179], v[200:203], v[18:21]
	v_mfma_f32_16x16x32_bf16 v[6:9], v[168:171], v[208:211], v[6:9]
	v_mfma_f32_16x16x32_bf16 v[2:5], v[176:179], v[208:211], v[2:5]
	s_setprio 0
	s_barrier
	s_add_i32 s52, 0, 0x18000
	s_add_i32 s53, 0, 0x1c000
	v_add_u32_e32 v160, s52, v149
	v_add_u32_e32 v176, s53, v149
	ds_read_b128 v[140:143], v160
	ds_read_b128 v[152:155], v160 offset:1024
	ds_read_b128 v[156:159], v160 offset:2048
	ds_read_b128 v[160:163], v160 offset:3072
	ds_read_b128 v[164:167], v176
	ds_read_b128 v[168:171], v176 offset:1024
	ds_read_b128 v[172:175], v176 offset:2048
	ds_read_b128 v[176:179], v176 offset:3072
	s_add_u32 s22, s22, 0x40000
	s_addc_u32 s23, s23, 0
	s_mov_b32 m0, s31
	v_lshl_add_u64 v[218:219], s[22:23], 0, v[134:135]
	ds_read_b128 v[180:183], v151 offset:32768
	ds_read_b128 v[184:187], v151 offset:33792
	ds_read_b128 v[188:191], v151 offset:34816
	ds_read_b128 v[192:195], v151 offset:35840
	ds_read_b128 v[196:199], v151 offset:36864
	ds_read_b128 v[200:203], v151 offset:37888
	ds_read_b128 v[204:207], v151 offset:38912
	ds_read_b128 v[208:211], v151 offset:39936
	global_load_lds_dwordx4 v[218:219], off
	v_lshl_add_u64 v[218:219], s[22:23], 0, v[132:133]
	s_mov_b32 m0, s36
	s_nop 0
	global_load_lds_dwordx4 v[218:219], off
	s_waitcnt vmcnt(8)
	s_waitcnt lgkmcnt(0)
	v_mfma_f32_16x16x32_bf16 v[126:129], v[140:143], v[180:183], v[126:129]
	v_mfma_f32_16x16x32_bf16 v[122:125], v[156:159], v[180:183], v[122:125]
	v_mfma_f32_16x16x32_bf16 v[110:113], v[140:143], v[188:191], v[110:113]
	s_barrier
	s_setprio 1
	s_waitcnt lgkmcnt(0)
	v_mfma_f32_16x16x32_bf16 v[106:109], v[156:159], v[188:191], v[106:109]
	v_mfma_f32_16x16x32_bf16 v[94:97], v[140:143], v[196:199], v[94:97]
	v_mfma_f32_16x16x32_bf16 v[90:93], v[156:159], v[196:199], v[90:93]
	v_mfma_f32_16x16x32_bf16 v[78:81], v[140:143], v[204:207], v[78:81]
	v_mfma_f32_16x16x32_bf16 v[74:77], v[156:159], v[204:207], v[74:77]
	v_mfma_f32_16x16x32_bf16 v[126:129], v[152:155], v[184:187], v[126:129]
	v_mfma_f32_16x16x32_bf16 v[122:125], v[160:163], v[184:187], v[122:125]
	v_mfma_f32_16x16x32_bf16 v[110:113], v[152:155], v[192:195], v[110:113]
	v_mfma_f32_16x16x32_bf16 v[106:109], v[160:163], v[192:195], v[106:109]
	v_mfma_f32_16x16x32_bf16 v[94:97], v[152:155], v[200:203], v[94:97]
	v_mfma_f32_16x16x32_bf16 v[90:93], v[160:163], v[200:203], v[90:93]
	v_mfma_f32_16x16x32_bf16 v[78:81], v[152:155], v[208:211], v[78:81]
	v_mfma_f32_16x16x32_bf16 v[74:77], v[160:163], v[208:211], v[74:77]
	s_setprio 0
	s_setprio 1
	v_mfma_f32_16x16x32_bf16 v[118:121], v[164:167], v[180:183], v[118:121]
	v_mfma_f32_16x16x32_bf16 v[114:117], v[172:175], v[180:183], v[114:117]
	v_mfma_f32_16x16x32_bf16 v[102:105], v[164:167], v[188:191], v[102:105]
	v_mfma_f32_16x16x32_bf16 v[98:101], v[172:175], v[188:191], v[98:101]
	v_mfma_f32_16x16x32_bf16 v[86:89], v[164:167], v[196:199], v[86:89]
	v_mfma_f32_16x16x32_bf16 v[82:85], v[172:175], v[196:199], v[82:85]
	v_mfma_f32_16x16x32_bf16 v[70:73], v[164:167], v[204:207], v[70:73]
	v_mfma_f32_16x16x32_bf16 v[66:69], v[172:175], v[204:207], v[66:69]
	v_mfma_f32_16x16x32_bf16 v[118:121], v[168:171], v[184:187], v[118:121]
	v_mfma_f32_16x16x32_bf16 v[114:117], v[176:179], v[184:187], v[114:117]
	v_mfma_f32_16x16x32_bf16 v[102:105], v[168:171], v[192:195], v[102:105]
	v_mfma_f32_16x16x32_bf16 v[98:101], v[176:179], v[192:195], v[98:101]
	v_mfma_f32_16x16x32_bf16 v[86:89], v[168:171], v[200:203], v[86:89]
	v_mfma_f32_16x16x32_bf16 v[82:85], v[176:179], v[200:203], v[82:85]
	v_mfma_f32_16x16x32_bf16 v[70:73], v[168:171], v[208:211], v[70:73]
	v_mfma_f32_16x16x32_bf16 v[66:69], v[176:179], v[208:211], v[66:69]
	s_setprio 0
	s_barrier
; #define PG8_STAGE(bufoff, gbase, voff) do { _Pragma("unroll") for (int _i = 0; _i < 2; ++_i) \
;         __builtin_amdgcn_global_load_lds((const unsigned*)((const char*)(gbase) + (voff)[_i]), (PG8_LAS unsigned*)(lds + (bufoff) + ldsw + _i * 8192), 16, 0, 0); } while (0)
; #define PG8_WAIT_V(n) asm volatile("s_waitcnt vmcnt(" #n ")" ::: "memory")
; #define PG8_WAIT_L(n) asm volatile("s_waitcnt lgkmcnt(" #n ")" ::: "memory")
; template <class Epi, class Sched, bool ALIGN_EPI = false, bool SP2 = false, bool GATHER = false>
; __device__ __forceinline__ void gemm_phase(PG8_LAS unsigned char* lds, const Gemm g, const Sched& S, const Epi& E, int tid_in, const int* rowsrc = nullptr, PG8_LAS int* idx_lds = nullptr) {
;     ...
;             PG8_LDA(At, 1, 1); PG8_STAGE(PG8_SB(1, 0), b3, voffB); PG8_STAGE(PG8_SB(1, 1), b3 + hstep, voffB); PG8_STAGE(PG8_SA(1, 0), a3, PG8_OS(0));
;             PG8_WAIT_V(8); PG8_WAIT_L(0); PG8_BAR; PG8_MMA(1, 0, At, B0); PG8_MMA(1, 1, At, B1); PG8_BAR; PG8_SCHED;
;             } else {
;             PG8_LDB(B0, 0, 0); PG8_SCHED; PG8_LDA(At, 0, 0); PG8_STAGE(PG8_SA(1, 1), a1 + hstepA, PG8_OA(1));
;             PG8_WAIT_L(8); PG8_BAR; PG8_WAIT_L(0); PG8_MMA(0, 0, At, B0); PG8_BAR; PG8_SCHED;
;             PG8_LDB(B1, 0, 1); PG8_STAGE(PG8_SB(0, 0), b2, voffB);
;             PG8_BAR; PG8_WAIT_L(0); PG8_MMA(0, 1, At, B1); PG8_BAR;
;             PG8_LDA(At, 0, 1); PG8_STAGE(PG8_SA(0, 0), a2, PG8_OS(0));
;             PG8_BAR; PG8_WAIT_L(0); PG8_MMA(1, 0, At, B0); PG8_BAR; PG8_SCHED;
;             PG8_STAGE(PG8_SB(0, 1), b2 + hstep, voffB);
;             PG8_WAIT_V(6); PG8_BAR; PG8_MMA(1, 1, At, B1); PG8_BAR;
;             PG8_LDB(B0, 1, 0); PG8_SCHED; PG8_LDA(At, 1, 0); PG8_STAGE(PG8_SA(0, 1), a2 + hstepA, PG8_OS(1));
;             PG8_WAIT_L(8); PG8_BAR; PG8_WAIT_L(0); PG8_MMA(0, 0, At, B0); PG8_BAR; PG8_SCHED;
;             PG8_LDB(B1, 1, 1); PG8_STAGE(PG8_SB(1, 0), b3, voffB);
;             PG8_BAR; PG8_WAIT_L(0); PG8_MMA(0, 1, At, B1); PG8_BAR;
;             PG8_LDA(At, 1, 1); PG8_STAGE(PG8_SA(1, 0), a3, PG8_OS(0));
;             PG8_BAR; PG8_WAIT_L(0); PG8_MMA(1, 0, At, B0); PG8_BAR; PG8_SCHED;
;             PG8_STAGE(PG8_SB(1, 1), b3 + hstep, voffB);
;             PG8_WAIT_V(6); PG8_BAR; PG8_MMA(1, 1, At, B1); PG8_BAR;
;             }
;         }
;         if constexpr (ALIGN_EPI) { if (wr == 0) PG8_BAR; }
	s_add_i32 s22, s52, s28
	v_lshl_add_u64 v[144:145], v[144:145], 0, s[10:11]
	s_mov_b32 m0, s22
	ds_read_b128 v[180:183], v151 offset:49152
	ds_read_b128 v[184:187], v151 offset:50176
	ds_read_b128 v[188:191], v151 offset:51200
	ds_read_b128 v[192:195], v151 offset:52224
	ds_read_b128 v[196:199], v151 offset:53248
	ds_read_b128 v[200:203], v151 offset:54272
	ds_read_b128 v[204:207], v151 offset:55296
	ds_read_b128 v[208:211], v151 offset:56320
	global_load_lds_dwordx4 v[144:145], off
	s_add_i32 m0, s22, 0x2000
	s_add_u32 s20, s20, 0x40080
	v_lshl_add_u64 v[144:145], v[212:213], 0, s[10:11]
	s_addc_u32 s21, s21, 0
	s_add_i32 s22, s53, s28
	global_load_lds_dwordx4 v[144:145], off
	v_lshl_add_u64 v[144:145], s[20:21], 0, v[0:1]
	s_mov_b32 m0, s22
	s_nop 0
	global_load_lds_dwordx4 v[144:145], off
	v_lshl_add_u64 v[144:145], s[20:21], 0, v[130:131]
	s_add_i32 m0, s22, 0x2000
	s_nop 0
	global_load_lds_dwordx4 v[144:145], off
	v_lshl_add_u64 v[144:145], v[214:215], 0, s[10:11]
	s_mov_b32 m0, s38
	s_nop 0
	global_load_lds_dwordx4 v[144:145], off
	v_lshl_add_u64 v[144:145], v[216:217], 0, s[10:11]
	s_mov_b32 m0, s39
	s_nop 0
	global_load_lds_dwordx4 v[144:145], off
	s_waitcnt vmcnt(8)
	s_waitcnt lgkmcnt(0)
	v_mfma_f32_16x16x32_bf16 v[62:65], v[140:143], v[180:183], v[62:65]
	v_mfma_f32_16x16x32_bf16 v[58:61], v[156:159], v[180:183], v[58:61]
	v_mfma_f32_16x16x32_bf16 v[46:49], v[140:143], v[188:191], v[46:49]
	s_barrier
	s_setprio 1
	s_waitcnt lgkmcnt(0)
	v_mfma_f32_16x16x32_bf16 v[42:45], v[156:159], v[188:191], v[42:45]
	v_mfma_f32_16x16x32_bf16 v[30:33], v[140:143], v[196:199], v[30:33]
	v_mfma_f32_16x16x32_bf16 v[26:29], v[156:159], v[196:199], v[26:29]
	v_mfma_f32_16x16x32_bf16 v[14:17], v[140:143], v[204:207], v[14:17]
	v_mfma_f32_16x16x32_bf16 v[10:13], v[156:159], v[204:207], v[10:13]
	v_mfma_f32_16x16x32_bf16 v[62:65], v[152:155], v[184:187], v[62:65]
	v_mfma_f32_16x16x32_bf16 v[58:61], v[160:163], v[184:187], v[58:61]
	v_mfma_f32_16x16x32_bf16 v[46:49], v[152:155], v[192:195], v[46:49]
	v_mfma_f32_16x16x32_bf16 v[42:45], v[160:163], v[192:195], v[42:45]
	v_mfma_f32_16x16x32_bf16 v[30:33], v[152:155], v[200:203], v[30:33]
	v_mfma_f32_16x16x32_bf16 v[26:29], v[160:163], v[200:203], v[26:29]
	v_mfma_f32_16x16x32_bf16 v[14:17], v[152:155], v[208:211], v[14:17]
	v_mfma_f32_16x16x32_bf16 v[10:13], v[160:163], v[208:211], v[10:13]
	s_setprio 0
	s_setprio 1
	v_mfma_f32_16x16x32_bf16 v[54:57], v[164:167], v[180:183], v[54:57]
	v_mfma_f32_16x16x32_bf16 v[50:53], v[172:175], v[180:183], v[50:53]
	v_mfma_f32_16x16x32_bf16 v[38:41], v[164:167], v[188:191], v[38:41]
	v_mfma_f32_16x16x32_bf16 v[34:37], v[172:175], v[188:191], v[34:37]
	v_mfma_f32_16x16x32_bf16 v[22:25], v[164:167], v[196:199], v[22:25]
	v_mfma_f32_16x16x32_bf16 v[18:21], v[172:175], v[196:199], v[18:21]
	v_mfma_f32_16x16x32_bf16 v[6:9], v[164:167], v[204:207], v[6:9]
	v_mfma_f32_16x16x32_bf16 v[2:5], v[172:175], v[204:207], v[2:5]
	v_mfma_f32_16x16x32_bf16 v[54:57], v[168:171], v[184:187], v[54:57]
	v_mfma_f32_16x16x32_bf16 v[50:53], v[176:179], v[184:187], v[50:53]
	v_mfma_f32_16x16x32_bf16 v[38:41], v[168:171], v[192:195], v[38:41]
	v_mfma_f32_16x16x32_bf16 v[34:37], v[176:179], v[192:195], v[34:37]
	v_mfma_f32_16x16x32_bf16 v[22:25], v[168:171], v[200:203], v[22:25]
	v_mfma_f32_16x16x32_bf16 v[18:21], v[176:179], v[200:203], v[18:21]
	v_mfma_f32_16x16x32_bf16 v[6:9], v[168:171], v[208:211], v[6:9]
	v_mfma_f32_16x16x32_bf16 v[2:5], v[176:179], v[208:211], v[2:5]
	s_setprio 0
	s_barrier
	s_add_i32 s51, s51, 2
	s_add_u32 s18, s18, 0x100
	s_addc_u32 s19, s19, 0
	s_add_u32 s49, s49, 0x100
	s_addc_u32 s50, s50, 0
	s_cmp_gt_u32 s51, 13
	s_cbranch_scc0 .LBB0_390
	s_mov_b32 s97, 1
	s_and_b64 vcc, exec, s[6:7]
	s_cbranch_vccz .LBB0_393
	s_barrier

; #define GEMM_CALL(EPI, ORD, g, S, E) pg8::gemm_phase<EPI, ORD, PG8_ALIGN, PG8_SP2>(F.lds, g, S, E, F.tid)
; #define PH_END   if (ph + 1 < hi) { for (int br_ = 0; br_ < BAR_REP; ++br_) xcd_barrier(bar); } } ++ph;
; __global__ void __launch_bounds__(NTHREADS, 2) fwd_kernel(Args args) {
;     ...
;             PH_BEGIN for (int rep_ = 0; rep_ < REPN(14); ++rep_) if (EN(14)) { pg8::Gemm g{(const bf16*)(F.ws + R_UV), (const bf16*)(F.ws + WS_SG_WOUT), rows_out, 1024, 2048}; pg8::StaticOrder S; S.init(rows_out, 1024, F.G, (int)blockIdx.x);
;                 pg8::EpiResid E{(bf16*)(F.ws + WS_XB), MOD + (size_t)layer * 9 * 6144 + 2048, rep_ == 0 ? 1.0f : 0.0f}; GEMM_CALL(pg8::EpiResid, pg8::StaticOrder, g, S, E); } PH_END
.LBB0_603:
	s_mov_b32 s97, 0
	v_readlane_b32 s4, v251, 10
	v_readlane_b32 s5, v251, 11
	s_cmp_ge_i32 s2, s4
	s_cselect_b64 s[0:1], -1, 0
	s_cmp_lt_i32 s2, s5
	s_cselect_b64 s[4:5], -1, 0
	s_and_b64 s[4:5], s[0:1], s[4:5]
	s_mov_b64 s[0:1], -1
	s_and_b64 vcc, exec, s[4:5]
	s_cbranch_vccnz .LBB0_605
	s_add_i32 s0, s44, 5
	v_writelane_b32 v252, s0, 37
	s_mov_b64 s[0:1], 0

; #define PG8_STAGE(bufoff, gbase, voff) do { _Pragma("unroll") for (int _i = 0; _i < 2; ++_i) \
;         __builtin_amdgcn_global_load_lds((const unsigned*)((const char*)(gbase) + (voff)[_i]), (PG8_LAS unsigned*)(lds + (bufoff) + ldsw + _i * 8192), 16, 0, 0); } while (0)
; #define PG8_LDA(dst, b, h) do { _Pragma("unroll") for (int m = 0; m < 4; ++m) _Pragma("unroll") for (int k = 0; k < 2; ++k) dst[m][k] = *(const PG8_LAS bf16x8*)(lds + PG8_SA(b, h) + aoff + m * 2048 + k * 1024); } while (0)
; #define PG8_LDB(dst, b, h) do { _Pragma("unroll") for (int n = 0; n < 2; ++n) _Pragma("unroll") for (int k = 0; k < 2; ++k) dst[n][k] = *(const PG8_LAS bf16x8*)(lds + PG8_SB(b, h) + boff + n * 2048 + k * 1024); } while (0)
; #define PG8_MMA(ai, bj, At, Bt) do { __builtin_amdgcn_s_setprio(1); _Pragma("unroll") for (int m = 0; m < 4; ++m) _Pragma("unroll") for (int n = 0; n < 2; ++n) _Pragma("unroll") for (int k = 0; k < 2; ++k) \
;         acc[ai][bj][m][n] = __builtin_amdgcn_mfma_f32_16x16x32_bf16(Bt[n][k], At[m][k], acc[ai][bj][m][n], 0, 0, 0); __builtin_amdgcn_s_setprio(0); } while (0)
; #define PG8_WAIT_V(n) asm volatile("s_waitcnt vmcnt(" #n ")" ::: "memory")
; #define PG8_BAR __builtin_amdgcn_s_barrier()
; template <class Epi, class Sched, bool ALIGN_EPI = false, bool SP2 = false, bool GATHER = false>
; __device__ __forceinline__ void gemm_phase(PG8_LAS unsigned char* lds, const Gemm g, const Sched& S, const Epi& E, int tid_in, const int* rowsrc = nullptr, PG8_LAS int* idx_lds = nullptr) {
;     ...
;         for (int t = 0; t < nt; t += 2) {
;             const bool last = (t == nt - 2);
;             if constexpr (GATHER) {
; #pragma unroll
;                 for (int h_ = 0; h_ < 2; ++h_) { gS[h_][0] = last ? gN[h_][0] : gA[h_][0]; gS[h_][1] = last ? gN[h_][1] : gA[h_][1]; } }
;             const char* a1 = cA + (size_t)(t + 1) * kstep;
;             const char* a2 = last ? nA : cA + (size_t)(t + 2) * kstep; const char* b2 = last ? nB : cB + (size_t)(t + 2) * kstep;
;             const char* a3 = a2 + kstep; const char* b3 = b2 + kstep;
;             if (last && has_next) S.a_ready(nxt);
;             if constexpr (SP2) {
;             PG8_LDB(B0, 0, 0); PG8_LDB(B1, 0, 1); PG8_SCHED; PG8_LDA(At, 0, 0); PG8_STAGE(PG8_SA(1, 1), a1 + hstepA, PG8_OA(1));
;             PG8_WAIT_V(8); PG8_WAIT_L(0); PG8_BAR; PG8_MMA(0, 0, At, B0); PG8_MMA(0, 1, At, B1); PG8_BAR; PG8_SCHED;
.LBB0_615:
	s_add_u32 s22, s20, 0xfff80080
	s_addc_u32 s23, s21, -1
	s_add_i32 s58, 0, 0x10000
	s_cmp_eq_u32 s57, 28
	s_cselect_b32 s25, s9, s23
	s_cselect_b32 s24, s17, s22
	s_cselect_b32 s23, s7, s56
	s_cselect_b32 s22, s19, s55
	s_add_i32 s60, 0, 0x14000
	v_add_u32_e32 v142, s58, v184
	v_add_u32_e32 v182, s60, v184
	ds_read_b128 v[122:125], v142
	ds_read_b128 v[126:129], v142 offset:1024
	ds_read_b128 v[134:137], v142 offset:2048
	ds_read_b128 v[142:145], v142 offset:3072
	ds_read_b128 v[174:177], v182
	ds_read_b128 v[178:181], v182 offset:1024
	ds_read_b128 v[188:191], v182 offset:2048
	ds_read_b128 v[192:195], v182 offset:3072
	v_lshl_add_u64 v[182:183], s[20:21], 0, v[170:171]
	s_add_i32 m0, s39, 0xc000
	ds_read_b128 v[196:199], v186
	ds_read_b128 v[200:203], v186 offset:1024
	ds_read_b128 v[204:207], v186 offset:2048
	ds_read_b128 v[208:211], v186 offset:3072
	ds_read_b128 v[212:215], v186 offset:4096
	ds_read_b128 v[216:219], v186 offset:5120
	ds_read_b128 v[220:223], v186 offset:6144
	ds_read_b128 v[224:227], v186 offset:7168
	global_load_lds_dwordx4 v[182:183], off
	v_lshl_add_u64 v[182:183], s[20:21], 0, v[172:173]
	s_add_i32 m0, s39, 0xe000
	s_nop 0
	global_load_lds_dwordx4 v[182:183], off
	s_cmp_eq_u32 s97, 0
	s_cbranch_scc1 .Lew3_a
	s_waitcnt vmcnt(24)
	s_branch .Lew3_b

; #define PG8_STAGE(bufoff, gbase, voff) do { _Pragma("unroll") for (int _i = 0; _i < 2; ++_i) \
;         __builtin_amdgcn_global_load_lds((const unsigned*)((const char*)(gbase) + (voff)[_i]), (PG8_LAS unsigned*)(lds + (bufoff) + ldsw + _i * 8192), 16, 0, 0); } while (0)
; #define PG8_LDA(dst, b, h) do { _Pragma("unroll") for (int m = 0; m < 4; ++m) _Pragma("unroll") for (int k = 0; k < 2; ++k) dst[m][k] = *(const PG8_LAS bf16x8*)(lds + PG8_SA(b, h) + aoff + m * 2048 + k * 1024); } while (0)
; #define PG8_LDB(dst, b, h) do { _Pragma("unroll") for (int n = 0; n < 2; ++n) _Pragma("unroll") for (int k = 0; k < 2; ++k) dst[n][k] = *(const PG8_LAS bf16x8*)(lds + PG8_SB(b, h) + boff + n * 2048 + k * 1024); } while (0)
; #define PG8_MMA(ai, bj, At, Bt) do { __builtin_amdgcn_s_setprio(1); _Pragma("unroll") for (int m = 0; m < 4; ++m) _Pragma("unroll") for (int n = 0; n < 2; ++n) _Pragma("unroll") for (int k = 0; k < 2; ++k) \
;         acc[ai][bj][m][n] = __builtin_amdgcn_mfma_f32_16x16x32_bf16(Bt[n][k], At[m][k], acc[ai][bj][m][n], 0, 0, 0); __builtin_amdgcn_s_setprio(0); } while (0)
; #define PG8_WAIT_V(n) asm volatile("s_waitcnt vmcnt(" #n ")" ::: "memory")
; #define PG8_WAIT_L(n) asm volatile("s_waitcnt lgkmcnt(" #n ")" ::: "memory")
; #define PG8_BAR __builtin_amdgcn_s_barrier()
; #define PG8_SCHED __builtin_amdgcn_sched_barrier(0)
; template <class Epi, class Sched, bool ALIGN_EPI = false, bool SP2 = false, bool GATHER = false>
; __device__ __forceinline__ void gemm_phase(PG8_LAS unsigned char* lds, const Gemm g, const Sched& S, const Epi& E, int tid_in, const int* rowsrc = nullptr, PG8_LAS int* idx_lds = nullptr) {
;     ...
;             PG8_LDB(B0, 0, 0); PG8_LDB(B1, 0, 1); PG8_SCHED; PG8_LDA(At, 0, 0); PG8_STAGE(PG8_SA(1, 1), a1 + hstepA, PG8_OA(1));
;             PG8_WAIT_V(8); PG8_WAIT_L(0); PG8_BAR; PG8_MMA(0, 0, At, B0); PG8_MMA(0, 1, At, B1); PG8_BAR; PG8_SCHED;
;             PG8_LDA(At, 0, 1); PG8_STAGE(PG8_SB(0, 0), b2, voffB); PG8_STAGE(PG8_SB(0, 1), b2 + hstep, voffB); PG8_STAGE(PG8_SA(0, 0), a2, PG8_OS(0));
.Lew3_b:
	s_waitcnt lgkmcnt(0)
	v_mfma_f32_16x16x32_bf16 v[138:141], v[122:125], v[196:199], v[138:141]
	v_mfma_f32_16x16x32_bf16 v[130:133], v[134:137], v[196:199], v[130:133]
	v_mfma_f32_16x16x32_bf16 v[118:121], v[122:125], v[204:207], v[118:121]
	s_barrier
	s_setprio 1
	s_waitcnt lgkmcnt(0)
	v_mfma_f32_16x16x32_bf16 v[106:109], v[134:137], v[204:207], v[106:109]
	v_mfma_f32_16x16x32_bf16 v[102:105], v[122:125], v[212:215], v[102:105]
	v_mfma_f32_16x16x32_bf16 v[90:93], v[134:137], v[212:215], v[90:93]
	v_mfma_f32_16x16x32_bf16 v[86:89], v[122:125], v[220:223], v[86:89]
	v_mfma_f32_16x16x32_bf16 v[74:77], v[134:137], v[220:223], v[74:77]
	v_mfma_f32_16x16x32_bf16 v[138:141], v[126:129], v[200:203], v[138:141]
	v_mfma_f32_16x16x32_bf16 v[130:133], v[142:145], v[200:203], v[130:133]
	v_mfma_f32_16x16x32_bf16 v[118:121], v[126:129], v[208:211], v[118:121]
	v_mfma_f32_16x16x32_bf16 v[106:109], v[142:145], v[208:211], v[106:109]
	v_mfma_f32_16x16x32_bf16 v[102:105], v[126:129], v[216:219], v[102:105]
	v_mfma_f32_16x16x32_bf16 v[90:93], v[142:145], v[216:219], v[90:93]
	v_mfma_f32_16x16x32_bf16 v[86:89], v[126:129], v[224:227], v[86:89]
	v_mfma_f32_16x16x32_bf16 v[74:77], v[142:145], v[224:227], v[74:77]
	s_setprio 0
	s_setprio 1
	v_mfma_f32_16x16x32_bf16 v[114:117], v[174:177], v[196:199], v[114:117]
	v_mfma_f32_16x16x32_bf16 v[110:113], v[188:191], v[196:199], v[110:113]
	v_mfma_f32_16x16x32_bf16 v[98:101], v[174:177], v[204:207], v[98:101]
	v_mfma_f32_16x16x32_bf16 v[94:97], v[188:191], v[204:207], v[94:97]
	v_mfma_f32_16x16x32_bf16 v[82:85], v[174:177], v[212:215], v[82:85]
	v_mfma_f32_16x16x32_bf16 v[78:81], v[188:191], v[212:215], v[78:81]
	v_mfma_f32_16x16x32_bf16 v[70:73], v[174:177], v[220:223], v[70:73]
	v_mfma_f32_16x16x32_bf16 v[66:69], v[188:191], v[220:223], v[66:69]
	v_mfma_f32_16x16x32_bf16 v[114:117], v[178:181], v[200:203], v[114:117]
	v_mfma_f32_16x16x32_bf16 v[110:113], v[192:195], v[200:203], v[110:113]
	v_mfma_f32_16x16x32_bf16 v[98:101], v[178:181], v[208:211], v[98:101]
	v_mfma_f32_16x16x32_bf16 v[94:97], v[192:195], v[208:211], v[94:97]
	v_mfma_f32_16x16x32_bf16 v[82:85], v[178:181], v[216:219], v[82:85]
	v_mfma_f32_16x16x32_bf16 v[78:81], v[192:195], v[216:219], v[78:81]
	v_mfma_f32_16x16x32_bf16 v[70:73], v[178:181], v[224:227], v[70:73]
	v_mfma_f32_16x16x32_bf16 v[66:69], v[192:195], v[224:227], v[66:69]
	s_setprio 0
	s_barrier
	s_add_i32 s58, s58, s38
	v_lshl_add_u64 v[182:183], s[22:23], 0, v[0:1]
	s_mov_b32 m0, s58
	ds_read_b128 v[196:199], v186 offset:16384
	ds_read_b128 v[200:203], v186 offset:17408
	ds_read_b128 v[204:207], v186 offset:18432
	ds_read_b128 v[208:211], v186 offset:19456
	ds_read_b128 v[212:215], v186 offset:20480
	ds_read_b128 v[216:219], v186 offset:21504
	ds_read_b128 v[220:223], v186 offset:22528
	ds_read_b128 v[224:227], v186 offset:23552
	global_load_lds_dwordx4 v[182:183], off
	s_add_i32 m0, s58, 0x2000
	s_add_u32 s58, s22, 0x80000
	v_lshl_add_u64 v[228:229], s[22:23], 0, v[148:149]
	s_addc_u32 s59, s23, 0
	s_add_i32 s60, s60, s38
	global_load_lds_dwordx4 v[228:229], off
	v_lshl_add_u64 v[230:231], s[58:59], 0, v[0:1]
	s_mov_b32 m0, s60
	v_lshl_add_u64 v[232:233], s[24:25], 0, v[150:151]
	global_load_lds_dwordx4 v[230:231], off
	v_lshl_add_u64 v[230:231], s[58:59], 0, v[148:149]
	s_add_i32 m0, s60, 0x2000
	s_nop 0
	global_load_lds_dwordx4 v[230:231], off
	v_lshl_add_u64 v[230:231], s[24:25], 0, v[152:153]
	s_mov_b32 m0, s39
	s_nop 0
	global_load_lds_dwordx4 v[230:231], off
	s_mov_b32 m0, s41
	s_nop 0
	global_load_lds_dwordx4 v[232:233], off
	s_cmp_eq_u32 s97, 0
	s_cbranch_scc1 .Lew4_a
	s_waitcnt vmcnt(24)
	s_branch .Lew4_b

; #define PG8_STAGE(bufoff, gbase, voff) do { _Pragma("unroll") for (int _i = 0; _i < 2; ++_i) \
;         __builtin_amdgcn_global_load_lds((const unsigned*)((const char*)(gbase) + (voff)[_i]), (PG8_LAS unsigned*)(lds + (bufoff) + ldsw + _i * 8192), 16, 0, 0); } while (0)
; #define PG8_LDA(dst, b, h) do { _Pragma("unroll") for (int m = 0; m < 4; ++m) _Pragma("unroll") for (int k = 0; k < 2; ++k) dst[m][k] = *(const PG8_LAS bf16x8*)(lds + PG8_SA(b, h) + aoff + m * 2048 + k * 1024); } while (0)
; #define PG8_LDB(dst, b, h) do { _Pragma("unroll") for (int n = 0; n < 2; ++n) _Pragma("unroll") for (int k = 0; k < 2; ++k) dst[n][k] = *(const PG8_LAS bf16x8*)(lds + PG8_SB(b, h) + boff + n * 2048 + k * 1024); } while (0)
; #define PG8_MMA(ai, bj, At, Bt) do { __builtin_amdgcn_s_setprio(1); _Pragma("unroll") for (int m = 0; m < 4; ++m) _Pragma("unroll") for (int n = 0; n < 2; ++n) _Pragma("unroll") for (int k = 0; k < 2; ++k) \
;         acc[ai][bj][m][n] = __builtin_amdgcn_mfma_f32_16x16x32_bf16(Bt[n][k], At[m][k], acc[ai][bj][m][n], 0, 0, 0); __builtin_amdgcn_s_setprio(0); } while (0)
; #define PG8_WAIT_V(n) asm volatile("s_waitcnt vmcnt(" #n ")" ::: "memory")
; #define PG8_WAIT_L(n) asm volatile("s_waitcnt lgkmcnt(" #n ")" ::: "memory")
; #define PG8_BAR __builtin_amdgcn_s_barrier()
; #define PG8_SCHED __builtin_amdgcn_sched_barrier(0)
; template <class Epi, class Sched, bool ALIGN_EPI = false, bool SP2 = false, bool GATHER = false>
; __device__ __forceinline__ void gemm_phase(PG8_LAS unsigned char* lds, const Gemm g, const Sched& S, const Epi& E, int tid_in, const int* rowsrc = nullptr, PG8_LAS int* idx_lds = nullptr) {
;     ...
;             PG8_WAIT_V(8); PG8_WAIT_L(0); PG8_BAR; PG8_MMA(1, 0, At, B0); PG8_MMA(1, 1, At, B1); PG8_BAR; PG8_SCHED;
;             PG8_LDB(B0, 1, 0); PG8_LDB(B1, 1, 1); PG8_SCHED; PG8_LDA(At, 1, 0); PG8_STAGE(PG8_SA(0, 1), a2 + hstepA, PG8_OS(1));
;             PG8_WAIT_V(8); PG8_WAIT_L(0); PG8_BAR; PG8_MMA(0, 0, At, B0); PG8_MMA(0, 1, At, B1); PG8_BAR; PG8_SCHED;
.Lew4_b:
	s_mov_b32 s97, 0
	s_waitcnt lgkmcnt(0)
	v_mfma_f32_16x16x32_bf16 v[62:65], v[122:125], v[196:199], v[62:65]
	v_mfma_f32_16x16x32_bf16 v[58:61], v[134:137], v[196:199], v[58:61]
	v_mfma_f32_16x16x32_bf16 v[54:57], v[122:125], v[204:207], v[54:57]
	s_barrier
	s_setprio 1
	s_waitcnt lgkmcnt(0)
	v_mfma_f32_16x16x32_bf16 v[42:45], v[134:137], v[204:207], v[42:45]
	v_mfma_f32_16x16x32_bf16 v[38:41], v[122:125], v[212:215], v[38:41]
	v_mfma_f32_16x16x32_bf16 v[26:29], v[134:137], v[212:215], v[26:29]
	v_mfma_f32_16x16x32_bf16 v[22:25], v[122:125], v[220:223], v[22:25]
	v_mfma_f32_16x16x32_bf16 v[10:13], v[134:137], v[220:223], v[10:13]
	v_mfma_f32_16x16x32_bf16 v[62:65], v[126:129], v[200:203], v[62:65]
	v_mfma_f32_16x16x32_bf16 v[58:61], v[142:145], v[200:203], v[58:61]
	v_mfma_f32_16x16x32_bf16 v[54:57], v[126:129], v[208:211], v[54:57]
	v_mfma_f32_16x16x32_bf16 v[42:45], v[142:145], v[208:211], v[42:45]
	v_mfma_f32_16x16x32_bf16 v[38:41], v[126:129], v[216:219], v[38:41]
	v_mfma_f32_16x16x32_bf16 v[26:29], v[142:145], v[216:219], v[26:29]
	v_mfma_f32_16x16x32_bf16 v[22:25], v[126:129], v[224:227], v[22:25]
	v_mfma_f32_16x16x32_bf16 v[10:13], v[142:145], v[224:227], v[10:13]
	s_setprio 0
	s_setprio 1
	v_mfma_f32_16x16x32_bf16 v[50:53], v[174:177], v[196:199], v[50:53]
	v_mfma_f32_16x16x32_bf16 v[46:49], v[188:191], v[196:199], v[46:49]
	v_mfma_f32_16x16x32_bf16 v[34:37], v[174:177], v[204:207], v[34:37]
	v_mfma_f32_16x16x32_bf16 v[30:33], v[188:191], v[204:207], v[30:33]
	v_mfma_f32_16x16x32_bf16 v[18:21], v[174:177], v[212:215], v[18:21]
	v_mfma_f32_16x16x32_bf16 v[14:17], v[188:191], v[212:215], v[14:17]
	v_mfma_f32_16x16x32_bf16 v[6:9], v[174:177], v[220:223], v[6:9]
	v_mfma_f32_16x16x32_bf16 v[2:5], v[188:191], v[220:223], v[2:5]
	v_mfma_f32_16x16x32_bf16 v[50:53], v[178:181], v[200:203], v[50:53]
	v_mfma_f32_16x16x32_bf16 v[46:49], v[192:195], v[200:203], v[46:49]
	v_mfma_f32_16x16x32_bf16 v[34:37], v[178:181], v[208:211], v[34:37]
	v_mfma_f32_16x16x32_bf16 v[30:33], v[192:195], v[208:211], v[30:33]
	v_mfma_f32_16x16x32_bf16 v[18:21], v[178:181], v[216:219], v[18:21]
	v_mfma_f32_16x16x32_bf16 v[14:17], v[192:195], v[216:219], v[14:17]
	v_mfma_f32_16x16x32_bf16 v[6:9], v[178:181], v[224:227], v[6:9]
	v_mfma_f32_16x16x32_bf16 v[2:5], v[192:195], v[224:227], v[2:5]
	s_setprio 0
	s_barrier
	s_add_i32 s58, 0, 0x18000
	s_add_i32 s59, 0, 0x1c000
	v_add_u32_e32 v142, s58, v184
	v_add_u32_e32 v187, s59, v184
	ds_read_b128 v[122:125], v142
	ds_read_b128 v[126:129], v142 offset:1024
	ds_read_b128 v[134:137], v142 offset:2048
	ds_read_b128 v[142:145], v142 offset:3072
	ds_read_b128 v[174:177], v187
	ds_read_b128 v[178:181], v187 offset:1024
	ds_read_b128 v[188:191], v187 offset:2048
	ds_read_b128 v[192:195], v187 offset:3072
	s_add_u32 s24, s24, 0x80000
	s_addc_u32 s25, s25, 0
	s_mov_b32 m0, s43
	v_lshl_add_u64 v[234:235], s[24:25], 0, v[152:153]
	ds_read_b128 v[196:199], v186 offset:32768
	ds_read_b128 v[200:203], v186 offset:33792
	ds_read_b128 v[204:207], v186 offset:34816
	ds_read_b128 v[208:211], v186 offset:35840
	ds_read_b128 v[212:215], v186 offset:36864
	ds_read_b128 v[216:219], v186 offset:37888
	ds_read_b128 v[220:223], v186 offset:38912
	ds_read_b128 v[224:227], v186 offset:39936
	global_load_lds_dwordx4 v[234:235], off
	v_lshl_add_u64 v[234:235], s[24:25], 0, v[150:151]
	s_mov_b32 m0, s45
	s_nop 0
	global_load_lds_dwordx4 v[234:235], off
	s_waitcnt vmcnt(8)
	s_waitcnt lgkmcnt(0)
	v_mfma_f32_16x16x32_bf16 v[138:141], v[122:125], v[196:199], v[138:141]
	v_mfma_f32_16x16x32_bf16 v[130:133], v[134:137], v[196:199], v[130:133]
	v_mfma_f32_16x16x32_bf16 v[118:121], v[122:125], v[204:207], v[118:121]
	s_barrier
	s_setprio 1
	s_waitcnt lgkmcnt(0)
	v_mfma_f32_16x16x32_bf16 v[106:109], v[134:137], v[204:207], v[106:109]
	v_mfma_f32_16x16x32_bf16 v[102:105], v[122:125], v[212:215], v[102:105]
	v_mfma_f32_16x16x32_bf16 v[90:93], v[134:137], v[212:215], v[90:93]
	v_mfma_f32_16x16x32_bf16 v[86:89], v[122:125], v[220:223], v[86:89]
	v_mfma_f32_16x16x32_bf16 v[74:77], v[134:137], v[220:223], v[74:77]
	v_mfma_f32_16x16x32_bf16 v[138:141], v[126:129], v[200:203], v[138:141]
	v_mfma_f32_16x16x32_bf16 v[130:133], v[142:145], v[200:203], v[130:133]
	v_mfma_f32_16x16x32_bf16 v[118:121], v[126:129], v[208:211], v[118:121]
	v_mfma_f32_16x16x32_bf16 v[106:109], v[142:145], v[208:211], v[106:109]
	v_mfma_f32_16x16x32_bf16 v[102:105], v[126:129], v[216:219], v[102:105]
	v_mfma_f32_16x16x32_bf16 v[90:93], v[142:145], v[216:219], v[90:93]
	v_mfma_f32_16x16x32_bf16 v[86:89], v[126:129], v[224:227], v[86:89]
	v_mfma_f32_16x16x32_bf16 v[74:77], v[142:145], v[224:227], v[74:77]
	s_setprio 0
	s_setprio 1
	v_mfma_f32_16x16x32_bf16 v[114:117], v[174:177], v[196:199], v[114:117]
	v_mfma_f32_16x16x32_bf16 v[110:113], v[188:191], v[196:199], v[110:113]
	v_mfma_f32_16x16x32_bf16 v[98:101], v[174:177], v[204:207], v[98:101]
	v_mfma_f32_16x16x32_bf16 v[94:97], v[188:191], v[204:207], v[94:97]
	v_mfma_f32_16x16x32_bf16 v[82:85], v[174:177], v[212:215], v[82:85]
	v_mfma_f32_16x16x32_bf16 v[78:81], v[188:191], v[212:215], v[78:81]
	v_mfma_f32_16x16x32_bf16 v[70:73], v[174:177], v[220:223], v[70:73]
	v_mfma_f32_16x16x32_bf16 v[66:69], v[188:191], v[220:223], v[66:69]
	v_mfma_f32_16x16x32_bf16 v[114:117], v[178:181], v[200:203], v[114:117]
	v_mfma_f32_16x16x32_bf16 v[110:113], v[192:195], v[200:203], v[110:113]
	v_mfma_f32_16x16x32_bf16 v[98:101], v[178:181], v[208:211], v[98:101]
	v_mfma_f32_16x16x32_bf16 v[94:97], v[192:195], v[208:211], v[94:97]
	v_mfma_f32_16x16x32_bf16 v[82:85], v[178:181], v[216:219], v[82:85]
	v_mfma_f32_16x16x32_bf16 v[78:81], v[192:195], v[216:219], v[78:81]
	v_mfma_f32_16x16x32_bf16 v[70:73], v[178:181], v[224:227], v[70:73]
	v_mfma_f32_16x16x32_bf16 v[66:69], v[192:195], v[224:227], v[66:69]
	s_setprio 0
	s_barrier
; #define PG8_STAGE(bufoff, gbase, voff) do { _Pragma("unroll") for (int _i = 0; _i < 2; ++_i) \
;         __builtin_amdgcn_global_load_lds((const unsigned*)((const char*)(gbase) + (voff)[_i]), (PG8_LAS unsigned*)(lds + (bufoff) + ldsw + _i * 8192), 16, 0, 0); } while (0)
; #define PG8_WAIT_V(n) asm volatile("s_waitcnt vmcnt(" #n ")" ::: "memory")
; #define PG8_WAIT_L(n) asm volatile("s_waitcnt lgkmcnt(" #n ")" ::: "memory")
; template <class Epi, class Sched, bool ALIGN_EPI = false, bool SP2 = false, bool GATHER = false>
; __device__ __forceinline__ void gemm_phase(PG8_LAS unsigned char* lds, const Gemm g, const Sched& S, const Epi& E, int tid_in, const int* rowsrc = nullptr, PG8_LAS int* idx_lds = nullptr) {
;     ...
;             PG8_LDA(At, 1, 1); PG8_STAGE(PG8_SB(1, 0), b3, voffB); PG8_STAGE(PG8_SB(1, 1), b3 + hstep, voffB); PG8_STAGE(PG8_SA(1, 0), a3, PG8_OS(0));
;             PG8_WAIT_V(8); PG8_WAIT_L(0); PG8_BAR; PG8_MMA(1, 0, At, B0); PG8_MMA(1, 1, At, B1); PG8_BAR; PG8_SCHED;
;             } else {
;             PG8_LDB(B0, 0, 0); PG8_SCHED; PG8_LDA(At, 0, 0); PG8_STAGE(PG8_SA(1, 1), a1 + hstepA, PG8_OA(1));
;             PG8_WAIT_L(8); PG8_BAR; PG8_WAIT_L(0); PG8_MMA(0, 0, At, B0); PG8_BAR; PG8_SCHED;
;             PG8_LDB(B1, 0, 1); PG8_STAGE(PG8_SB(0, 0), b2, voffB);
;             PG8_BAR; PG8_WAIT_L(0); PG8_MMA(0, 1, At, B1); PG8_BAR;
;             PG8_LDA(At, 0, 1); PG8_STAGE(PG8_SA(0, 0), a2, PG8_OS(0));
;             PG8_BAR; PG8_WAIT_L(0); PG8_MMA(1, 0, At, B0); PG8_BAR; PG8_SCHED;
;             PG8_STAGE(PG8_SB(0, 1), b2 + hstep, voffB);
;             PG8_WAIT_V(6); PG8_BAR; PG8_MMA(1, 1, At, B1); PG8_BAR;
;             PG8_LDB(B0, 1, 0); PG8_SCHED; PG8_LDA(At, 1, 0); PG8_STAGE(PG8_SA(0, 1), a2 + hstepA, PG8_OS(1));
;             PG8_WAIT_L(8); PG8_BAR; PG8_WAIT_L(0); PG8_MMA(0, 0, At, B0); PG8_BAR; PG8_SCHED;
;             PG8_LDB(B1, 1, 1); PG8_STAGE(PG8_SB(1, 0), b3, voffB);
;             PG8_BAR; PG8_WAIT_L(0); PG8_MMA(0, 1, At, B1); PG8_BAR;
;             PG8_LDA(At, 1, 1); PG8_STAGE(PG8_SA(1, 0), a3, PG8_OS(0));
;             PG8_BAR; PG8_WAIT_L(0); PG8_MMA(1, 0, At, B0); PG8_BAR; PG8_SCHED;
;             PG8_STAGE(PG8_SB(1, 1), b3 + hstep, voffB);
;             PG8_WAIT_V(6); PG8_BAR; PG8_MMA(1, 1, At, B1); PG8_BAR;
;             }
;         }
;         if constexpr (ALIGN_EPI) { if (wr == 0) PG8_BAR; }
	s_add_i32 s24, s58, s38
	v_lshl_add_u64 v[182:183], v[182:183], 0, s[10:11]
	s_mov_b32 m0, s24
	ds_read_b128 v[196:199], v186 offset:49152
	ds_read_b128 v[200:203], v186 offset:50176
	ds_read_b128 v[204:207], v186 offset:51200
	ds_read_b128 v[208:211], v186 offset:52224
	ds_read_b128 v[212:215], v186 offset:53248
	ds_read_b128 v[216:219], v186 offset:54272
	ds_read_b128 v[220:223], v186 offset:55296
	ds_read_b128 v[224:227], v186 offset:56320
	global_load_lds_dwordx4 v[182:183], off
	s_add_i32 m0, s24, 0x2000
	s_add_u32 s22, s22, 0x80080
	v_lshl_add_u64 v[182:183], v[228:229], 0, s[10:11]
	s_addc_u32 s23, s23, 0
	s_add_i32 s24, s59, s38
	global_load_lds_dwordx4 v[182:183], off
	v_lshl_add_u64 v[182:183], s[22:23], 0, v[0:1]
	s_mov_b32 m0, s24
	s_nop 0
	global_load_lds_dwordx4 v[182:183], off
	v_lshl_add_u64 v[182:183], s[22:23], 0, v[148:149]
	s_add_i32 m0, s24, 0x2000
	s_nop 0
	global_load_lds_dwordx4 v[182:183], off
	v_lshl_add_u64 v[182:183], v[230:231], 0, s[10:11]
	s_mov_b32 m0, s52
	s_nop 0
	global_load_lds_dwordx4 v[182:183], off
	v_lshl_add_u64 v[182:183], v[232:233], 0, s[10:11]
	s_mov_b32 m0, s53
	s_nop 0
	global_load_lds_dwordx4 v[182:183], off
	s_waitcnt vmcnt(8)
	s_waitcnt lgkmcnt(0)
	v_mfma_f32_16x16x32_bf16 v[62:65], v[122:125], v[196:199], v[62:65]
	v_mfma_f32_16x16x32_bf16 v[58:61], v[134:137], v[196:199], v[58:61]
	v_mfma_f32_16x16x32_bf16 v[54:57], v[122:125], v[204:207], v[54:57]
	s_barrier
	s_setprio 1
	s_waitcnt lgkmcnt(0)
	v_mfma_f32_16x16x32_bf16 v[42:45], v[134:137], v[204:207], v[42:45]
	v_mfma_f32_16x16x32_bf16 v[38:41], v[122:125], v[212:215], v[38:41]
	v_mfma_f32_16x16x32_bf16 v[26:29], v[134:137], v[212:215], v[26:29]
	v_mfma_f32_16x16x32_bf16 v[22:25], v[122:125], v[220:223], v[22:25]
	v_mfma_f32_16x16x32_bf16 v[10:13], v[134:137], v[220:223], v[10:13]
	v_mfma_f32_16x16x32_bf16 v[62:65], v[126:129], v[200:203], v[62:65]
	v_mfma_f32_16x16x32_bf16 v[58:61], v[142:145], v[200:203], v[58:61]
	v_mfma_f32_16x16x32_bf16 v[54:57], v[126:129], v[208:211], v[54:57]
	v_mfma_f32_16x16x32_bf16 v[42:45], v[142:145], v[208:211], v[42:45]
	v_mfma_f32_16x16x32_bf16 v[38:41], v[126:129], v[216:219], v[38:41]
	v_mfma_f32_16x16x32_bf16 v[26:29], v[142:145], v[216:219], v[26:29]
	v_mfma_f32_16x16x32_bf16 v[22:25], v[126:129], v[224:227], v[22:25]
	v_mfma_f32_16x16x32_bf16 v[10:13], v[142:145], v[224:227], v[10:13]
	s_setprio 0
	s_setprio 1
	v_mfma_f32_16x16x32_bf16 v[50:53], v[174:177], v[196:199], v[50:53]
	v_mfma_f32_16x16x32_bf16 v[46:49], v[188:191], v[196:199], v[46:49]
	v_mfma_f32_16x16x32_bf16 v[34:37], v[174:177], v[204:207], v[34:37]
	v_mfma_f32_16x16x32_bf16 v[30:33], v[188:191], v[204:207], v[30:33]
	v_mfma_f32_16x16x32_bf16 v[18:21], v[174:177], v[212:215], v[18:21]
	v_mfma_f32_16x16x32_bf16 v[14:17], v[188:191], v[212:215], v[14:17]
	v_mfma_f32_16x16x32_bf16 v[6:9], v[174:177], v[220:223], v[6:9]
	v_mfma_f32_16x16x32_bf16 v[2:5], v[188:191], v[220:223], v[2:5]
	v_mfma_f32_16x16x32_bf16 v[50:53], v[178:181], v[200:203], v[50:53]
	v_mfma_f32_16x16x32_bf16 v[46:49], v[192:195], v[200:203], v[46:49]
	v_mfma_f32_16x16x32_bf16 v[34:37], v[178:181], v[208:211], v[34:37]
	v_mfma_f32_16x16x32_bf16 v[30:33], v[192:195], v[208:211], v[30:33]
	v_mfma_f32_16x16x32_bf16 v[18:21], v[178:181], v[216:219], v[18:21]
	v_mfma_f32_16x16x32_bf16 v[14:17], v[192:195], v[216:219], v[14:17]
	v_mfma_f32_16x16x32_bf16 v[6:9], v[178:181], v[224:227], v[6:9]
	v_mfma_f32_16x16x32_bf16 v[2:5], v[192:195], v[224:227], v[2:5]
	s_setprio 0
	s_barrier
	s_add_i32 s57, s57, 2
	s_add_u32 s20, s20, 0x100
	s_addc_u32 s21, s21, 0
	s_add_u32 s55, s55, 0x100
	s_addc_u32 s56, s56, 0
	s_cmp_gt_u32 s57, 29
	s_cbranch_scc0 .LBB0_615
	s_mov_b32 s97, 1
	s_and_b64 vcc, exec, s[4:5]
	s_cbranch_vccz .LBB0_618
	s_barrier

; #define GEMM_CALL(EPI, ORD, g, S, E) pg8::gemm_phase<EPI, ORD, PG8_ALIGN, PG8_SP2>(F.lds, g, S, E, F.tid)
; #define PH_END   if (ph + 1 < hi) { for (int br_ = 0; br_ < BAR_REP; ++br_) xcd_barrier(bar); } } ++ph;
; __global__ void __launch_bounds__(NTHREADS, 2) fwd_kernel(Args args) {
;     ...
;         } else if (kind == 1) {
;             PH_BEGIN for (int rep_ = 0; rep_ < REPN(12); ++rep_) if (EN(12)) { pg8::Gemm g{H, (const bf16*)(F.ws + WS_DIFF_WIN), MROWS, 3072, 1024}; pg8::StaticOrder S; S.init(MROWS, 3072, F.G, (int)blockIdx.x);
;                 pg8::EpiStore<0> E{(bf16*)(F.ws + R_QKV), 3072}; GEMM_CALL(pg8::EpiStore<0>, pg8::StaticOrder, g, S, E); } PH_END
.LBB0_679:
	s_and_b64 vcc, exec, s[0:1]
	s_cbranch_vccz .LBB0_1113
	s_mov_b32 s97, 0
	v_readlane_b32 s4, v251, 10
	v_readlane_b32 s5, v251, 11
	s_cmp_ge_i32 s40, s4
	s_cselect_b64 s[0:1], -1, 0
	s_cmp_lt_i32 s40, s5
	s_cselect_b64 s[4:5], -1, 0
	s_and_b64 s[4:5], s[0:1], s[4:5]
	s_mov_b64 s[0:1], -1
	s_and_b64 vcc, exec, s[4:5]
	s_cbranch_vccnz .LBB0_682
	s_add_i32 s2, s44, 2
	s_mov_b64 s[0:1], 0

; #define PG8_STAGE(bufoff, gbase, voff) do { _Pragma("unroll") for (int _i = 0; _i < 2; ++_i) \
;         __builtin_amdgcn_global_load_lds((const unsigned*)((const char*)(gbase) + (voff)[_i]), (PG8_LAS unsigned*)(lds + (bufoff) + ldsw + _i * 8192), 16, 0, 0); } while (0)
; #define PG8_LDA(dst, b, h) do { _Pragma("unroll") for (int m = 0; m < 4; ++m) _Pragma("unroll") for (int k = 0; k < 2; ++k) dst[m][k] = *(const PG8_LAS bf16x8*)(lds + PG8_SA(b, h) + aoff + m * 2048 + k * 1024); } while (0)
; #define PG8_LDB(dst, b, h) do { _Pragma("unroll") for (int n = 0; n < 2; ++n) _Pragma("unroll") for (int k = 0; k < 2; ++k) dst[n][k] = *(const PG8_LAS bf16x8*)(lds + PG8_SB(b, h) + boff + n * 2048 + k * 1024); } while (0)
; #define PG8_SCHED __builtin_amdgcn_sched_barrier(0)
; template <class Epi, class Sched, bool ALIGN_EPI = false, bool SP2 = false, bool GATHER = false>
; __device__ __forceinline__ void gemm_phase(PG8_LAS unsigned char* lds, const Gemm g, const Sched& S, const Epi& E, int tid_in, const int* rowsrc = nullptr, PG8_LAS int* idx_lds = nullptr) {
;     ...
;         for (int t = 0; t < nt; t += 2) {
;             const bool last = (t == nt - 2);
;             if constexpr (GATHER) {
; #pragma unroll
;                 for (int h_ = 0; h_ < 2; ++h_) { gS[h_][0] = last ? gN[h_][0] : gA[h_][0]; gS[h_][1] = last ? gN[h_][1] : gA[h_][1]; } }
;             const char* a1 = cA + (size_t)(t + 1) * kstep;
;             const char* a2 = last ? nA : cA + (size_t)(t + 2) * kstep; const char* b2 = last ? nB : cB + (size_t)(t + 2) * kstep;
;             const char* a3 = a2 + kstep; const char* b3 = b2 + kstep;
;             if (last && has_next) S.a_ready(nxt);
;             if constexpr (SP2) {
;             PG8_LDB(B0, 0, 0); PG8_LDB(B1, 0, 1); PG8_SCHED; PG8_LDA(At, 0, 0); PG8_STAGE(PG8_SA(1, 1), a1 + hstepA, PG8_OA(1));
.LBB0_692:
	s_add_u32 s22, s20, 0xfffc0080
	s_addc_u32 s23, s21, -1
	s_add_i32 s52, 0, 0x10000
	s_cmp_eq_u32 s51, 12
	s_cselect_b32 s25, s15, s23
	s_cselect_b32 s24, s47, s22
	s_cselect_b32 s23, s13, s50
	s_cselect_b32 s22, s48, s49
	s_add_i32 s54, 0, 0x14000
	v_add_u32_e32 v158, s52, v145
	v_add_u32_e32 v174, s54, v145
	ds_read_b128 v[140:143], v158
	ds_read_b128 v[150:153], v158 offset:1024
	ds_read_b128 v[154:157], v158 offset:2048
	ds_read_b128 v[158:161], v158 offset:3072
	ds_read_b128 v[162:165], v174
	ds_read_b128 v[166:169], v174 offset:1024
	ds_read_b128 v[170:173], v174 offset:2048
	ds_read_b128 v[174:177], v174 offset:3072
	v_lshl_add_u64 v[178:179], s[20:21], 0, v[136:137]
	s_add_i32 m0, s31, 0xc000
	ds_read_b128 v[184:187], v149
	ds_read_b128 v[188:191], v149 offset:1024
	ds_read_b128 v[192:195], v149 offset:2048
	ds_read_b128 v[196:199], v149 offset:3072
	ds_read_b128 v[200:203], v149 offset:4096
	ds_read_b128 v[204:207], v149 offset:5120
	ds_read_b128 v[208:211], v149 offset:6144
	ds_read_b128 v[212:215], v149 offset:7168
	global_load_lds_dwordx4 v[178:179], off
	v_lshl_add_u64 v[178:179], s[20:21], 0, v[138:139]
	s_add_i32 m0, s31, 0xe000
	s_nop 0
	global_load_lds_dwordx4 v[178:179], off
	s_cmp_eq_u32 s97, 0
	s_cbranch_scc1 .Lew5_a
	s_waitcnt vmcnt(24)
	s_branch .Lew5_b

; #define PG8_STAGE(bufoff, gbase, voff) do { _Pragma("unroll") for (int _i = 0; _i < 2; ++_i) \
;         __builtin_amdgcn_global_load_lds((const unsigned*)((const char*)(gbase) + (voff)[_i]), (PG8_LAS unsigned*)(lds + (bufoff) + ldsw + _i * 8192), 16, 0, 0); } while (0)
; #define PG8_LDA(dst, b, h) do { _Pragma("unroll") for (int m = 0; m < 4; ++m) _Pragma("unroll") for (int k = 0; k < 2; ++k) dst[m][k] = *(const PG8_LAS bf16x8*)(lds + PG8_SA(b, h) + aoff + m * 2048 + k * 1024); } while (0)
; #define PG8_LDB(dst, b, h) do { _Pragma("unroll") for (int n = 0; n < 2; ++n) _Pragma("unroll") for (int k = 0; k < 2; ++k) dst[n][k] = *(const PG8_LAS bf16x8*)(lds + PG8_SB(b, h) + boff + n * 2048 + k * 1024); } while (0)
; #define PG8_MMA(ai, bj, At, Bt) do { __builtin_amdgcn_s_setprio(1); _Pragma("unroll") for (int m = 0; m < 4; ++m) _Pragma("unroll") for (int n = 0; n < 2; ++n) _Pragma("unroll") for (int k = 0; k < 2; ++k) \
;         acc[ai][bj][m][n] = __builtin_amdgcn_mfma_f32_16x16x32_bf16(Bt[n][k], At[m][k], acc[ai][bj][m][n], 0, 0, 0); __builtin_amdgcn_s_setprio(0); } while (0)
; #define PG8_WAIT_V(n) asm volatile("s_waitcnt vmcnt(" #n ")" ::: "memory")
; #define PG8_WAIT_L(n) asm volatile("s_waitcnt lgkmcnt(" #n ")" ::: "memory")
; #define PG8_BAR __builtin_amdgcn_s_barrier()
; #define PG8_SCHED __builtin_amdgcn_sched_barrier(0)
; template <class Epi, class Sched, bool ALIGN_EPI = false, bool SP2 = false, bool GATHER = false>
; __device__ __forceinline__ void gemm_phase(PG8_LAS unsigned char* lds, const Gemm g, const Sched& S, const Epi& E, int tid_in, const int* rowsrc = nullptr, PG8_LAS int* idx_lds = nullptr) {
;     ...
;             PG8_LDB(B0, 0, 0); PG8_LDB(B1, 0, 1); PG8_SCHED; PG8_LDA(At, 0, 0); PG8_STAGE(PG8_SA(1, 1), a1 + hstepA, PG8_OA(1));
;             PG8_WAIT_V(8); PG8_WAIT_L(0); PG8_BAR; PG8_MMA(0, 0, At, B0); PG8_MMA(0, 1, At, B1); PG8_BAR; PG8_SCHED;
;             PG8_LDA(At, 0, 1); PG8_STAGE(PG8_SB(0, 0), b2, voffB); PG8_STAGE(PG8_SB(0, 1), b2 + hstep, voffB); PG8_STAGE(PG8_SA(0, 0), a2, PG8_OS(0));
.Lew5_b:
	s_waitcnt lgkmcnt(0)
	v_mfma_f32_16x16x32_bf16 v[126:129], v[140:143], v[184:187], v[126:129]
	v_mfma_f32_16x16x32_bf16 v[122:125], v[154:157], v[184:187], v[122:125]
	v_mfma_f32_16x16x32_bf16 v[118:121], v[140:143], v[192:195], v[118:121]
	s_barrier
	s_setprio 1
	s_waitcnt lgkmcnt(0)
	v_mfma_f32_16x16x32_bf16 v[110:113], v[154:157], v[192:195], v[110:113]
	v_mfma_f32_16x16x32_bf16 v[102:105], v[140:143], v[200:203], v[102:105]
	v_mfma_f32_16x16x32_bf16 v[94:97], v[154:157], v[200:203], v[94:97]
	v_mfma_f32_16x16x32_bf16 v[86:89], v[140:143], v[208:211], v[86:89]
	v_mfma_f32_16x16x32_bf16 v[78:81], v[154:157], v[208:211], v[78:81]
	v_mfma_f32_16x16x32_bf16 v[126:129], v[150:153], v[188:191], v[126:129]
	v_mfma_f32_16x16x32_bf16 v[122:125], v[158:161], v[188:191], v[122:125]
	v_mfma_f32_16x16x32_bf16 v[118:121], v[150:153], v[196:199], v[118:121]
	v_mfma_f32_16x16x32_bf16 v[110:113], v[158:161], v[196:199], v[110:113]
	v_mfma_f32_16x16x32_bf16 v[102:105], v[150:153], v[204:207], v[102:105]
	v_mfma_f32_16x16x32_bf16 v[94:97], v[158:161], v[204:207], v[94:97]
	v_mfma_f32_16x16x32_bf16 v[86:89], v[150:153], v[212:215], v[86:89]
	v_mfma_f32_16x16x32_bf16 v[78:81], v[158:161], v[212:215], v[78:81]
	s_setprio 0
	s_setprio 1
	v_mfma_f32_16x16x32_bf16 v[114:117], v[162:165], v[184:187], v[114:117]
	v_mfma_f32_16x16x32_bf16 v[106:109], v[170:173], v[184:187], v[106:109]
	v_mfma_f32_16x16x32_bf16 v[98:101], v[162:165], v[192:195], v[98:101]
	v_mfma_f32_16x16x32_bf16 v[90:93], v[170:173], v[192:195], v[90:93]
	v_mfma_f32_16x16x32_bf16 v[82:85], v[162:165], v[200:203], v[82:85]
	v_mfma_f32_16x16x32_bf16 v[74:77], v[170:173], v[200:203], v[74:77]
	v_mfma_f32_16x16x32_bf16 v[70:73], v[162:165], v[208:211], v[70:73]
	v_mfma_f32_16x16x32_bf16 v[66:69], v[170:173], v[208:211], v[66:69]
	v_mfma_f32_16x16x32_bf16 v[114:117], v[166:169], v[188:191], v[114:117]
	v_mfma_f32_16x16x32_bf16 v[106:109], v[174:177], v[188:191], v[106:109]
	v_mfma_f32_16x16x32_bf16 v[98:101], v[166:169], v[196:199], v[98:101]
	v_mfma_f32_16x16x32_bf16 v[90:93], v[174:177], v[196:199], v[90:93]
	v_mfma_f32_16x16x32_bf16 v[82:85], v[166:169], v[204:207], v[82:85]
	v_mfma_f32_16x16x32_bf16 v[74:77], v[174:177], v[204:207], v[74:77]
	v_mfma_f32_16x16x32_bf16 v[70:73], v[166:169], v[212:215], v[70:73]
	v_mfma_f32_16x16x32_bf16 v[66:69], v[174:177], v[212:215], v[66:69]
	s_setprio 0
	s_barrier
	s_add_i32 s52, s52, s30
	v_lshl_add_u64 v[178:179], s[22:23], 0, v[0:1]
	s_mov_b32 m0, s52
	ds_read_b128 v[184:187], v149 offset:16384
	ds_read_b128 v[188:191], v149 offset:17408
	ds_read_b128 v[192:195], v149 offset:18432
	ds_read_b128 v[196:199], v149 offset:19456
	ds_read_b128 v[200:203], v149 offset:20480
	ds_read_b128 v[204:207], v149 offset:21504
	ds_read_b128 v[208:211], v149 offset:22528
	ds_read_b128 v[212:215], v149 offset:23552
	global_load_lds_dwordx4 v[178:179], off
	s_add_i32 m0, s52, 0x2000
	s_add_u32 s52, s22, 0x40000
	v_lshl_add_u64 v[180:181], s[22:23], 0, v[130:131]
	s_addc_u32 s53, s23, 0
	s_add_i32 s54, s54, s30
	global_load_lds_dwordx4 v[180:181], off
	v_lshl_add_u64 v[182:183], s[52:53], 0, v[0:1]
	s_mov_b32 m0, s54
	v_lshl_add_u64 v[216:217], s[24:25], 0, v[132:133]
	global_load_lds_dwordx4 v[182:183], off
	v_lshl_add_u64 v[182:183], s[52:53], 0, v[130:131]
	s_add_i32 m0, s54, 0x2000
	s_nop 0
	global_load_lds_dwordx4 v[182:183], off
	v_lshl_add_u64 v[182:183], s[24:25], 0, v[134:135]
	s_mov_b32 m0, s31
	s_nop 0
	global_load_lds_dwordx4 v[182:183], off
	s_mov_b32 m0, s34
	s_nop 0
	global_load_lds_dwordx4 v[216:217], off
	s_cmp_eq_u32 s97, 0
	s_cbranch_scc1 .Lew6_a
	s_waitcnt vmcnt(24)
	s_branch .Lew6_b

; #define PG8_STAGE(bufoff, gbase, voff) do { _Pragma("unroll") for (int _i = 0; _i < 2; ++_i) \
;         __builtin_amdgcn_global_load_lds((const unsigned*)((const char*)(gbase) + (voff)[_i]), (PG8_LAS unsigned*)(lds + (bufoff) + ldsw + _i * 8192), 16, 0, 0); } while (0)
; #define PG8_LDA(dst, b, h) do { _Pragma("unroll") for (int m = 0; m < 4; ++m) _Pragma("unroll") for (int k = 0; k < 2; ++k) dst[m][k] = *(const PG8_LAS bf16x8*)(lds + PG8_SA(b, h) + aoff + m * 2048 + k * 1024); } while (0)
; #define PG8_LDB(dst, b, h) do { _Pragma("unroll") for (int n = 0; n < 2; ++n) _Pragma("unroll") for (int k = 0; k < 2; ++k) dst[n][k] = *(const PG8_LAS bf16x8*)(lds + PG8_SB(b, h) + boff + n * 2048 + k * 1024); } while (0)
; #define PG8_MMA(ai, bj, At, Bt) do { __builtin_amdgcn_s_setprio(1); _Pragma("unroll") for (int m = 0; m < 4; ++m) _Pragma("unroll") for (int n = 0; n < 2; ++n) _Pragma("unroll") for (int k = 0; k < 2; ++k) \
;         acc[ai][bj][m][n] = __builtin_amdgcn_mfma_f32_16x16x32_bf16(Bt[n][k], At[m][k], acc[ai][bj][m][n], 0, 0, 0); __builtin_amdgcn_s_setprio(0); } while (0)
; #define PG8_WAIT_V(n) asm volatile("s_waitcnt vmcnt(" #n ")" ::: "memory")
; #define PG8_WAIT_L(n) asm volatile("s_waitcnt lgkmcnt(" #n ")" ::: "memory")
; #define PG8_BAR __builtin_amdgcn_s_barrier()
; #define PG8_SCHED __builtin_amdgcn_sched_barrier(0)
; template <class Epi, class Sched, bool ALIGN_EPI = false, bool SP2 = false, bool GATHER = false>
; __device__ __forceinline__ void gemm_phase(PG8_LAS unsigned char* lds, const Gemm g, const Sched& S, const Epi& E, int tid_in, const int* rowsrc = nullptr, PG8_LAS int* idx_lds = nullptr) {
;     ...
;             PG8_WAIT_V(8); PG8_WAIT_L(0); PG8_BAR; PG8_MMA(1, 0, At, B0); PG8_MMA(1, 1, At, B1); PG8_BAR; PG8_SCHED;
;             PG8_LDB(B0, 1, 0); PG8_LDB(B1, 1, 1); PG8_SCHED; PG8_LDA(At, 1, 0); PG8_STAGE(PG8_SA(0, 1), a2 + hstepA, PG8_OS(1));
;             PG8_WAIT_V(8); PG8_WAIT_L(0); PG8_BAR; PG8_MMA(0, 0, At, B0); PG8_MMA(0, 1, At, B1); PG8_BAR; PG8_SCHED;
.Lew6_b:
	s_mov_b32 s97, 0
	s_waitcnt lgkmcnt(0)
	v_mfma_f32_16x16x32_bf16 v[62:65], v[140:143], v[184:187], v[62:65]
	v_mfma_f32_16x16x32_bf16 v[58:61], v[154:157], v[184:187], v[58:61]
	v_mfma_f32_16x16x32_bf16 v[54:57], v[140:143], v[192:195], v[54:57]
	s_barrier
	s_setprio 1
	s_waitcnt lgkmcnt(0)
	v_mfma_f32_16x16x32_bf16 v[46:49], v[154:157], v[192:195], v[46:49]
	v_mfma_f32_16x16x32_bf16 v[38:41], v[140:143], v[200:203], v[38:41]
	v_mfma_f32_16x16x32_bf16 v[30:33], v[154:157], v[200:203], v[30:33]
	v_mfma_f32_16x16x32_bf16 v[22:25], v[140:143], v[208:211], v[22:25]
	v_mfma_f32_16x16x32_bf16 v[14:17], v[154:157], v[208:211], v[14:17]
	v_mfma_f32_16x16x32_bf16 v[62:65], v[150:153], v[188:191], v[62:65]
	v_mfma_f32_16x16x32_bf16 v[58:61], v[158:161], v[188:191], v[58:61]
	v_mfma_f32_16x16x32_bf16 v[54:57], v[150:153], v[196:199], v[54:57]
	v_mfma_f32_16x16x32_bf16 v[46:49], v[158:161], v[196:199], v[46:49]
	v_mfma_f32_16x16x32_bf16 v[38:41], v[150:153], v[204:207], v[38:41]
	v_mfma_f32_16x16x32_bf16 v[30:33], v[158:161], v[204:207], v[30:33]
	v_mfma_f32_16x16x32_bf16 v[22:25], v[150:153], v[212:215], v[22:25]
	v_mfma_f32_16x16x32_bf16 v[14:17], v[158:161], v[212:215], v[14:17]
	s_setprio 0
	s_setprio 1
	v_mfma_f32_16x16x32_bf16 v[50:53], v[162:165], v[184:187], v[50:53]
	v_mfma_f32_16x16x32_bf16 v[42:45], v[170:173], v[184:187], v[42:45]
	v_mfma_f32_16x16x32_bf16 v[34:37], v[162:165], v[192:195], v[34:37]
	v_mfma_f32_16x16x32_bf16 v[26:29], v[170:173], v[192:195], v[26:29]
	v_mfma_f32_16x16x32_bf16 v[18:21], v[162:165], v[200:203], v[18:21]
	v_mfma_f32_16x16x32_bf16 v[10:13], v[170:173], v[200:203], v[10:13]
	v_mfma_f32_16x16x32_bf16 v[6:9], v[162:165], v[208:211], v[6:9]
	v_mfma_f32_16x16x32_bf16 v[2:5], v[170:173], v[208:211], v[2:5]
	v_mfma_f32_16x16x32_bf16 v[50:53], v[166:169], v[188:191], v[50:53]
	v_mfma_f32_16x16x32_bf16 v[42:45], v[174:177], v[188:191], v[42:45]
	v_mfma_f32_16x16x32_bf16 v[34:37], v[166:169], v[196:199], v[34:37]
	v_mfma_f32_16x16x32_bf16 v[26:29], v[174:177], v[196:199], v[26:29]
	v_mfma_f32_16x16x32_bf16 v[18:21], v[166:169], v[204:207], v[18:21]
	v_mfma_f32_16x16x32_bf16 v[10:13], v[174:177], v[204:207], v[10:13]
	v_mfma_f32_16x16x32_bf16 v[6:9], v[166:169], v[212:215], v[6:9]
	v_mfma_f32_16x16x32_bf16 v[2:5], v[174:177], v[212:215], v[2:5]
	s_setprio 0
	s_barrier
	s_add_i32 s52, 0, 0x18000
	s_add_i32 s53, 0, 0x1c000
	v_add_u32_e32 v158, s52, v145
	v_add_u32_e32 v174, s53, v145
	ds_read_b128 v[140:143], v158
	ds_read_b128 v[150:153], v158 offset:1024
	ds_read_b128 v[154:157], v158 offset:2048
	ds_read_b128 v[158:161], v158 offset:3072
	ds_read_b128 v[162:165], v174
	ds_read_b128 v[166:169], v174 offset:1024
	ds_read_b128 v[170:173], v174 offset:2048
	ds_read_b128 v[174:177], v174 offset:3072
	s_add_u32 s24, s24, 0x40000
	s_addc_u32 s25, s25, 0
	s_mov_b32 m0, s35
	v_lshl_add_u64 v[218:219], s[24:25], 0, v[134:135]
	ds_read_b128 v[184:187], v149 offset:32768
	ds_read_b128 v[188:191], v149 offset:33792
	ds_read_b128 v[192:195], v149 offset:34816
	ds_read_b128 v[196:199], v149 offset:35840
	ds_read_b128 v[200:203], v149 offset:36864
	ds_read_b128 v[204:207], v149 offset:37888
	ds_read_b128 v[208:211], v149 offset:38912
	ds_read_b128 v[212:215], v149 offset:39936
	global_load_lds_dwordx4 v[218:219], off
	v_lshl_add_u64 v[218:219], s[24:25], 0, v[132:133]
	s_mov_b32 m0, s36
	s_nop 0
	global_load_lds_dwordx4 v[218:219], off
	s_waitcnt vmcnt(8)
	s_waitcnt lgkmcnt(0)
	v_mfma_f32_16x16x32_bf16 v[126:129], v[140:143], v[184:187], v[126:129]
	v_mfma_f32_16x16x32_bf16 v[122:125], v[154:157], v[184:187], v[122:125]
	v_mfma_f32_16x16x32_bf16 v[118:121], v[140:143], v[192:195], v[118:121]
	s_barrier
	s_setprio 1
	s_waitcnt lgkmcnt(0)
	v_mfma_f32_16x16x32_bf16 v[110:113], v[154:157], v[192:195], v[110:113]
	v_mfma_f32_16x16x32_bf16 v[102:105], v[140:143], v[200:203], v[102:105]
	v_mfma_f32_16x16x32_bf16 v[94:97], v[154:157], v[200:203], v[94:97]
	v_mfma_f32_16x16x32_bf16 v[86:89], v[140:143], v[208:211], v[86:89]
	v_mfma_f32_16x16x32_bf16 v[78:81], v[154:157], v[208:211], v[78:81]
	v_mfma_f32_16x16x32_bf16 v[126:129], v[150:153], v[188:191], v[126:129]
	v_mfma_f32_16x16x32_bf16 v[122:125], v[158:161], v[188:191], v[122:125]
	v_mfma_f32_16x16x32_bf16 v[118:121], v[150:153], v[196:199], v[118:121]
	v_mfma_f32_16x16x32_bf16 v[110:113], v[158:161], v[196:199], v[110:113]
	v_mfma_f32_16x16x32_bf16 v[102:105], v[150:153], v[204:207], v[102:105]
	v_mfma_f32_16x16x32_bf16 v[94:97], v[158:161], v[204:207], v[94:97]
	v_mfma_f32_16x16x32_bf16 v[86:89], v[150:153], v[212:215], v[86:89]
	v_mfma_f32_16x16x32_bf16 v[78:81], v[158:161], v[212:215], v[78:81]
	s_setprio 0
	s_setprio 1
	v_mfma_f32_16x16x32_bf16 v[114:117], v[162:165], v[184:187], v[114:117]
	v_mfma_f32_16x16x32_bf16 v[106:109], v[170:173], v[184:187], v[106:109]
	v_mfma_f32_16x16x32_bf16 v[98:101], v[162:165], v[192:195], v[98:101]
	v_mfma_f32_16x16x32_bf16 v[90:93], v[170:173], v[192:195], v[90:93]
	v_mfma_f32_16x16x32_bf16 v[82:85], v[162:165], v[200:203], v[82:85]
	v_mfma_f32_16x16x32_bf16 v[74:77], v[170:173], v[200:203], v[74:77]
	v_mfma_f32_16x16x32_bf16 v[70:73], v[162:165], v[208:211], v[70:73]
	v_mfma_f32_16x16x32_bf16 v[66:69], v[170:173], v[208:211], v[66:69]
	v_mfma_f32_16x16x32_bf16 v[114:117], v[166:169], v[188:191], v[114:117]
	v_mfma_f32_16x16x32_bf16 v[106:109], v[174:177], v[188:191], v[106:109]
	v_mfma_f32_16x16x32_bf16 v[98:101], v[166:169], v[196:199], v[98:101]
	v_mfma_f32_16x16x32_bf16 v[90:93], v[174:177], v[196:199], v[90:93]
	v_mfma_f32_16x16x32_bf16 v[82:85], v[166:169], v[204:207], v[82:85]
	v_mfma_f32_16x16x32_bf16 v[74:77], v[174:177], v[204:207], v[74:77]
	v_mfma_f32_16x16x32_bf16 v[70:73], v[166:169], v[212:215], v[70:73]
	v_mfma_f32_16x16x32_bf16 v[66:69], v[174:177], v[212:215], v[66:69]
	s_setprio 0
	s_barrier
; #define PG8_STAGE(bufoff, gbase, voff) do { _Pragma("unroll") for (int _i = 0; _i < 2; ++_i) \
;         __builtin_amdgcn_global_load_lds((const unsigned*)((const char*)(gbase) + (voff)[_i]), (PG8_LAS unsigned*)(lds + (bufoff) + ldsw + _i * 8192), 16, 0, 0); } while (0)
; #define PG8_LDA(dst, b, h) do { _Pragma("unroll") for (int m = 0; m < 4; ++m) _Pragma("unroll") for (int k = 0; k < 2; ++k) dst[m][k] = *(const PG8_LAS bf16x8*)(lds + PG8_SA(b, h) + aoff + m * 2048 + k * 1024); } while (0)
; #define PG8_MMA(ai, bj, At, Bt) do { __builtin_amdgcn_s_setprio(1); _Pragma("unroll") for (int m = 0; m < 4; ++m) _Pragma("unroll") for (int n = 0; n < 2; ++n) _Pragma("unroll") for (int k = 0; k < 2; ++k) \
;         acc[ai][bj][m][n] = __builtin_amdgcn_mfma_f32_16x16x32_bf16(Bt[n][k], At[m][k], acc[ai][bj][m][n], 0, 0, 0); __builtin_amdgcn_s_setprio(0); } while (0)
; #define PG8_WAIT_V(n) asm volatile("s_waitcnt vmcnt(" #n ")" ::: "memory")
; #define PG8_WAIT_L(n) asm volatile("s_waitcnt lgkmcnt(" #n ")" ::: "memory")
; #define PG8_BAR __builtin_amdgcn_s_barrier()
; #define PG8_SCHED __builtin_amdgcn_sched_barrier(0)
; template <class Epi, class Sched, bool ALIGN_EPI = false, bool SP2 = false, bool GATHER = false>
; __device__ __forceinline__ void gemm_phase(PG8_LAS unsigned char* lds, const Gemm g, const Sched& S, const Epi& E, int tid_in, const int* rowsrc = nullptr, PG8_LAS int* idx_lds = nullptr) {
;     ...
;             PG8_LDA(At, 1, 1); PG8_STAGE(PG8_SB(1, 0), b3, voffB); PG8_STAGE(PG8_SB(1, 1), b3 + hstep, voffB); PG8_STAGE(PG8_SA(1, 0), a3, PG8_OS(0));
;             PG8_WAIT_V(8); PG8_WAIT_L(0); PG8_BAR; PG8_MMA(1, 0, At, B0); PG8_MMA(1, 1, At, B1); PG8_BAR; PG8_SCHED;
;     ...
;         if constexpr (ALIGN_EPI) { if (wr == 0) PG8_BAR; }
	s_add_i32 s24, s52, s30
	v_lshl_add_u64 v[178:179], v[178:179], 0, s[10:11]
	s_mov_b32 m0, s24
	ds_read_b128 v[184:187], v149 offset:49152
	ds_read_b128 v[188:191], v149 offset:50176
	ds_read_b128 v[192:195], v149 offset:51200
	ds_read_b128 v[196:199], v149 offset:52224
	ds_read_b128 v[200:203], v149 offset:53248
	ds_read_b128 v[204:207], v149 offset:54272
	ds_read_b128 v[208:211], v149 offset:55296
	ds_read_b128 v[212:215], v149 offset:56320
	global_load_lds_dwordx4 v[178:179], off
	s_add_i32 m0, s24, 0x2000
	s_add_u32 s22, s22, 0x40080
	v_lshl_add_u64 v[178:179], v[180:181], 0, s[10:11]
	s_addc_u32 s23, s23, 0
	s_add_i32 s24, s53, s30
	global_load_lds_dwordx4 v[178:179], off
	v_lshl_add_u64 v[178:179], s[22:23], 0, v[0:1]
	s_mov_b32 m0, s24
	s_nop 0
	global_load_lds_dwordx4 v[178:179], off
	v_lshl_add_u64 v[178:179], s[22:23], 0, v[130:131]
	s_add_i32 m0, s24, 0x2000
	s_nop 0
	global_load_lds_dwordx4 v[178:179], off
	v_lshl_add_u64 v[178:179], v[182:183], 0, s[10:11]
	s_mov_b32 m0, s38
	s_nop 0
	global_load_lds_dwordx4 v[178:179], off
	v_lshl_add_u64 v[178:179], v[216:217], 0, s[10:11]
	s_mov_b32 m0, s39
	s_nop 0
	global_load_lds_dwordx4 v[178:179], off
	s_waitcnt vmcnt(8)
	s_waitcnt lgkmcnt(0)
	v_mfma_f32_16x16x32_bf16 v[62:65], v[140:143], v[184:187], v[62:65]
	v_mfma_f32_16x16x32_bf16 v[58:61], v[154:157], v[184:187], v[58:61]
	v_mfma_f32_16x16x32_bf16 v[54:57], v[140:143], v[192:195], v[54:57]
	s_barrier
	s_setprio 1
	s_waitcnt lgkmcnt(0)
	v_mfma_f32_16x16x32_bf16 v[46:49], v[154:157], v[192:195], v[46:49]
	v_mfma_f32_16x16x32_bf16 v[38:41], v[140:143], v[200:203], v[38:41]
	v_mfma_f32_16x16x32_bf16 v[30:33], v[154:157], v[200:203], v[30:33]
	v_mfma_f32_16x16x32_bf16 v[22:25], v[140:143], v[208:211], v[22:25]
	v_mfma_f32_16x16x32_bf16 v[14:17], v[154:157], v[208:211], v[14:17]
	v_mfma_f32_16x16x32_bf16 v[62:65], v[150:153], v[188:191], v[62:65]
	v_mfma_f32_16x16x32_bf16 v[58:61], v[158:161], v[188:191], v[58:61]
	v_mfma_f32_16x16x32_bf16 v[54:57], v[150:153], v[196:199], v[54:57]
	v_mfma_f32_16x16x32_bf16 v[46:49], v[158:161], v[196:199], v[46:49]
	v_mfma_f32_16x16x32_bf16 v[38:41], v[150:153], v[204:207], v[38:41]
	v_mfma_f32_16x16x32_bf16 v[30:33], v[158:161], v[204:207], v[30:33]
	v_mfma_f32_16x16x32_bf16 v[22:25], v[150:153], v[212:215], v[22:25]
	v_mfma_f32_16x16x32_bf16 v[14:17], v[158:161], v[212:215], v[14:17]
	s_setprio 0
	s_setprio 1
	v_mfma_f32_16x16x32_bf16 v[50:53], v[162:165], v[184:187], v[50:53]
	v_mfma_f32_16x16x32_bf16 v[42:45], v[170:173], v[184:187], v[42:45]
	v_mfma_f32_16x16x32_bf16 v[34:37], v[162:165], v[192:195], v[34:37]
	v_mfma_f32_16x16x32_bf16 v[26:29], v[170:173], v[192:195], v[26:29]
	v_mfma_f32_16x16x32_bf16 v[18:21], v[162:165], v[200:203], v[18:21]
	v_mfma_f32_16x16x32_bf16 v[10:13], v[170:173], v[200:203], v[10:13]
	v_mfma_f32_16x16x32_bf16 v[6:9], v[162:165], v[208:211], v[6:9]
	v_mfma_f32_16x16x32_bf16 v[2:5], v[170:173], v[208:211], v[2:5]
	v_mfma_f32_16x16x32_bf16 v[50:53], v[166:169], v[188:191], v[50:53]
	v_mfma_f32_16x16x32_bf16 v[42:45], v[174:177], v[188:191], v[42:45]
	v_mfma_f32_16x16x32_bf16 v[34:37], v[166:169], v[196:199], v[34:37]
	v_mfma_f32_16x16x32_bf16 v[26:29], v[174:177], v[196:199], v[26:29]
	v_mfma_f32_16x16x32_bf16 v[18:21], v[166:169], v[204:207], v[18:21]
	v_mfma_f32_16x16x32_bf16 v[10:13], v[174:177], v[204:207], v[10:13]
	v_mfma_f32_16x16x32_bf16 v[6:9], v[166:169], v[212:215], v[6:9]
	v_mfma_f32_16x16x32_bf16 v[2:5], v[174:177], v[212:215], v[2:5]
	s_setprio 0
	s_barrier
	s_add_i32 s51, s51, 2
	s_add_u32 s20, s20, 0x100
	s_addc_u32 s21, s21, 0
	s_add_u32 s49, s49, 0x100
	s_addc_u32 s50, s50, 0
	s_cmp_gt_u32 s51, 13
	s_cbranch_scc0 .LBB0_692
	s_mov_b32 s97, 1
	s_and_b64 vcc, exec, s[8:9]
	s_cbranch_vccz .LBB0_695
	s_barrier

.LBB0_1089:
	s_mov_b32 s97, 0
	v_readlane_b32 s4, v251, 10
	v_readlane_b32 s5, v251, 11
	s_cmp_ge_i32 s2, s4
	s_cselect_b64 s[0:1], -1, 0
	s_cmp_lt_i32 s2, s5
	s_cselect_b64 s[4:5], -1, 0
	s_and_b64 s[4:5], s[0:1], s[4:5]
	s_mov_b64 s[0:1], -1
	s_and_b64 vcc, exec, s[4:5]
	s_cbranch_vccnz .LBB0_1091
	s_add_i32 s0, s44, 6
	v_writelane_b32 v252, s0, 37
	s_mov_b64 s[0:1], 0

; #define PG8_STAGE(bufoff, gbase, voff) do { _Pragma("unroll") for (int _i = 0; _i < 2; ++_i) \
;         __builtin_amdgcn_global_load_lds((const unsigned*)((const char*)(gbase) + (voff)[_i]), (PG8_LAS unsigned*)(lds + (bufoff) + ldsw + _i * 8192), 16, 0, 0); } while (0)
; #define PG8_LDA(dst, b, h) do { _Pragma("unroll") for (int m = 0; m < 4; ++m) _Pragma("unroll") for (int k = 0; k < 2; ++k) dst[m][k] = *(const PG8_LAS bf16x8*)(lds + PG8_SA(b, h) + aoff + m * 2048 + k * 1024); } while (0)
; #define PG8_LDB(dst, b, h) do { _Pragma("unroll") for (int n = 0; n < 2; ++n) _Pragma("unroll") for (int k = 0; k < 2; ++k) dst[n][k] = *(const PG8_LAS bf16x8*)(lds + PG8_SB(b, h) + boff + n * 2048 + k * 1024); } while (0)
; #define PG8_SCHED __builtin_amdgcn_sched_barrier(0)
; template <class Epi, class Sched, bool ALIGN_EPI = false, bool SP2 = false, bool GATHER = false>
; __device__ __forceinline__ void gemm_phase(PG8_LAS unsigned char* lds, const Gemm g, const Sched& S, const Epi& E, int tid_in, const int* rowsrc = nullptr, PG8_LAS int* idx_lds = nullptr) {
;     ...
;         for (int t = 0; t < nt; t += 2) {
;             const bool last = (t == nt - 2);
;             if constexpr (GATHER) {
; #pragma unroll
;                 for (int h_ = 0; h_ < 2; ++h_) { gS[h_][0] = last ? gN[h_][0] : gA[h_][0]; gS[h_][1] = last ? gN[h_][1] : gA[h_][1]; } }
;             const char* a1 = cA + (size_t)(t + 1) * kstep;
;             const char* a2 = last ? nA : cA + (size_t)(t + 2) * kstep; const char* b2 = last ? nB : cB + (size_t)(t + 2) * kstep;
;             const char* a3 = a2 + kstep; const char* b3 = b2 + kstep;
;             if (last && has_next) S.a_ready(nxt);
;             if constexpr (SP2) {
;             PG8_LDB(B0, 0, 0); PG8_LDB(B1, 0, 1); PG8_SCHED; PG8_LDA(At, 0, 0); PG8_STAGE(PG8_SA(1, 1), a1 + hstepA, PG8_OA(1));
.LBB0_1101:
	s_add_u32 s22, s20, 0xfffc0080
	s_addc_u32 s23, s21, -1
	s_add_i32 s58, 0, 0x10000
	s_cmp_eq_u32 s57, 12
	s_cselect_b32 s25, s9, s23
	s_cselect_b32 s24, s17, s22
	s_cselect_b32 s23, s7, s56
	s_cselect_b32 s22, s19, s55
	s_add_i32 s60, 0, 0x14000
	v_add_u32_e32 v142, s58, v184
	v_add_u32_e32 v182, s60, v184
	ds_read_b128 v[122:125], v142
	ds_read_b128 v[126:129], v142 offset:1024
	ds_read_b128 v[134:137], v142 offset:2048
	ds_read_b128 v[142:145], v142 offset:3072
	ds_read_b128 v[174:177], v182
	ds_read_b128 v[178:181], v182 offset:1024
	ds_read_b128 v[188:191], v182 offset:2048
	ds_read_b128 v[192:195], v182 offset:3072
	v_lshl_add_u64 v[182:183], s[20:21], 0, v[170:171]
	s_add_i32 m0, s39, 0xc000
	ds_read_b128 v[196:199], v186
	ds_read_b128 v[200:203], v186 offset:1024
	ds_read_b128 v[204:207], v186 offset:2048
	ds_read_b128 v[208:211], v186 offset:3072
	ds_read_b128 v[212:215], v186 offset:4096
	ds_read_b128 v[216:219], v186 offset:5120
	ds_read_b128 v[220:223], v186 offset:6144
	ds_read_b128 v[224:227], v186 offset:7168
	global_load_lds_dwordx4 v[182:183], off
	v_lshl_add_u64 v[182:183], s[20:21], 0, v[172:173]
	s_add_i32 m0, s39, 0xe000
	s_nop 0
	global_load_lds_dwordx4 v[182:183], off
	s_cmp_eq_u32 s97, 0
	s_cbranch_scc1 .Lew7_a
	s_waitcnt vmcnt(24)
	s_branch .Lew7_b

; #define PG8_STAGE(bufoff, gbase, voff) do { _Pragma("unroll") for (int _i = 0; _i < 2; ++_i) \
;         __builtin_amdgcn_global_load_lds((const unsigned*)((const char*)(gbase) + (voff)[_i]), (PG8_LAS unsigned*)(lds + (bufoff) + ldsw + _i * 8192), 16, 0, 0); } while (0)
; #define PG8_LDA(dst, b, h) do { _Pragma("unroll") for (int m = 0; m < 4; ++m) _Pragma("unroll") for (int k = 0; k < 2; ++k) dst[m][k] = *(const PG8_LAS bf16x8*)(lds + PG8_SA(b, h) + aoff + m * 2048 + k * 1024); } while (0)
; #define PG8_LDB(dst, b, h) do { _Pragma("unroll") for (int n = 0; n < 2; ++n) _Pragma("unroll") for (int k = 0; k < 2; ++k) dst[n][k] = *(const PG8_LAS bf16x8*)(lds + PG8_SB(b, h) + boff + n * 2048 + k * 1024); } while (0)
; #define PG8_MMA(ai, bj, At, Bt) do { __builtin_amdgcn_s_setprio(1); _Pragma("unroll") for (int m = 0; m < 4; ++m) _Pragma("unroll") for (int n = 0; n < 2; ++n) _Pragma("unroll") for (int k = 0; k < 2; ++k) \
;         acc[ai][bj][m][n] = __builtin_amdgcn_mfma_f32_16x16x32_bf16(Bt[n][k], At[m][k], acc[ai][bj][m][n], 0, 0, 0); __builtin_amdgcn_s_setprio(0); } while (0)
; #define PG8_WAIT_V(n) asm volatile("s_waitcnt vmcnt(" #n ")" ::: "memory")
; #define PG8_WAIT_L(n) asm volatile("s_waitcnt lgkmcnt(" #n ")" ::: "memory")
; #define PG8_BAR __builtin_amdgcn_s_barrier()
; #define PG8_SCHED __builtin_amdgcn_sched_barrier(0)
; template <class Epi, class Sched, bool ALIGN_EPI = false, bool SP2 = false, bool GATHER = false>
; __device__ __forceinline__ void gemm_phase(PG8_LAS unsigned char* lds, const Gemm g, const Sched& S, const Epi& E, int tid_in, const int* rowsrc = nullptr, PG8_LAS int* idx_lds = nullptr) {
;     ...
;             PG8_LDB(B0, 0, 0); PG8_LDB(B1, 0, 1); PG8_SCHED; PG8_LDA(At, 0, 0); PG8_STAGE(PG8_SA(1, 1), a1 + hstepA, PG8_OA(1));
;             PG8_WAIT_V(8); PG8_WAIT_L(0); PG8_BAR; PG8_MMA(0, 0, At, B0); PG8_MMA(0, 1, At, B1); PG8_BAR; PG8_SCHED;
;             PG8_LDA(At, 0, 1); PG8_STAGE(PG8_SB(0, 0), b2, voffB); PG8_STAGE(PG8_SB(0, 1), b2 + hstep, voffB); PG8_STAGE(PG8_SA(0, 0), a2, PG8_OS(0));
.Lew7_b:
	s_waitcnt lgkmcnt(0)
	v_mfma_f32_16x16x32_bf16 v[138:141], v[122:125], v[196:199], v[138:141]
	v_mfma_f32_16x16x32_bf16 v[130:133], v[134:137], v[196:199], v[130:133]
	v_mfma_f32_16x16x32_bf16 v[118:121], v[122:125], v[204:207], v[118:121]
	s_barrier
	s_setprio 1
	s_waitcnt lgkmcnt(0)
	v_mfma_f32_16x16x32_bf16 v[106:109], v[134:137], v[204:207], v[106:109]
	v_mfma_f32_16x16x32_bf16 v[102:105], v[122:125], v[212:215], v[102:105]
	v_mfma_f32_16x16x32_bf16 v[90:93], v[134:137], v[212:215], v[90:93]
	v_mfma_f32_16x16x32_bf16 v[86:89], v[122:125], v[220:223], v[86:89]
	v_mfma_f32_16x16x32_bf16 v[74:77], v[134:137], v[220:223], v[74:77]
	v_mfma_f32_16x16x32_bf16 v[138:141], v[126:129], v[200:203], v[138:141]
	v_mfma_f32_16x16x32_bf16 v[130:133], v[142:145], v[200:203], v[130:133]
	v_mfma_f32_16x16x32_bf16 v[118:121], v[126:129], v[208:211], v[118:121]
	v_mfma_f32_16x16x32_bf16 v[106:109], v[142:145], v[208:211], v[106:109]
	v_mfma_f32_16x16x32_bf16 v[102:105], v[126:129], v[216:219], v[102:105]
	v_mfma_f32_16x16x32_bf16 v[90:93], v[142:145], v[216:219], v[90:93]
	v_mfma_f32_16x16x32_bf16 v[86:89], v[126:129], v[224:227], v[86:89]
	v_mfma_f32_16x16x32_bf16 v[74:77], v[142:145], v[224:227], v[74:77]
	s_setprio 0
	s_setprio 1
	v_mfma_f32_16x16x32_bf16 v[114:117], v[174:177], v[196:199], v[114:117]
	v_mfma_f32_16x16x32_bf16 v[110:113], v[188:191], v[196:199], v[110:113]
	v_mfma_f32_16x16x32_bf16 v[98:101], v[174:177], v[204:207], v[98:101]
	v_mfma_f32_16x16x32_bf16 v[94:97], v[188:191], v[204:207], v[94:97]
	v_mfma_f32_16x16x32_bf16 v[82:85], v[174:177], v[212:215], v[82:85]
	v_mfma_f32_16x16x32_bf16 v[78:81], v[188:191], v[212:215], v[78:81]
	v_mfma_f32_16x16x32_bf16 v[70:73], v[174:177], v[220:223], v[70:73]
	v_mfma_f32_16x16x32_bf16 v[66:69], v[188:191], v[220:223], v[66:69]
	v_mfma_f32_16x16x32_bf16 v[114:117], v[178:181], v[200:203], v[114:117]
	v_mfma_f32_16x16x32_bf16 v[110:113], v[192:195], v[200:203], v[110:113]
	v_mfma_f32_16x16x32_bf16 v[98:101], v[178:181], v[208:211], v[98:101]
	v_mfma_f32_16x16x32_bf16 v[94:97], v[192:195], v[208:211], v[94:97]
	v_mfma_f32_16x16x32_bf16 v[82:85], v[178:181], v[216:219], v[82:85]
	v_mfma_f32_16x16x32_bf16 v[78:81], v[192:195], v[216:219], v[78:81]
	v_mfma_f32_16x16x32_bf16 v[70:73], v[178:181], v[224:227], v[70:73]
	v_mfma_f32_16x16x32_bf16 v[66:69], v[192:195], v[224:227], v[66:69]
	s_setprio 0
	s_barrier
	s_add_i32 s58, s58, s38
	v_lshl_add_u64 v[182:183], s[22:23], 0, v[0:1]
	s_mov_b32 m0, s58
	ds_read_b128 v[196:199], v186 offset:16384
	ds_read_b128 v[200:203], v186 offset:17408
	ds_read_b128 v[204:207], v186 offset:18432
	ds_read_b128 v[208:211], v186 offset:19456
	ds_read_b128 v[212:215], v186 offset:20480
	ds_read_b128 v[216:219], v186 offset:21504
	ds_read_b128 v[220:223], v186 offset:22528
	ds_read_b128 v[224:227], v186 offset:23552
	global_load_lds_dwordx4 v[182:183], off
	s_add_i32 m0, s58, 0x2000
	s_add_u32 s58, s22, 0x40000
	v_lshl_add_u64 v[228:229], s[22:23], 0, v[148:149]
	s_addc_u32 s59, s23, 0
	s_add_i32 s60, s60, s38
	global_load_lds_dwordx4 v[228:229], off
	v_lshl_add_u64 v[230:231], s[58:59], 0, v[0:1]
	s_mov_b32 m0, s60
	v_lshl_add_u64 v[232:233], s[24:25], 0, v[150:151]
	global_load_lds_dwordx4 v[230:231], off
	v_lshl_add_u64 v[230:231], s[58:59], 0, v[148:149]
	s_add_i32 m0, s60, 0x2000
	s_nop 0
	global_load_lds_dwordx4 v[230:231], off
	v_lshl_add_u64 v[230:231], s[24:25], 0, v[152:153]
	s_mov_b32 m0, s39
	s_nop 0
	global_load_lds_dwordx4 v[230:231], off
	s_mov_b32 m0, s41
	s_nop 0
	global_load_lds_dwordx4 v[232:233], off
	s_cmp_eq_u32 s97, 0
	s_cbranch_scc1 .Lew8_a
	s_waitcnt vmcnt(24)
	s_branch .Lew8_b

; #define PG8_STAGE(bufoff, gbase, voff) do { _Pragma("unroll") for (int _i = 0; _i < 2; ++_i) \
;         __builtin_amdgcn_global_load_lds((const unsigned*)((const char*)(gbase) + (voff)[_i]), (PG8_LAS unsigned*)(lds + (bufoff) + ldsw + _i * 8192), 16, 0, 0); } while (0)
; #define PG8_LDA(dst, b, h) do { _Pragma("unroll") for (int m = 0; m < 4; ++m) _Pragma("unroll") for (int k = 0; k < 2; ++k) dst[m][k] = *(const PG8_LAS bf16x8*)(lds + PG8_SA(b, h) + aoff + m * 2048 + k * 1024); } while (0)
; #define PG8_LDB(dst, b, h) do { _Pragma("unroll") for (int n = 0; n < 2; ++n) _Pragma("unroll") for (int k = 0; k < 2; ++k) dst[n][k] = *(const PG8_LAS bf16x8*)(lds + PG8_SB(b, h) + boff + n * 2048 + k * 1024); } while (0)
; #define PG8_MMA(ai, bj, At, Bt) do { __builtin_amdgcn_s_setprio(1); _Pragma("unroll") for (int m = 0; m < 4; ++m) _Pragma("unroll") for (int n = 0; n < 2; ++n) _Pragma("unroll") for (int k = 0; k < 2; ++k) \
;         acc[ai][bj][m][n] = __builtin_amdgcn_mfma_f32_16x16x32_bf16(Bt[n][k], At[m][k], acc[ai][bj][m][n], 0, 0, 0); __builtin_amdgcn_s_setprio(0); } while (0)
; #define PG8_WAIT_V(n) asm volatile("s_waitcnt vmcnt(" #n ")" ::: "memory")
; #define PG8_WAIT_L(n) asm volatile("s_waitcnt lgkmcnt(" #n ")" ::: "memory")
; #define PG8_BAR __builtin_amdgcn_s_barrier()
; #define PG8_SCHED __builtin_amdgcn_sched_barrier(0)
; template <class Epi, class Sched, bool ALIGN_EPI = false, bool SP2 = false, bool GATHER = false>
; __device__ __forceinline__ void gemm_phase(PG8_LAS unsigned char* lds, const Gemm g, const Sched& S, const Epi& E, int tid_in, const int* rowsrc = nullptr, PG8_LAS int* idx_lds = nullptr) {
;     ...
;             PG8_WAIT_V(8); PG8_WAIT_L(0); PG8_BAR; PG8_MMA(1, 0, At, B0); PG8_MMA(1, 1, At, B1); PG8_BAR; PG8_SCHED;
;             PG8_LDB(B0, 1, 0); PG8_LDB(B1, 1, 1); PG8_SCHED; PG8_LDA(At, 1, 0); PG8_STAGE(PG8_SA(0, 1), a2 + hstepA, PG8_OS(1));
;             PG8_WAIT_V(8); PG8_WAIT_L(0); PG8_BAR; PG8_MMA(0, 0, At, B0); PG8_MMA(0, 1, At, B1); PG8_BAR; PG8_SCHED;
.Lew8_b:
	s_mov_b32 s97, 0
	s_waitcnt lgkmcnt(0)
	v_mfma_f32_16x16x32_bf16 v[62:65], v[122:125], v[196:199], v[62:65]
	v_mfma_f32_16x16x32_bf16 v[58:61], v[134:137], v[196:199], v[58:61]
	v_mfma_f32_16x16x32_bf16 v[54:57], v[122:125], v[204:207], v[54:57]
	s_barrier
	s_setprio 1
	s_waitcnt lgkmcnt(0)
	v_mfma_f32_16x16x32_bf16 v[42:45], v[134:137], v[204:207], v[42:45]
	v_mfma_f32_16x16x32_bf16 v[38:41], v[122:125], v[212:215], v[38:41]
	v_mfma_f32_16x16x32_bf16 v[26:29], v[134:137], v[212:215], v[26:29]
	v_mfma_f32_16x16x32_bf16 v[22:25], v[122:125], v[220:223], v[22:25]
	v_mfma_f32_16x16x32_bf16 v[10:13], v[134:137], v[220:223], v[10:13]
	v_mfma_f32_16x16x32_bf16 v[62:65], v[126:129], v[200:203], v[62:65]
	v_mfma_f32_16x16x32_bf16 v[58:61], v[142:145], v[200:203], v[58:61]
	v_mfma_f32_16x16x32_bf16 v[54:57], v[126:129], v[208:211], v[54:57]
	v_mfma_f32_16x16x32_bf16 v[42:45], v[142:145], v[208:211], v[42:45]
	v_mfma_f32_16x16x32_bf16 v[38:41], v[126:129], v[216:219], v[38:41]
	v_mfma_f32_16x16x32_bf16 v[26:29], v[142:145], v[216:219], v[26:29]
	v_mfma_f32_16x16x32_bf16 v[22:25], v[126:129], v[224:227], v[22:25]
	v_mfma_f32_16x16x32_bf16 v[10:13], v[142:145], v[224:227], v[10:13]
	s_setprio 0
	s_setprio 1
	v_mfma_f32_16x16x32_bf16 v[50:53], v[174:177], v[196:199], v[50:53]
	v_mfma_f32_16x16x32_bf16 v[46:49], v[188:191], v[196:199], v[46:49]
	v_mfma_f32_16x16x32_bf16 v[34:37], v[174:177], v[204:207], v[34:37]
	v_mfma_f32_16x16x32_bf16 v[30:33], v[188:191], v[204:207], v[30:33]
	v_mfma_f32_16x16x32_bf16 v[18:21], v[174:177], v[212:215], v[18:21]
	v_mfma_f32_16x16x32_bf16 v[14:17], v[188:191], v[212:215], v[14:17]
	v_mfma_f32_16x16x32_bf16 v[6:9], v[174:177], v[220:223], v[6:9]
	v_mfma_f32_16x16x32_bf16 v[2:5], v[188:191], v[220:223], v[2:5]
	v_mfma_f32_16x16x32_bf16 v[50:53], v[178:181], v[200:203], v[50:53]
	v_mfma_f32_16x16x32_bf16 v[46:49], v[192:195], v[200:203], v[46:49]
	v_mfma_f32_16x16x32_bf16 v[34:37], v[178:181], v[208:211], v[34:37]
	v_mfma_f32_16x16x32_bf16 v[30:33], v[192:195], v[208:211], v[30:33]
	v_mfma_f32_16x16x32_bf16 v[18:21], v[178:181], v[216:219], v[18:21]
	v_mfma_f32_16x16x32_bf16 v[14:17], v[192:195], v[216:219], v[14:17]
	v_mfma_f32_16x16x32_bf16 v[6:9], v[178:181], v[224:227], v[6:9]
	v_mfma_f32_16x16x32_bf16 v[2:5], v[192:195], v[224:227], v[2:5]
	s_setprio 0
	s_barrier
	s_add_i32 s58, 0, 0x18000
	s_add_i32 s59, 0, 0x1c000
	v_add_u32_e32 v142, s58, v184
	v_add_u32_e32 v187, s59, v184
	ds_read_b128 v[122:125], v142
	ds_read_b128 v[126:129], v142 offset:1024
	ds_read_b128 v[134:137], v142 offset:2048
	ds_read_b128 v[142:145], v142 offset:3072
	ds_read_b128 v[174:177], v187
	ds_read_b128 v[178:181], v187 offset:1024
	ds_read_b128 v[188:191], v187 offset:2048
	ds_read_b128 v[192:195], v187 offset:3072
	s_add_u32 s24, s24, 0x40000
	s_addc_u32 s25, s25, 0
	s_mov_b32 m0, s43
	v_lshl_add_u64 v[234:235], s[24:25], 0, v[152:153]
	ds_read_b128 v[196:199], v186 offset:32768
	ds_read_b128 v[200:203], v186 offset:33792
	ds_read_b128 v[204:207], v186 offset:34816
	ds_read_b128 v[208:211], v186 offset:35840
	ds_read_b128 v[212:215], v186 offset:36864
	ds_read_b128 v[216:219], v186 offset:37888
	ds_read_b128 v[220:223], v186 offset:38912
	ds_read_b128 v[224:227], v186 offset:39936
	global_load_lds_dwordx4 v[234:235], off
	v_lshl_add_u64 v[234:235], s[24:25], 0, v[150:151]
	s_mov_b32 m0, s45
	s_nop 0
	global_load_lds_dwordx4 v[234:235], off
	s_waitcnt vmcnt(8)
	s_waitcnt lgkmcnt(0)
	v_mfma_f32_16x16x32_bf16 v[138:141], v[122:125], v[196:199], v[138:141]
	v_mfma_f32_16x16x32_bf16 v[130:133], v[134:137], v[196:199], v[130:133]
	v_mfma_f32_16x16x32_bf16 v[118:121], v[122:125], v[204:207], v[118:121]
	s_barrier
	s_setprio 1
	s_waitcnt lgkmcnt(0)
	v_mfma_f32_16x16x32_bf16 v[106:109], v[134:137], v[204:207], v[106:109]
	v_mfma_f32_16x16x32_bf16 v[102:105], v[122:125], v[212:215], v[102:105]
	v_mfma_f32_16x16x32_bf16 v[90:93], v[134:137], v[212:215], v[90:93]
	v_mfma_f32_16x16x32_bf16 v[86:89], v[122:125], v[220:223], v[86:89]
	v_mfma_f32_16x16x32_bf16 v[74:77], v[134:137], v[220:223], v[74:77]
	v_mfma_f32_16x16x32_bf16 v[138:141], v[126:129], v[200:203], v[138:141]
	v_mfma_f32_16x16x32_bf16 v[130:133], v[142:145], v[200:203], v[130:133]
	v_mfma_f32_16x16x32_bf16 v[118:121], v[126:129], v[208:211], v[118:121]
	v_mfma_f32_16x16x32_bf16 v[106:109], v[142:145], v[208:211], v[106:109]
	v_mfma_f32_16x16x32_bf16 v[102:105], v[126:129], v[216:219], v[102:105]
	v_mfma_f32_16x16x32_bf16 v[90:93], v[142:145], v[216:219], v[90:93]
	v_mfma_f32_16x16x32_bf16 v[86:89], v[126:129], v[224:227], v[86:89]
	v_mfma_f32_16x16x32_bf16 v[74:77], v[142:145], v[224:227], v[74:77]
	s_setprio 0
	s_setprio 1
	v_mfma_f32_16x16x32_bf16 v[114:117], v[174:177], v[196:199], v[114:117]
	v_mfma_f32_16x16x32_bf16 v[110:113], v[188:191], v[196:199], v[110:113]
	v_mfma_f32_16x16x32_bf16 v[98:101], v[174:177], v[204:207], v[98:101]
	v_mfma_f32_16x16x32_bf16 v[94:97], v[188:191], v[204:207], v[94:97]
	v_mfma_f32_16x16x32_bf16 v[82:85], v[174:177], v[212:215], v[82:85]
	v_mfma_f32_16x16x32_bf16 v[78:81], v[188:191], v[212:215], v[78:81]
	v_mfma_f32_16x16x32_bf16 v[70:73], v[174:177], v[220:223], v[70:73]
	v_mfma_f32_16x16x32_bf16 v[66:69], v[188:191], v[220:223], v[66:69]
	v_mfma_f32_16x16x32_bf16 v[114:117], v[178:181], v[200:203], v[114:117]
	v_mfma_f32_16x16x32_bf16 v[110:113], v[192:195], v[200:203], v[110:113]
	v_mfma_f32_16x16x32_bf16 v[98:101], v[178:181], v[208:211], v[98:101]
	v_mfma_f32_16x16x32_bf16 v[94:97], v[192:195], v[208:211], v[94:97]
	v_mfma_f32_16x16x32_bf16 v[82:85], v[178:181], v[216:219], v[82:85]
	v_mfma_f32_16x16x32_bf16 v[78:81], v[192:195], v[216:219], v[78:81]
	v_mfma_f32_16x16x32_bf16 v[70:73], v[178:181], v[224:227], v[70:73]
	v_mfma_f32_16x16x32_bf16 v[66:69], v[192:195], v[224:227], v[66:69]
	s_setprio 0
	s_barrier
; #define PG8_STAGE(bufoff, gbase, voff) do { _Pragma("unroll") for (int _i = 0; _i < 2; ++_i) \
;         __builtin_amdgcn_global_load_lds((const unsigned*)((const char*)(gbase) + (voff)[_i]), (PG8_LAS unsigned*)(lds + (bufoff) + ldsw + _i * 8192), 16, 0, 0); } while (0)
; #define PG8_LDA(dst, b, h) do { _Pragma("unroll") for (int m = 0; m < 4; ++m) _Pragma("unroll") for (int k = 0; k < 2; ++k) dst[m][k] = *(const PG8_LAS bf16x8*)(lds + PG8_SA(b, h) + aoff + m * 2048 + k * 1024); } while (0)
; #define PG8_MMA(ai, bj, At, Bt) do { __builtin_amdgcn_s_setprio(1); _Pragma("unroll") for (int m = 0; m < 4; ++m) _Pragma("unroll") for (int n = 0; n < 2; ++n) _Pragma("unroll") for (int k = 0; k < 2; ++k) \
;         acc[ai][bj][m][n] = __builtin_amdgcn_mfma_f32_16x16x32_bf16(Bt[n][k], At[m][k], acc[ai][bj][m][n], 0, 0, 0); __builtin_amdgcn_s_setprio(0); } while (0)
; #define PG8_WAIT_V(n) asm volatile("s_waitcnt vmcnt(" #n ")" ::: "memory")
; #define PG8_WAIT_L(n) asm volatile("s_waitcnt lgkmcnt(" #n ")" ::: "memory")
; #define PG8_BAR __builtin_amdgcn_s_barrier()
; #define PG8_SCHED __builtin_amdgcn_sched_barrier(0)
; template <class Epi, class Sched, bool ALIGN_EPI = false, bool SP2 = false, bool GATHER = false>
; __device__ __forceinline__ void gemm_phase(PG8_LAS unsigned char* lds, const Gemm g, const Sched& S, const Epi& E, int tid_in, const int* rowsrc = nullptr, PG8_LAS int* idx_lds = nullptr) {
;     ...
;             PG8_LDA(At, 1, 1); PG8_STAGE(PG8_SB(1, 0), b3, voffB); PG8_STAGE(PG8_SB(1, 1), b3 + hstep, voffB); PG8_STAGE(PG8_SA(1, 0), a3, PG8_OS(0));
;             PG8_WAIT_V(8); PG8_WAIT_L(0); PG8_BAR; PG8_MMA(1, 0, At, B0); PG8_MMA(1, 1, At, B1); PG8_BAR; PG8_SCHED;
;     ...
;         if constexpr (ALIGN_EPI) { if (wr == 0) PG8_BAR; }
	s_add_i32 s24, s58, s38
	v_lshl_add_u64 v[182:183], v[182:183], 0, s[10:11]
	s_mov_b32 m0, s24
	ds_read_b128 v[196:199], v186 offset:49152
	ds_read_b128 v[200:203], v186 offset:50176
	ds_read_b128 v[204:207], v186 offset:51200
	ds_read_b128 v[208:211], v186 offset:52224
	ds_read_b128 v[212:215], v186 offset:53248
	ds_read_b128 v[216:219], v186 offset:54272
	ds_read_b128 v[220:223], v186 offset:55296
	ds_read_b128 v[224:227], v186 offset:56320
	global_load_lds_dwordx4 v[182:183], off
	s_add_i32 m0, s24, 0x2000
	s_add_u32 s22, s22, 0x40080
	v_lshl_add_u64 v[182:183], v[228:229], 0, s[10:11]
	s_addc_u32 s23, s23, 0
	s_add_i32 s24, s59, s38
	global_load_lds_dwordx4 v[182:183], off
	v_lshl_add_u64 v[182:183], s[22:23], 0, v[0:1]
	s_mov_b32 m0, s24
	s_nop 0
	global_load_lds_dwordx4 v[182:183], off
	v_lshl_add_u64 v[182:183], s[22:23], 0, v[148:149]
	s_add_i32 m0, s24, 0x2000
	s_nop 0
	global_load_lds_dwordx4 v[182:183], off
	v_lshl_add_u64 v[182:183], v[230:231], 0, s[10:11]
	s_mov_b32 m0, s52
	s_nop 0
	global_load_lds_dwordx4 v[182:183], off
	v_lshl_add_u64 v[182:183], v[232:233], 0, s[10:11]
	s_mov_b32 m0, s53
	s_nop 0
	global_load_lds_dwordx4 v[182:183], off
	s_waitcnt vmcnt(8)
	s_waitcnt lgkmcnt(0)
	v_mfma_f32_16x16x32_bf16 v[62:65], v[122:125], v[196:199], v[62:65]
	v_mfma_f32_16x16x32_bf16 v[58:61], v[134:137], v[196:199], v[58:61]
	v_mfma_f32_16x16x32_bf16 v[54:57], v[122:125], v[204:207], v[54:57]
	s_barrier
	s_setprio 1
	s_waitcnt lgkmcnt(0)
	v_mfma_f32_16x16x32_bf16 v[42:45], v[134:137], v[204:207], v[42:45]
	v_mfma_f32_16x16x32_bf16 v[38:41], v[122:125], v[212:215], v[38:41]
	v_mfma_f32_16x16x32_bf16 v[26:29], v[134:137], v[212:215], v[26:29]
	v_mfma_f32_16x16x32_bf16 v[22:25], v[122:125], v[220:223], v[22:25]
	v_mfma_f32_16x16x32_bf16 v[10:13], v[134:137], v[220:223], v[10:13]
	v_mfma_f32_16x16x32_bf16 v[62:65], v[126:129], v[200:203], v[62:65]
	v_mfma_f32_16x16x32_bf16 v[58:61], v[142:145], v[200:203], v[58:61]
	v_mfma_f32_16x16x32_bf16 v[54:57], v[126:129], v[208:211], v[54:57]
	v_mfma_f32_16x16x32_bf16 v[42:45], v[142:145], v[208:211], v[42:45]
	v_mfma_f32_16x16x32_bf16 v[38:41], v[126:129], v[216:219], v[38:41]
	v_mfma_f32_16x16x32_bf16 v[26:29], v[142:145], v[216:219], v[26:29]
	v_mfma_f32_16x16x32_bf16 v[22:25], v[126:129], v[224:227], v[22:25]
	v_mfma_f32_16x16x32_bf16 v[10:13], v[142:145], v[224:227], v[10:13]
	s_setprio 0
	s_setprio 1
	v_mfma_f32_16x16x32_bf16 v[50:53], v[174:177], v[196:199], v[50:53]
	v_mfma_f32_16x16x32_bf16 v[46:49], v[188:191], v[196:199], v[46:49]
	v_mfma_f32_16x16x32_bf16 v[34:37], v[174:177], v[204:207], v[34:37]
	v_mfma_f32_16x16x32_bf16 v[30:33], v[188:191], v[204:207], v[30:33]
	v_mfma_f32_16x16x32_bf16 v[18:21], v[174:177], v[212:215], v[18:21]
	v_mfma_f32_16x16x32_bf16 v[14:17], v[188:191], v[212:215], v[14:17]
	v_mfma_f32_16x16x32_bf16 v[6:9], v[174:177], v[220:223], v[6:9]
	v_mfma_f32_16x16x32_bf16 v[2:5], v[188:191], v[220:223], v[2:5]
	v_mfma_f32_16x16x32_bf16 v[50:53], v[178:181], v[200:203], v[50:53]
	v_mfma_f32_16x16x32_bf16 v[46:49], v[192:195], v[200:203], v[46:49]
	v_mfma_f32_16x16x32_bf16 v[34:37], v[178:181], v[208:211], v[34:37]
	v_mfma_f32_16x16x32_bf16 v[30:33], v[192:195], v[208:211], v[30:33]
	v_mfma_f32_16x16x32_bf16 v[18:21], v[178:181], v[216:219], v[18:21]
	v_mfma_f32_16x16x32_bf16 v[14:17], v[192:195], v[216:219], v[14:17]
	v_mfma_f32_16x16x32_bf16 v[6:9], v[178:181], v[224:227], v[6:9]
	v_mfma_f32_16x16x32_bf16 v[2:5], v[192:195], v[224:227], v[2:5]
	s_setprio 0
	s_barrier
	s_add_i32 s57, s57, 2
	s_add_u32 s20, s20, 0x100
	s_addc_u32 s21, s21, 0
	s_add_u32 s55, s55, 0x100
	s_addc_u32 s56, s56, 0
	s_cmp_gt_u32 s57, 13
	s_cbranch_scc0 .LBB0_1101
	s_mov_b32 s97, 1
	s_and_b64 vcc, exec, s[4:5]
	s_cbranch_vccz .LBB0_1104
	s_barrier

.LBB0_1115:
	v_readlane_b32 s0, v252, 34
	v_readlane_b32 s1, v252, 35
	s_and_b64 s[0:1], s[0:1], exec
	s_mov_b32 s0, 0xb00000
	s_mov_b32 s97, 0
	v_readlane_b32 s4, v251, 10
	s_cselect_b32 s47, s0, 0x400000
	v_readlane_b32 s5, v251, 11
	s_cmp_ge_i32 s40, s4
	s_cselect_b64 s[0:1], -1, 0
	s_cmp_lt_i32 s40, s5
	s_cselect_b64 s[4:5], -1, 0
	s_and_b64 s[4:5], s[0:1], s[4:5]
	s_mov_b64 s[0:1], -1
	s_and_b64 vcc, exec, s[4:5]
	s_cbranch_vccnz .LBB0_1117
	s_add_i32 s2, s44, 2
	s_mov_b64 s[0:1], 0

; #define PG8_STAGE(bufoff, gbase, voff) do { _Pragma("unroll") for (int _i = 0; _i < 2; ++_i) \
;         __builtin_amdgcn_global_load_lds((const unsigned*)((const char*)(gbase) + (voff)[_i]), (PG8_LAS unsigned*)(lds + (bufoff) + ldsw + _i * 8192), 16, 0, 0); } while (0)
; #define PG8_LDA(dst, b, h) do { _Pragma("unroll") for (int m = 0; m < 4; ++m) _Pragma("unroll") for (int k = 0; k < 2; ++k) dst[m][k] = *(const PG8_LAS bf16x8*)(lds + PG8_SA(b, h) + aoff + m * 2048 + k * 1024); } while (0)
; #define PG8_LDB(dst, b, h) do { _Pragma("unroll") for (int n = 0; n < 2; ++n) _Pragma("unroll") for (int k = 0; k < 2; ++k) dst[n][k] = *(const PG8_LAS bf16x8*)(lds + PG8_SB(b, h) + boff + n * 2048 + k * 1024); } while (0)
; #define PG8_SCHED __builtin_amdgcn_sched_barrier(0)
; template <class Epi, class Sched, bool ALIGN_EPI = false, bool SP2 = false, bool GATHER = false>
; __device__ __forceinline__ void gemm_phase(PG8_LAS unsigned char* lds, const Gemm g, const Sched& S, const Epi& E, int tid_in, const int* rowsrc = nullptr, PG8_LAS int* idx_lds = nullptr) {
;     ...
;         for (int t = 0; t < nt; t += 2) {
;             const bool last = (t == nt - 2);
;             if constexpr (GATHER) {
; #pragma unroll
;                 for (int h_ = 0; h_ < 2; ++h_) { gS[h_][0] = last ? gN[h_][0] : gA[h_][0]; gS[h_][1] = last ? gN[h_][1] : gA[h_][1]; } }
;             const char* a1 = cA + (size_t)(t + 1) * kstep;
;             const char* a2 = last ? nA : cA + (size_t)(t + 2) * kstep; const char* b2 = last ? nB : cB + (size_t)(t + 2) * kstep;
;             const char* a3 = a2 + kstep; const char* b3 = b2 + kstep;
;             if (last && has_next) S.a_ready(nxt);
;             if constexpr (SP2) {
;             PG8_LDB(B0, 0, 0); PG8_LDB(B1, 0, 1); PG8_SCHED; PG8_LDA(At, 0, 0); PG8_STAGE(PG8_SA(1, 1), a1 + hstepA, PG8_OA(1));
.LBB0_1127:
	s_add_u32 s22, s20, 0xfffc0080
	s_addc_u32 s23, s21, -1
	s_add_i32 s52, 0, 0x10000
	s_cmp_eq_u32 s51, 12
	s_cselect_b32 s25, s15, s23
	s_cselect_b32 s24, s45, s22
	v_add_u32_e32 v140, s52, v143
	s_cselect_b32 s23, s13, s50
	s_cselect_b32 s22, s48, s49
	s_add_i32 s54, 0, 0x14000
	ds_read_b128 v[148:151], v140
	ds_read_b128 v[152:155], v140 offset:1024
	ds_read_b128 v[156:159], v140 offset:2048
	ds_read_b128 v[160:163], v140 offset:3072
	v_add_u32_e32 v140, s54, v143
	ds_read_b128 v[164:167], v140
	ds_read_b128 v[168:171], v140 offset:1024
	ds_read_b128 v[172:175], v140 offset:2048
	ds_read_b128 v[184:187], v140 offset:3072
	v_lshl_add_u64 v[140:141], s[20:21], 0, v[136:137]
	s_add_i32 m0, s31, 0xc000
	ds_read_b128 v[188:191], v145
	ds_read_b128 v[192:195], v145 offset:1024
	ds_read_b128 v[196:199], v145 offset:2048
	ds_read_b128 v[200:203], v145 offset:3072
	ds_read_b128 v[204:207], v145 offset:4096
	ds_read_b128 v[208:211], v145 offset:5120
	ds_read_b128 v[212:215], v145 offset:6144
	ds_read_b128 v[216:219], v145 offset:7168
	global_load_lds_dwordx4 v[140:141], off
	v_lshl_add_u64 v[140:141], s[20:21], 0, v[138:139]
	s_add_i32 m0, s31, 0xe000
	s_nop 0
	global_load_lds_dwordx4 v[140:141], off
	s_cmp_eq_u32 s97, 0
	s_cbranch_scc1 .Lew9_a
	s_waitcnt vmcnt(24)
	s_branch .Lew9_b

; #define PG8_STAGE(bufoff, gbase, voff) do { _Pragma("unroll") for (int _i = 0; _i < 2; ++_i) \
;         __builtin_amdgcn_global_load_lds((const unsigned*)((const char*)(gbase) + (voff)[_i]), (PG8_LAS unsigned*)(lds + (bufoff) + ldsw + _i * 8192), 16, 0, 0); } while (0)
; #define PG8_LDA(dst, b, h) do { _Pragma("unroll") for (int m = 0; m < 4; ++m) _Pragma("unroll") for (int k = 0; k < 2; ++k) dst[m][k] = *(const PG8_LAS bf16x8*)(lds + PG8_SA(b, h) + aoff + m * 2048 + k * 1024); } while (0)
; #define PG8_LDB(dst, b, h) do { _Pragma("unroll") for (int n = 0; n < 2; ++n) _Pragma("unroll") for (int k = 0; k < 2; ++k) dst[n][k] = *(const PG8_LAS bf16x8*)(lds + PG8_SB(b, h) + boff + n * 2048 + k * 1024); } while (0)
; #define PG8_MMA(ai, bj, At, Bt) do { __builtin_amdgcn_s_setprio(1); _Pragma("unroll") for (int m = 0; m < 4; ++m) _Pragma("unroll") for (int n = 0; n < 2; ++n) _Pragma("unroll") for (int k = 0; k < 2; ++k) \
;         acc[ai][bj][m][n] = __builtin_amdgcn_mfma_f32_16x16x32_bf16(Bt[n][k], At[m][k], acc[ai][bj][m][n], 0, 0, 0); __builtin_amdgcn_s_setprio(0); } while (0)
; #define PG8_WAIT_V(n) asm volatile("s_waitcnt vmcnt(" #n ")" ::: "memory")
; #define PG8_WAIT_L(n) asm volatile("s_waitcnt lgkmcnt(" #n ")" ::: "memory")
; #define PG8_BAR __builtin_amdgcn_s_barrier()
; #define PG8_SCHED __builtin_amdgcn_sched_barrier(0)
; template <class Epi, class Sched, bool ALIGN_EPI = false, bool SP2 = false, bool GATHER = false>
; __device__ __forceinline__ void gemm_phase(PG8_LAS unsigned char* lds, const Gemm g, const Sched& S, const Epi& E, int tid_in, const int* rowsrc = nullptr, PG8_LAS int* idx_lds = nullptr) {
;     ...
;             PG8_LDB(B0, 0, 0); PG8_LDB(B1, 0, 1); PG8_SCHED; PG8_LDA(At, 0, 0); PG8_STAGE(PG8_SA(1, 1), a1 + hstepA, PG8_OA(1));
;             PG8_WAIT_V(8); PG8_WAIT_L(0); PG8_BAR; PG8_MMA(0, 0, At, B0); PG8_MMA(0, 1, At, B1); PG8_BAR; PG8_SCHED;
;             PG8_LDA(At, 0, 1); PG8_STAGE(PG8_SB(0, 0), b2, voffB); PG8_STAGE(PG8_SB(0, 1), b2 + hstep, voffB); PG8_STAGE(PG8_SA(0, 0), a2, PG8_OS(0));
.Lew9_b:
	s_waitcnt lgkmcnt(0)
	v_mfma_f32_16x16x32_bf16 v[126:129], v[148:151], v[188:191], v[126:129]
	v_mfma_f32_16x16x32_bf16 v[122:125], v[156:159], v[188:191], v[122:125]
	v_mfma_f32_16x16x32_bf16 v[118:121], v[148:151], v[196:199], v[118:121]
	s_barrier
	s_setprio 1
	s_waitcnt lgkmcnt(0)
	v_mfma_f32_16x16x32_bf16 v[110:113], v[156:159], v[196:199], v[110:113]
	v_mfma_f32_16x16x32_bf16 v[102:105], v[148:151], v[204:207], v[102:105]
	v_mfma_f32_16x16x32_bf16 v[94:97], v[156:159], v[204:207], v[94:97]
	v_mfma_f32_16x16x32_bf16 v[86:89], v[148:151], v[212:215], v[86:89]
	v_mfma_f32_16x16x32_bf16 v[78:81], v[156:159], v[212:215], v[78:81]
	v_mfma_f32_16x16x32_bf16 v[126:129], v[152:155], v[192:195], v[126:129]
	v_mfma_f32_16x16x32_bf16 v[122:125], v[160:163], v[192:195], v[122:125]
	v_mfma_f32_16x16x32_bf16 v[118:121], v[152:155], v[200:203], v[118:121]
	v_mfma_f32_16x16x32_bf16 v[110:113], v[160:163], v[200:203], v[110:113]
	v_mfma_f32_16x16x32_bf16 v[102:105], v[152:155], v[208:211], v[102:105]
	v_mfma_f32_16x16x32_bf16 v[94:97], v[160:163], v[208:211], v[94:97]
	v_mfma_f32_16x16x32_bf16 v[86:89], v[152:155], v[216:219], v[86:89]
	v_mfma_f32_16x16x32_bf16 v[78:81], v[160:163], v[216:219], v[78:81]
	s_setprio 0
	s_setprio 1
	v_mfma_f32_16x16x32_bf16 v[114:117], v[164:167], v[188:191], v[114:117]
	v_mfma_f32_16x16x32_bf16 v[106:109], v[172:175], v[188:191], v[106:109]
	v_mfma_f32_16x16x32_bf16 v[98:101], v[164:167], v[196:199], v[98:101]
	v_mfma_f32_16x16x32_bf16 v[90:93], v[172:175], v[196:199], v[90:93]
	v_mfma_f32_16x16x32_bf16 v[82:85], v[164:167], v[204:207], v[82:85]
	v_mfma_f32_16x16x32_bf16 v[74:77], v[172:175], v[204:207], v[74:77]
	v_mfma_f32_16x16x32_bf16 v[70:73], v[164:167], v[212:215], v[70:73]
	v_mfma_f32_16x16x32_bf16 v[66:69], v[172:175], v[212:215], v[66:69]
	v_mfma_f32_16x16x32_bf16 v[114:117], v[168:171], v[192:195], v[114:117]
	v_mfma_f32_16x16x32_bf16 v[106:109], v[184:187], v[192:195], v[106:109]
	v_mfma_f32_16x16x32_bf16 v[98:101], v[168:171], v[200:203], v[98:101]
	v_mfma_f32_16x16x32_bf16 v[90:93], v[184:187], v[200:203], v[90:93]
	v_mfma_f32_16x16x32_bf16 v[82:85], v[168:171], v[208:211], v[82:85]
	v_mfma_f32_16x16x32_bf16 v[74:77], v[184:187], v[208:211], v[74:77]
	v_mfma_f32_16x16x32_bf16 v[70:73], v[168:171], v[216:219], v[70:73]
	v_mfma_f32_16x16x32_bf16 v[66:69], v[184:187], v[216:219], v[66:69]
	s_setprio 0
	s_barrier
	s_add_i32 s52, s52, s30
	v_lshl_add_u64 v[140:141], s[22:23], 0, v[0:1]
	s_mov_b32 m0, s52
	ds_read_b128 v[188:191], v145 offset:16384
	ds_read_b128 v[192:195], v145 offset:17408
	ds_read_b128 v[196:199], v145 offset:18432
	ds_read_b128 v[200:203], v145 offset:19456
	ds_read_b128 v[204:207], v145 offset:20480
	ds_read_b128 v[208:211], v145 offset:21504
	ds_read_b128 v[212:215], v145 offset:22528
	ds_read_b128 v[216:219], v145 offset:23552
	global_load_lds_dwordx4 v[140:141], off
	s_add_i32 m0, s52, 0x2000
	s_add_u32 s52, s22, 0x40000
	v_lshl_add_u64 v[176:177], s[22:23], 0, v[130:131]
	s_addc_u32 s53, s23, 0
	s_add_i32 s54, s54, s30
	global_load_lds_dwordx4 v[176:177], off
	v_lshl_add_u64 v[178:179], s[52:53], 0, v[0:1]
	s_mov_b32 m0, s54
	v_lshl_add_u64 v[180:181], s[24:25], 0, v[132:133]
	global_load_lds_dwordx4 v[178:179], off
	v_lshl_add_u64 v[178:179], s[52:53], 0, v[130:131]
	s_add_i32 m0, s54, 0x2000
	s_nop 0
	global_load_lds_dwordx4 v[178:179], off
	v_lshl_add_u64 v[178:179], s[24:25], 0, v[134:135]
	s_mov_b32 m0, s31
	s_nop 0
	global_load_lds_dwordx4 v[178:179], off
	s_mov_b32 m0, s34
	s_nop 0
	global_load_lds_dwordx4 v[180:181], off
	s_cmp_eq_u32 s97, 0
	s_cbranch_scc1 .Lew10_a
	s_waitcnt vmcnt(24)
	s_branch .Lew10_b

; #define PG8_STAGE(bufoff, gbase, voff) do { _Pragma("unroll") for (int _i = 0; _i < 2; ++_i) \
;         __builtin_amdgcn_global_load_lds((const unsigned*)((const char*)(gbase) + (voff)[_i]), (PG8_LAS unsigned*)(lds + (bufoff) + ldsw + _i * 8192), 16, 0, 0); } while (0)
; #define PG8_LDA(dst, b, h) do { _Pragma("unroll") for (int m = 0; m < 4; ++m) _Pragma("unroll") for (int k = 0; k < 2; ++k) dst[m][k] = *(const PG8_LAS bf16x8*)(lds + PG8_SA(b, h) + aoff + m * 2048 + k * 1024); } while (0)
; #define PG8_LDB(dst, b, h) do { _Pragma("unroll") for (int n = 0; n < 2; ++n) _Pragma("unroll") for (int k = 0; k < 2; ++k) dst[n][k] = *(const PG8_LAS bf16x8*)(lds + PG8_SB(b, h) + boff + n * 2048 + k * 1024); } while (0)
; #define PG8_MMA(ai, bj, At, Bt) do { __builtin_amdgcn_s_setprio(1); _Pragma("unroll") for (int m = 0; m < 4; ++m) _Pragma("unroll") for (int n = 0; n < 2; ++n) _Pragma("unroll") for (int k = 0; k < 2; ++k) \
;         acc[ai][bj][m][n] = __builtin_amdgcn_mfma_f32_16x16x32_bf16(Bt[n][k], At[m][k], acc[ai][bj][m][n], 0, 0, 0); __builtin_amdgcn_s_setprio(0); } while (0)
; #define PG8_WAIT_V(n) asm volatile("s_waitcnt vmcnt(" #n ")" ::: "memory")
; #define PG8_WAIT_L(n) asm volatile("s_waitcnt lgkmcnt(" #n ")" ::: "memory")
; #define PG8_BAR __builtin_amdgcn_s_barrier()
; #define PG8_SCHED __builtin_amdgcn_sched_barrier(0)
; template <class Epi, class Sched, bool ALIGN_EPI = false, bool SP2 = false, bool GATHER = false>
; __device__ __forceinline__ void gemm_phase(PG8_LAS unsigned char* lds, const Gemm g, const Sched& S, const Epi& E, int tid_in, const int* rowsrc = nullptr, PG8_LAS int* idx_lds = nullptr) {
;     ...
;             PG8_WAIT_V(8); PG8_WAIT_L(0); PG8_BAR; PG8_MMA(1, 0, At, B0); PG8_MMA(1, 1, At, B1); PG8_BAR; PG8_SCHED;
;             PG8_LDB(B0, 1, 0); PG8_LDB(B1, 1, 1); PG8_SCHED; PG8_LDA(At, 1, 0); PG8_STAGE(PG8_SA(0, 1), a2 + hstepA, PG8_OS(1));
;             PG8_WAIT_V(8); PG8_WAIT_L(0); PG8_BAR; PG8_MMA(0, 0, At, B0); PG8_MMA(0, 1, At, B1); PG8_BAR; PG8_SCHED;
.Lew10_b:
	s_mov_b32 s97, 0
	s_waitcnt lgkmcnt(0)
	v_mfma_f32_16x16x32_bf16 v[62:65], v[148:151], v[188:191], v[62:65]
	v_mfma_f32_16x16x32_bf16 v[58:61], v[156:159], v[188:191], v[58:61]
	v_mfma_f32_16x16x32_bf16 v[54:57], v[148:151], v[196:199], v[54:57]
	s_barrier
	s_setprio 1
	s_waitcnt lgkmcnt(0)
	v_mfma_f32_16x16x32_bf16 v[46:49], v[156:159], v[196:199], v[46:49]
	v_mfma_f32_16x16x32_bf16 v[38:41], v[148:151], v[204:207], v[38:41]
	v_mfma_f32_16x16x32_bf16 v[30:33], v[156:159], v[204:207], v[30:33]
	v_mfma_f32_16x16x32_bf16 v[22:25], v[148:151], v[212:215], v[22:25]
	v_mfma_f32_16x16x32_bf16 v[14:17], v[156:159], v[212:215], v[14:17]
	v_mfma_f32_16x16x32_bf16 v[62:65], v[152:155], v[192:195], v[62:65]
	v_mfma_f32_16x16x32_bf16 v[58:61], v[160:163], v[192:195], v[58:61]
	v_mfma_f32_16x16x32_bf16 v[54:57], v[152:155], v[200:203], v[54:57]
	v_mfma_f32_16x16x32_bf16 v[46:49], v[160:163], v[200:203], v[46:49]
	v_mfma_f32_16x16x32_bf16 v[38:41], v[152:155], v[208:211], v[38:41]
	v_mfma_f32_16x16x32_bf16 v[30:33], v[160:163], v[208:211], v[30:33]
	v_mfma_f32_16x16x32_bf16 v[22:25], v[152:155], v[216:219], v[22:25]
	v_mfma_f32_16x16x32_bf16 v[14:17], v[160:163], v[216:219], v[14:17]
	s_setprio 0
	s_setprio 1
	v_mfma_f32_16x16x32_bf16 v[50:53], v[164:167], v[188:191], v[50:53]
	v_mfma_f32_16x16x32_bf16 v[42:45], v[172:175], v[188:191], v[42:45]
	v_mfma_f32_16x16x32_bf16 v[34:37], v[164:167], v[196:199], v[34:37]
	v_mfma_f32_16x16x32_bf16 v[26:29], v[172:175], v[196:199], v[26:29]
	v_mfma_f32_16x16x32_bf16 v[18:21], v[164:167], v[204:207], v[18:21]
	v_mfma_f32_16x16x32_bf16 v[10:13], v[172:175], v[204:207], v[10:13]
	v_mfma_f32_16x16x32_bf16 v[6:9], v[164:167], v[212:215], v[6:9]
	v_mfma_f32_16x16x32_bf16 v[2:5], v[172:175], v[212:215], v[2:5]
	v_mfma_f32_16x16x32_bf16 v[50:53], v[168:171], v[192:195], v[50:53]
	v_mfma_f32_16x16x32_bf16 v[42:45], v[184:187], v[192:195], v[42:45]
	v_mfma_f32_16x16x32_bf16 v[34:37], v[168:171], v[200:203], v[34:37]
	v_mfma_f32_16x16x32_bf16 v[26:29], v[184:187], v[200:203], v[26:29]
	v_mfma_f32_16x16x32_bf16 v[18:21], v[168:171], v[208:211], v[18:21]
	v_mfma_f32_16x16x32_bf16 v[10:13], v[184:187], v[208:211], v[10:13]
	v_mfma_f32_16x16x32_bf16 v[6:9], v[168:171], v[216:219], v[6:9]
	v_mfma_f32_16x16x32_bf16 v[2:5], v[184:187], v[216:219], v[2:5]
	s_setprio 0
	s_barrier
	s_add_i32 s52, 0, 0x18000
	s_add_i32 s53, 0, 0x1c000
	v_add_u32_e32 v160, s52, v143
	v_add_u32_e32 v182, s53, v143
	ds_read_b128 v[148:151], v160
	ds_read_b128 v[152:155], v160 offset:1024
	ds_read_b128 v[156:159], v160 offset:2048
	ds_read_b128 v[160:163], v160 offset:3072
	ds_read_b128 v[164:167], v182
	ds_read_b128 v[168:171], v182 offset:1024
	ds_read_b128 v[172:175], v182 offset:2048
	ds_read_b128 v[184:187], v182 offset:3072
	s_add_u32 s24, s24, 0x40000
	s_addc_u32 s25, s25, 0
	s_mov_b32 m0, s35
	v_lshl_add_u64 v[182:183], s[24:25], 0, v[134:135]
	ds_read_b128 v[188:191], v145 offset:32768
	ds_read_b128 v[192:195], v145 offset:33792
	ds_read_b128 v[196:199], v145 offset:34816
	ds_read_b128 v[200:203], v145 offset:35840
	ds_read_b128 v[204:207], v145 offset:36864
	ds_read_b128 v[208:211], v145 offset:37888
	ds_read_b128 v[212:215], v145 offset:38912
	ds_read_b128 v[216:219], v145 offset:39936
	global_load_lds_dwordx4 v[182:183], off
	v_lshl_add_u64 v[182:183], s[24:25], 0, v[132:133]
	s_mov_b32 m0, s36
	s_nop 0
	global_load_lds_dwordx4 v[182:183], off
	s_waitcnt vmcnt(8)
	s_waitcnt lgkmcnt(0)
	v_mfma_f32_16x16x32_bf16 v[126:129], v[148:151], v[188:191], v[126:129]
	v_mfma_f32_16x16x32_bf16 v[122:125], v[156:159], v[188:191], v[122:125]
	v_mfma_f32_16x16x32_bf16 v[118:121], v[148:151], v[196:199], v[118:121]
	s_barrier
	s_setprio 1
	s_waitcnt lgkmcnt(0)
	v_mfma_f32_16x16x32_bf16 v[110:113], v[156:159], v[196:199], v[110:113]
	v_mfma_f32_16x16x32_bf16 v[102:105], v[148:151], v[204:207], v[102:105]
	v_mfma_f32_16x16x32_bf16 v[94:97], v[156:159], v[204:207], v[94:97]
	v_mfma_f32_16x16x32_bf16 v[86:89], v[148:151], v[212:215], v[86:89]
	v_mfma_f32_16x16x32_bf16 v[78:81], v[156:159], v[212:215], v[78:81]
	v_mfma_f32_16x16x32_bf16 v[126:129], v[152:155], v[192:195], v[126:129]
	v_mfma_f32_16x16x32_bf16 v[122:125], v[160:163], v[192:195], v[122:125]
	v_mfma_f32_16x16x32_bf16 v[118:121], v[152:155], v[200:203], v[118:121]
	v_mfma_f32_16x16x32_bf16 v[110:113], v[160:163], v[200:203], v[110:113]
	v_mfma_f32_16x16x32_bf16 v[102:105], v[152:155], v[208:211], v[102:105]
	v_mfma_f32_16x16x32_bf16 v[94:97], v[160:163], v[208:211], v[94:97]
	v_mfma_f32_16x16x32_bf16 v[86:89], v[152:155], v[216:219], v[86:89]
	v_mfma_f32_16x16x32_bf16 v[78:81], v[160:163], v[216:219], v[78:81]
	s_setprio 0
	s_setprio 1
	v_mfma_f32_16x16x32_bf16 v[114:117], v[164:167], v[188:191], v[114:117]
	v_mfma_f32_16x16x32_bf16 v[106:109], v[172:175], v[188:191], v[106:109]
	v_mfma_f32_16x16x32_bf16 v[98:101], v[164:167], v[196:199], v[98:101]
	v_mfma_f32_16x16x32_bf16 v[90:93], v[172:175], v[196:199], v[90:93]
	v_mfma_f32_16x16x32_bf16 v[82:85], v[164:167], v[204:207], v[82:85]
	v_mfma_f32_16x16x32_bf16 v[74:77], v[172:175], v[204:207], v[74:77]
	v_mfma_f32_16x16x32_bf16 v[70:73], v[164:167], v[212:215], v[70:73]
	v_mfma_f32_16x16x32_bf16 v[66:69], v[172:175], v[212:215], v[66:69]
	v_mfma_f32_16x16x32_bf16 v[114:117], v[168:171], v[192:195], v[114:117]
	v_mfma_f32_16x16x32_bf16 v[106:109], v[184:187], v[192:195], v[106:109]
	v_mfma_f32_16x16x32_bf16 v[98:101], v[168:171], v[200:203], v[98:101]
	v_mfma_f32_16x16x32_bf16 v[90:93], v[184:187], v[200:203], v[90:93]
	v_mfma_f32_16x16x32_bf16 v[82:85], v[168:171], v[208:211], v[82:85]
	v_mfma_f32_16x16x32_bf16 v[74:77], v[184:187], v[208:211], v[74:77]
	v_mfma_f32_16x16x32_bf16 v[70:73], v[168:171], v[216:219], v[70:73]
	v_mfma_f32_16x16x32_bf16 v[66:69], v[184:187], v[216:219], v[66:69]
	s_setprio 0
	s_barrier
; #define PG8_STAGE(bufoff, gbase, voff) do { _Pragma("unroll") for (int _i = 0; _i < 2; ++_i) \
;         __builtin_amdgcn_global_load_lds((const unsigned*)((const char*)(gbase) + (voff)[_i]), (PG8_LAS unsigned*)(lds + (bufoff) + ldsw + _i * 8192), 16, 0, 0); } while (0)
; #define PG8_LDA(dst, b, h) do { _Pragma("unroll") for (int m = 0; m < 4; ++m) _Pragma("unroll") for (int k = 0; k < 2; ++k) dst[m][k] = *(const PG8_LAS bf16x8*)(lds + PG8_SA(b, h) + aoff + m * 2048 + k * 1024); } while (0)
; #define PG8_MMA(ai, bj, At, Bt) do { __builtin_amdgcn_s_setprio(1); _Pragma("unroll") for (int m = 0; m < 4; ++m) _Pragma("unroll") for (int n = 0; n < 2; ++n) _Pragma("unroll") for (int k = 0; k < 2; ++k) \
;         acc[ai][bj][m][n] = __builtin_amdgcn_mfma_f32_16x16x32_bf16(Bt[n][k], At[m][k], acc[ai][bj][m][n], 0, 0, 0); __builtin_amdgcn_s_setprio(0); } while (0)
; #define PG8_WAIT_V(n) asm volatile("s_waitcnt vmcnt(" #n ")" ::: "memory")
; #define PG8_WAIT_L(n) asm volatile("s_waitcnt lgkmcnt(" #n ")" ::: "memory")
; #define PG8_BAR __builtin_amdgcn_s_barrier()
; #define PG8_SCHED __builtin_amdgcn_sched_barrier(0)
; template <class Epi, class Sched, bool ALIGN_EPI = false, bool SP2 = false, bool GATHER = false>
; __device__ __forceinline__ void gemm_phase(PG8_LAS unsigned char* lds, const Gemm g, const Sched& S, const Epi& E, int tid_in, const int* rowsrc = nullptr, PG8_LAS int* idx_lds = nullptr) {
;     ...
;             PG8_LDA(At, 1, 1); PG8_STAGE(PG8_SB(1, 0), b3, voffB); PG8_STAGE(PG8_SB(1, 1), b3 + hstep, voffB); PG8_STAGE(PG8_SA(1, 0), a3, PG8_OS(0));
;             PG8_WAIT_V(8); PG8_WAIT_L(0); PG8_BAR; PG8_MMA(1, 0, At, B0); PG8_MMA(1, 1, At, B1); PG8_BAR; PG8_SCHED;
;     ...
;         if constexpr (ALIGN_EPI) { if (wr == 0) PG8_BAR; }
	s_add_i32 s24, s52, s30
	v_lshl_add_u64 v[140:141], v[140:141], 0, s[10:11]
	s_mov_b32 m0, s24
	ds_read_b128 v[188:191], v145 offset:49152
	ds_read_b128 v[192:195], v145 offset:50176
	ds_read_b128 v[196:199], v145 offset:51200
	ds_read_b128 v[200:203], v145 offset:52224
	ds_read_b128 v[204:207], v145 offset:53248
	ds_read_b128 v[208:211], v145 offset:54272
	ds_read_b128 v[212:215], v145 offset:55296
	ds_read_b128 v[216:219], v145 offset:56320
	global_load_lds_dwordx4 v[140:141], off
	s_add_i32 m0, s24, 0x2000
	s_add_u32 s22, s22, 0x40080
	v_lshl_add_u64 v[140:141], v[176:177], 0, s[10:11]
	s_addc_u32 s23, s23, 0
	s_add_i32 s24, s53, s30
	global_load_lds_dwordx4 v[140:141], off
	v_lshl_add_u64 v[140:141], s[22:23], 0, v[0:1]
	s_mov_b32 m0, s24
	s_nop 0
	global_load_lds_dwordx4 v[140:141], off
	v_lshl_add_u64 v[140:141], s[22:23], 0, v[130:131]
	s_add_i32 m0, s24, 0x2000
	s_nop 0
	global_load_lds_dwordx4 v[140:141], off
	v_lshl_add_u64 v[140:141], v[178:179], 0, s[10:11]
	s_mov_b32 m0, s38
	s_nop 0
	global_load_lds_dwordx4 v[140:141], off
	v_lshl_add_u64 v[140:141], v[180:181], 0, s[10:11]
	s_mov_b32 m0, s39
	s_nop 0
	global_load_lds_dwordx4 v[140:141], off
	s_waitcnt vmcnt(8)
	s_waitcnt lgkmcnt(0)
	v_mfma_f32_16x16x32_bf16 v[62:65], v[148:151], v[188:191], v[62:65]
	v_mfma_f32_16x16x32_bf16 v[58:61], v[156:159], v[188:191], v[58:61]
	v_mfma_f32_16x16x32_bf16 v[54:57], v[148:151], v[196:199], v[54:57]
	s_barrier
	s_setprio 1
	s_waitcnt lgkmcnt(0)
	v_mfma_f32_16x16x32_bf16 v[46:49], v[156:159], v[196:199], v[46:49]
	v_mfma_f32_16x16x32_bf16 v[38:41], v[148:151], v[204:207], v[38:41]
	v_mfma_f32_16x16x32_bf16 v[30:33], v[156:159], v[204:207], v[30:33]
	v_mfma_f32_16x16x32_bf16 v[22:25], v[148:151], v[212:215], v[22:25]
	v_mfma_f32_16x16x32_bf16 v[14:17], v[156:159], v[212:215], v[14:17]
	v_mfma_f32_16x16x32_bf16 v[62:65], v[152:155], v[192:195], v[62:65]
	v_mfma_f32_16x16x32_bf16 v[58:61], v[160:163], v[192:195], v[58:61]
	v_mfma_f32_16x16x32_bf16 v[54:57], v[152:155], v[200:203], v[54:57]
	v_mfma_f32_16x16x32_bf16 v[46:49], v[160:163], v[200:203], v[46:49]
	v_mfma_f32_16x16x32_bf16 v[38:41], v[152:155], v[208:211], v[38:41]
	v_mfma_f32_16x16x32_bf16 v[30:33], v[160:163], v[208:211], v[30:33]
	v_mfma_f32_16x16x32_bf16 v[22:25], v[152:155], v[216:219], v[22:25]
	v_mfma_f32_16x16x32_bf16 v[14:17], v[160:163], v[216:219], v[14:17]
	s_setprio 0
	s_setprio 1
	v_mfma_f32_16x16x32_bf16 v[50:53], v[164:167], v[188:191], v[50:53]
	v_mfma_f32_16x16x32_bf16 v[42:45], v[172:175], v[188:191], v[42:45]
	v_mfma_f32_16x16x32_bf16 v[34:37], v[164:167], v[196:199], v[34:37]
	v_mfma_f32_16x16x32_bf16 v[26:29], v[172:175], v[196:199], v[26:29]
	v_mfma_f32_16x16x32_bf16 v[18:21], v[164:167], v[204:207], v[18:21]
	v_mfma_f32_16x16x32_bf16 v[10:13], v[172:175], v[204:207], v[10:13]
	v_mfma_f32_16x16x32_bf16 v[6:9], v[164:167], v[212:215], v[6:9]
	v_mfma_f32_16x16x32_bf16 v[2:5], v[172:175], v[212:215], v[2:5]
	v_mfma_f32_16x16x32_bf16 v[50:53], v[168:171], v[192:195], v[50:53]
	v_mfma_f32_16x16x32_bf16 v[42:45], v[184:187], v[192:195], v[42:45]
	v_mfma_f32_16x16x32_bf16 v[34:37], v[168:171], v[200:203], v[34:37]
	v_mfma_f32_16x16x32_bf16 v[26:29], v[184:187], v[200:203], v[26:29]
	v_mfma_f32_16x16x32_bf16 v[18:21], v[168:171], v[208:211], v[18:21]
	v_mfma_f32_16x16x32_bf16 v[10:13], v[184:187], v[208:211], v[10:13]
	v_mfma_f32_16x16x32_bf16 v[6:9], v[168:171], v[216:219], v[6:9]
	v_mfma_f32_16x16x32_bf16 v[2:5], v[184:187], v[216:219], v[2:5]
	s_setprio 0
	s_barrier
	s_add_i32 s51, s51, 2
	s_add_u32 s20, s20, 0x100
	s_addc_u32 s21, s21, 0
	s_add_u32 s49, s49, 0x100
	s_addc_u32 s50, s50, 0
	s_cmp_gt_u32 s51, 13
	s_cbranch_scc0 .LBB0_1127
	s_mov_b32 s97, 1
	s_and_b64 vcc, exec, s[8:9]
	s_cbranch_vccz .LBB0_1130
	s_barrier

.LBB0_1215:
	s_mov_b32 s97, 0
	v_readlane_b32 s4, v251, 10
	v_readlane_b32 s5, v251, 11
	s_cmp_ge_i32 s2, s4
	s_cselect_b64 s[0:1], -1, 0
	s_cmp_lt_i32 s2, s5
	s_cselect_b64 s[4:5], -1, 0
	s_and_b64 s[4:5], s[0:1], s[4:5]
	s_mov_b64 s[0:1], -1
	s_and_b64 vcc, exec, s[4:5]
	s_cbranch_vccnz .LBB0_1217
	s_add_i32 s2, s44, 3
	s_mov_b64 s[0:1], 0

; #define PG8_STAGE(bufoff, gbase, voff) do { _Pragma("unroll") for (int _i = 0; _i < 2; ++_i) \
;         __builtin_amdgcn_global_load_lds((const unsigned*)((const char*)(gbase) + (voff)[_i]), (PG8_LAS unsigned*)(lds + (bufoff) + ldsw + _i * 8192), 16, 0, 0); } while (0)
; #define PG8_LDA(dst, b, h) do { _Pragma("unroll") for (int m = 0; m < 4; ++m) _Pragma("unroll") for (int k = 0; k < 2; ++k) dst[m][k] = *(const PG8_LAS bf16x8*)(lds + PG8_SA(b, h) + aoff + m * 2048 + k * 1024); } while (0)
; #define PG8_LDB(dst, b, h) do { _Pragma("unroll") for (int n = 0; n < 2; ++n) _Pragma("unroll") for (int k = 0; k < 2; ++k) dst[n][k] = *(const PG8_LAS bf16x8*)(lds + PG8_SB(b, h) + boff + n * 2048 + k * 1024); } while (0)
; #define PG8_SCHED __builtin_amdgcn_sched_barrier(0)
; template <class Epi, class Sched, bool ALIGN_EPI = false, bool SP2 = false, bool GATHER = false>
; __device__ __forceinline__ void gemm_phase(PG8_LAS unsigned char* lds, const Gemm g, const Sched& S, const Epi& E, int tid_in, const int* rowsrc = nullptr, PG8_LAS int* idx_lds = nullptr) {
;     ...
;         for (int t = 0; t < nt; t += 2) {
;             const bool last = (t == nt - 2);
;             if constexpr (GATHER) {
; #pragma unroll
;                 for (int h_ = 0; h_ < 2; ++h_) { gS[h_][0] = last ? gN[h_][0] : gA[h_][0]; gS[h_][1] = last ? gN[h_][1] : gA[h_][1]; } }
;             const char* a1 = cA + (size_t)(t + 1) * kstep;
;             const char* a2 = last ? nA : cA + (size_t)(t + 2) * kstep; const char* b2 = last ? nB : cB + (size_t)(t + 2) * kstep;
;             const char* a3 = a2 + kstep; const char* b3 = b2 + kstep;
;             if (last && has_next) S.a_ready(nxt);
;             if constexpr (SP2) {
;             PG8_LDB(B0, 0, 0); PG8_LDB(B1, 0, 1); PG8_SCHED; PG8_LDA(At, 0, 0); PG8_STAGE(PG8_SA(1, 1), a1 + hstepA, PG8_OA(1));
.LBB0_1227:
	s_add_u32 s26, s24, 0xfffc0080
	s_addc_u32 s27, s25, -1
	s_add_i32 s60, 0, 0x10000
	s_cmp_eq_u32 s59, 4
	s_cselect_b32 s29, s15, s27
	s_cselect_b32 s28, s55, s26
	v_add_u32_e32 v151, s60, v148
	s_cselect_b32 s27, s13, s58
	s_cselect_b32 s26, s56, s57
	s_add_i32 s62, 0, 0x14000
	ds_read_b128 v[140:143], v151
	ds_read_b128 v[152:155], v151 offset:1024
	ds_read_b128 v[156:159], v151 offset:2048
	ds_read_b128 v[160:163], v151 offset:3072
	v_add_u32_e32 v151, s62, v148
	ds_read_b128 v[164:167], v151
	ds_read_b128 v[168:171], v151 offset:1024
	ds_read_b128 v[172:175], v151 offset:2048
	ds_read_b128 v[184:187], v151 offset:3072
	v_lshl_add_u64 v[176:177], s[24:25], 0, v[136:137]
	s_add_i32 m0, s17, 0xc000
	ds_read_b128 v[188:191], v150
	ds_read_b128 v[192:195], v150 offset:1024
	ds_read_b128 v[196:199], v150 offset:2048
	ds_read_b128 v[200:203], v150 offset:3072
	ds_read_b128 v[204:207], v150 offset:4096
	ds_read_b128 v[208:211], v150 offset:5120
	ds_read_b128 v[212:215], v150 offset:6144
	ds_read_b128 v[216:219], v150 offset:7168
	global_load_lds_dwordx4 v[176:177], off
	v_lshl_add_u64 v[176:177], s[24:25], 0, v[138:139]
	s_add_i32 m0, s17, 0xe000
	s_nop 0
	global_load_lds_dwordx4 v[176:177], off
	s_cmp_eq_u32 s97, 0
	s_cbranch_scc1 .Lew11_a
	s_waitcnt vmcnt(24)
	s_branch .Lew11_b

; #define PG8_STAGE(bufoff, gbase, voff) do { _Pragma("unroll") for (int _i = 0; _i < 2; ++_i) \
;         __builtin_amdgcn_global_load_lds((const unsigned*)((const char*)(gbase) + (voff)[_i]), (PG8_LAS unsigned*)(lds + (bufoff) + ldsw + _i * 8192), 16, 0, 0); } while (0)
; #define PG8_LDA(dst, b, h) do { _Pragma("unroll") for (int m = 0; m < 4; ++m) _Pragma("unroll") for (int k = 0; k < 2; ++k) dst[m][k] = *(const PG8_LAS bf16x8*)(lds + PG8_SA(b, h) + aoff + m * 2048 + k * 1024); } while (0)
; #define PG8_LDB(dst, b, h) do { _Pragma("unroll") for (int n = 0; n < 2; ++n) _Pragma("unroll") for (int k = 0; k < 2; ++k) dst[n][k] = *(const PG8_LAS bf16x8*)(lds + PG8_SB(b, h) + boff + n * 2048 + k * 1024); } while (0)
; #define PG8_MMA(ai, bj, At, Bt) do { __builtin_amdgcn_s_setprio(1); _Pragma("unroll") for (int m = 0; m < 4; ++m) _Pragma("unroll") for (int n = 0; n < 2; ++n) _Pragma("unroll") for (int k = 0; k < 2; ++k) \
;         acc[ai][bj][m][n] = __builtin_amdgcn_mfma_f32_16x16x32_bf16(Bt[n][k], At[m][k], acc[ai][bj][m][n], 0, 0, 0); __builtin_amdgcn_s_setprio(0); } while (0)
; #define PG8_WAIT_V(n) asm volatile("s_waitcnt vmcnt(" #n ")" ::: "memory")
; #define PG8_WAIT_L(n) asm volatile("s_waitcnt lgkmcnt(" #n ")" ::: "memory")
; #define PG8_BAR __builtin_amdgcn_s_barrier()
; #define PG8_SCHED __builtin_amdgcn_sched_barrier(0)
; template <class Epi, class Sched, bool ALIGN_EPI = false, bool SP2 = false, bool GATHER = false>
; __device__ __forceinline__ void gemm_phase(PG8_LAS unsigned char* lds, const Gemm g, const Sched& S, const Epi& E, int tid_in, const int* rowsrc = nullptr, PG8_LAS int* idx_lds = nullptr) {
;     ...
;             PG8_LDB(B0, 0, 0); PG8_LDB(B1, 0, 1); PG8_SCHED; PG8_LDA(At, 0, 0); PG8_STAGE(PG8_SA(1, 1), a1 + hstepA, PG8_OA(1));
;             PG8_WAIT_V(8); PG8_WAIT_L(0); PG8_BAR; PG8_MMA(0, 0, At, B0); PG8_MMA(0, 1, At, B1); PG8_BAR; PG8_SCHED;
;             PG8_LDA(At, 0, 1); PG8_STAGE(PG8_SB(0, 0), b2, voffB); PG8_STAGE(PG8_SB(0, 1), b2 + hstep, voffB); PG8_STAGE(PG8_SA(0, 0), a2, PG8_OS(0));
.Lew11_b:
	s_waitcnt lgkmcnt(0)
	v_mfma_f32_16x16x32_bf16 v[126:129], v[140:143], v[188:191], v[126:129]
	v_mfma_f32_16x16x32_bf16 v[122:125], v[156:159], v[188:191], v[122:125]
	v_mfma_f32_16x16x32_bf16 v[118:121], v[140:143], v[196:199], v[118:121]
	s_barrier
	s_setprio 1
	s_waitcnt lgkmcnt(0)
	v_mfma_f32_16x16x32_bf16 v[110:113], v[156:159], v[196:199], v[110:113]
	v_mfma_f32_16x16x32_bf16 v[102:105], v[140:143], v[204:207], v[102:105]
	v_mfma_f32_16x16x32_bf16 v[94:97], v[156:159], v[204:207], v[94:97]
	v_mfma_f32_16x16x32_bf16 v[86:89], v[140:143], v[212:215], v[86:89]
	v_mfma_f32_16x16x32_bf16 v[78:81], v[156:159], v[212:215], v[78:81]
	v_mfma_f32_16x16x32_bf16 v[126:129], v[152:155], v[192:195], v[126:129]
	v_mfma_f32_16x16x32_bf16 v[122:125], v[160:163], v[192:195], v[122:125]
	v_mfma_f32_16x16x32_bf16 v[118:121], v[152:155], v[200:203], v[118:121]
	v_mfma_f32_16x16x32_bf16 v[110:113], v[160:163], v[200:203], v[110:113]
	v_mfma_f32_16x16x32_bf16 v[102:105], v[152:155], v[208:211], v[102:105]
	v_mfma_f32_16x16x32_bf16 v[94:97], v[160:163], v[208:211], v[94:97]
	v_mfma_f32_16x16x32_bf16 v[86:89], v[152:155], v[216:219], v[86:89]
	v_mfma_f32_16x16x32_bf16 v[78:81], v[160:163], v[216:219], v[78:81]
	s_setprio 0
	s_setprio 1
	v_mfma_f32_16x16x32_bf16 v[114:117], v[164:167], v[188:191], v[114:117]
	v_mfma_f32_16x16x32_bf16 v[106:109], v[172:175], v[188:191], v[106:109]
	v_mfma_f32_16x16x32_bf16 v[98:101], v[164:167], v[196:199], v[98:101]
	v_mfma_f32_16x16x32_bf16 v[90:93], v[172:175], v[196:199], v[90:93]
	v_mfma_f32_16x16x32_bf16 v[82:85], v[164:167], v[204:207], v[82:85]
	v_mfma_f32_16x16x32_bf16 v[74:77], v[172:175], v[204:207], v[74:77]
	v_mfma_f32_16x16x32_bf16 v[70:73], v[164:167], v[212:215], v[70:73]
	v_mfma_f32_16x16x32_bf16 v[66:69], v[172:175], v[212:215], v[66:69]
	v_mfma_f32_16x16x32_bf16 v[114:117], v[168:171], v[192:195], v[114:117]
	v_mfma_f32_16x16x32_bf16 v[106:109], v[184:187], v[192:195], v[106:109]
	v_mfma_f32_16x16x32_bf16 v[98:101], v[168:171], v[200:203], v[98:101]
	v_mfma_f32_16x16x32_bf16 v[90:93], v[184:187], v[200:203], v[90:93]
	v_mfma_f32_16x16x32_bf16 v[82:85], v[168:171], v[208:211], v[82:85]
	v_mfma_f32_16x16x32_bf16 v[74:77], v[184:187], v[208:211], v[74:77]
	v_mfma_f32_16x16x32_bf16 v[70:73], v[168:171], v[216:219], v[70:73]
	v_mfma_f32_16x16x32_bf16 v[66:69], v[184:187], v[216:219], v[66:69]
	s_setprio 0
	s_barrier
	s_add_i32 s60, s60, s49
	v_lshl_add_u64 v[176:177], s[26:27], 0, v[0:1]
	s_mov_b32 m0, s60
	ds_read_b128 v[188:191], v150 offset:16384
	ds_read_b128 v[192:195], v150 offset:17408
	ds_read_b128 v[196:199], v150 offset:18432
	ds_read_b128 v[200:203], v150 offset:19456
	ds_read_b128 v[204:207], v150 offset:20480
	ds_read_b128 v[208:211], v150 offset:21504
	ds_read_b128 v[212:215], v150 offset:22528
	ds_read_b128 v[216:219], v150 offset:23552
	global_load_lds_dwordx4 v[176:177], off
	s_add_i32 m0, s60, 0x2000
	s_add_u32 s60, s26, 0x20000
	v_lshl_add_u64 v[178:179], s[26:27], 0, v[130:131]
	s_addc_u32 s61, s27, 0
	s_add_i32 s62, s62, s49
	global_load_lds_dwordx4 v[178:179], off
	v_lshl_add_u64 v[180:181], s[60:61], 0, v[0:1]
	s_mov_b32 m0, s62
	v_lshl_add_u64 v[182:183], s[28:29], 0, v[132:133]
	global_load_lds_dwordx4 v[180:181], off
	v_lshl_add_u64 v[180:181], s[60:61], 0, v[130:131]
	s_add_i32 m0, s62, 0x2000
	s_nop 0
	global_load_lds_dwordx4 v[180:181], off
	v_lshl_add_u64 v[180:181], s[28:29], 0, v[134:135]
	s_mov_b32 m0, s17
	s_nop 0
	global_load_lds_dwordx4 v[180:181], off
	s_mov_b32 m0, s19
	s_nop 0
	global_load_lds_dwordx4 v[182:183], off
	s_cmp_eq_u32 s97, 0
	s_cbranch_scc1 .Lew12_a
	s_waitcnt vmcnt(24)
	s_branch .Lew12_b

; #define PG8_STAGE(bufoff, gbase, voff) do { _Pragma("unroll") for (int _i = 0; _i < 2; ++_i) \
;         __builtin_amdgcn_global_load_lds((const unsigned*)((const char*)(gbase) + (voff)[_i]), (PG8_LAS unsigned*)(lds + (bufoff) + ldsw + _i * 8192), 16, 0, 0); } while (0)
; #define PG8_LDA(dst, b, h) do { _Pragma("unroll") for (int m = 0; m < 4; ++m) _Pragma("unroll") for (int k = 0; k < 2; ++k) dst[m][k] = *(const PG8_LAS bf16x8*)(lds + PG8_SA(b, h) + aoff + m * 2048 + k * 1024); } while (0)
; #define PG8_LDB(dst, b, h) do { _Pragma("unroll") for (int n = 0; n < 2; ++n) _Pragma("unroll") for (int k = 0; k < 2; ++k) dst[n][k] = *(const PG8_LAS bf16x8*)(lds + PG8_SB(b, h) + boff + n * 2048 + k * 1024); } while (0)
; #define PG8_MMA(ai, bj, At, Bt) do { __builtin_amdgcn_s_setprio(1); _Pragma("unroll") for (int m = 0; m < 4; ++m) _Pragma("unroll") for (int n = 0; n < 2; ++n) _Pragma("unroll") for (int k = 0; k < 2; ++k) \
;         acc[ai][bj][m][n] = __builtin_amdgcn_mfma_f32_16x16x32_bf16(Bt[n][k], At[m][k], acc[ai][bj][m][n], 0, 0, 0); __builtin_amdgcn_s_setprio(0); } while (0)
; #define PG8_WAIT_V(n) asm volatile("s_waitcnt vmcnt(" #n ")" ::: "memory")
; #define PG8_WAIT_L(n) asm volatile("s_waitcnt lgkmcnt(" #n ")" ::: "memory")
; #define PG8_BAR __builtin_amdgcn_s_barrier()
; #define PG8_SCHED __builtin_amdgcn_sched_barrier(0)
; template <class Epi, class Sched, bool ALIGN_EPI = false, bool SP2 = false, bool GATHER = false>
; __device__ __forceinline__ void gemm_phase(PG8_LAS unsigned char* lds, const Gemm g, const Sched& S, const Epi& E, int tid_in, const int* rowsrc = nullptr, PG8_LAS int* idx_lds = nullptr) {
;     ...
;             PG8_WAIT_V(8); PG8_WAIT_L(0); PG8_BAR; PG8_MMA(1, 0, At, B0); PG8_MMA(1, 1, At, B1); PG8_BAR; PG8_SCHED;
;             PG8_LDB(B0, 1, 0); PG8_LDB(B1, 1, 1); PG8_SCHED; PG8_LDA(At, 1, 0); PG8_STAGE(PG8_SA(0, 1), a2 + hstepA, PG8_OS(1));
;             PG8_WAIT_V(8); PG8_WAIT_L(0); PG8_BAR; PG8_MMA(0, 0, At, B0); PG8_MMA(0, 1, At, B1); PG8_BAR; PG8_SCHED;
.Lew12_b:
	s_mov_b32 s97, 0
	s_waitcnt lgkmcnt(0)
	v_mfma_f32_16x16x32_bf16 v[62:65], v[140:143], v[188:191], v[62:65]
	v_mfma_f32_16x16x32_bf16 v[58:61], v[156:159], v[188:191], v[58:61]
	v_mfma_f32_16x16x32_bf16 v[54:57], v[140:143], v[196:199], v[54:57]
	s_barrier
	s_setprio 1
	s_waitcnt lgkmcnt(0)
	v_mfma_f32_16x16x32_bf16 v[46:49], v[156:159], v[196:199], v[46:49]
	v_mfma_f32_16x16x32_bf16 v[38:41], v[140:143], v[204:207], v[38:41]
	v_mfma_f32_16x16x32_bf16 v[30:33], v[156:159], v[204:207], v[30:33]
	v_mfma_f32_16x16x32_bf16 v[22:25], v[140:143], v[212:215], v[22:25]
	v_mfma_f32_16x16x32_bf16 v[14:17], v[156:159], v[212:215], v[14:17]
	v_mfma_f32_16x16x32_bf16 v[62:65], v[152:155], v[192:195], v[62:65]
	v_mfma_f32_16x16x32_bf16 v[58:61], v[160:163], v[192:195], v[58:61]
	v_mfma_f32_16x16x32_bf16 v[54:57], v[152:155], v[200:203], v[54:57]
	v_mfma_f32_16x16x32_bf16 v[46:49], v[160:163], v[200:203], v[46:49]
	v_mfma_f32_16x16x32_bf16 v[38:41], v[152:155], v[208:211], v[38:41]
	v_mfma_f32_16x16x32_bf16 v[30:33], v[160:163], v[208:211], v[30:33]
	v_mfma_f32_16x16x32_bf16 v[22:25], v[152:155], v[216:219], v[22:25]
	v_mfma_f32_16x16x32_bf16 v[14:17], v[160:163], v[216:219], v[14:17]
	s_setprio 0
	s_setprio 1
	v_mfma_f32_16x16x32_bf16 v[50:53], v[164:167], v[188:191], v[50:53]
	v_mfma_f32_16x16x32_bf16 v[42:45], v[172:175], v[188:191], v[42:45]
	v_mfma_f32_16x16x32_bf16 v[34:37], v[164:167], v[196:199], v[34:37]
	v_mfma_f32_16x16x32_bf16 v[26:29], v[172:175], v[196:199], v[26:29]
	v_mfma_f32_16x16x32_bf16 v[18:21], v[164:167], v[204:207], v[18:21]
	v_mfma_f32_16x16x32_bf16 v[10:13], v[172:175], v[204:207], v[10:13]
	v_mfma_f32_16x16x32_bf16 v[6:9], v[164:167], v[212:215], v[6:9]
	v_mfma_f32_16x16x32_bf16 v[2:5], v[172:175], v[212:215], v[2:5]
	v_mfma_f32_16x16x32_bf16 v[50:53], v[168:171], v[192:195], v[50:53]
	v_mfma_f32_16x16x32_bf16 v[42:45], v[184:187], v[192:195], v[42:45]
	v_mfma_f32_16x16x32_bf16 v[34:37], v[168:171], v[200:203], v[34:37]
	v_mfma_f32_16x16x32_bf16 v[26:29], v[184:187], v[200:203], v[26:29]
	v_mfma_f32_16x16x32_bf16 v[18:21], v[168:171], v[208:211], v[18:21]
	v_mfma_f32_16x16x32_bf16 v[10:13], v[184:187], v[208:211], v[10:13]
	v_mfma_f32_16x16x32_bf16 v[6:9], v[168:171], v[216:219], v[6:9]
	v_mfma_f32_16x16x32_bf16 v[2:5], v[184:187], v[216:219], v[2:5]
	s_setprio 0
	s_barrier
	s_add_i32 s60, 0, 0x18000
	v_add_u32_e32 v151, s60, v148
	s_add_i32 s61, 0, 0x1c000
	ds_read_b128 v[140:143], v151
	ds_read_b128 v[152:155], v151 offset:1024
	ds_read_b128 v[156:159], v151 offset:2048
	ds_read_b128 v[160:163], v151 offset:3072
	v_add_u32_e32 v151, s61, v148
	ds_read_b128 v[164:167], v151
	ds_read_b128 v[168:171], v151 offset:1024
	ds_read_b128 v[172:175], v151 offset:2048
	ds_read_b128 v[184:187], v151 offset:3072
	s_add_u32 s28, s28, 0x40000
	s_addc_u32 s29, s29, 0
	s_mov_b32 m0, s50
	v_lshl_add_u64 v[220:221], s[28:29], 0, v[134:135]
	ds_read_b128 v[188:191], v150 offset:32768
	ds_read_b128 v[192:195], v150 offset:33792
	ds_read_b128 v[196:199], v150 offset:34816
	ds_read_b128 v[200:203], v150 offset:35840
	ds_read_b128 v[204:207], v150 offset:36864
	ds_read_b128 v[208:211], v150 offset:37888
	ds_read_b128 v[212:215], v150 offset:38912
	ds_read_b128 v[216:219], v150 offset:39936
	global_load_lds_dwordx4 v[220:221], off
	v_lshl_add_u64 v[220:221], s[28:29], 0, v[132:133]
	s_mov_b32 m0, s51
	s_nop 0
	global_load_lds_dwordx4 v[220:221], off
	s_waitcnt vmcnt(8)
	s_waitcnt lgkmcnt(0)
	v_mfma_f32_16x16x32_bf16 v[126:129], v[140:143], v[188:191], v[126:129]
	v_mfma_f32_16x16x32_bf16 v[122:125], v[156:159], v[188:191], v[122:125]
	v_mfma_f32_16x16x32_bf16 v[118:121], v[140:143], v[196:199], v[118:121]
	s_barrier
	s_setprio 1
	s_waitcnt lgkmcnt(0)
	v_mfma_f32_16x16x32_bf16 v[110:113], v[156:159], v[196:199], v[110:113]
	v_mfma_f32_16x16x32_bf16 v[102:105], v[140:143], v[204:207], v[102:105]
	v_mfma_f32_16x16x32_bf16 v[94:97], v[156:159], v[204:207], v[94:97]
	v_mfma_f32_16x16x32_bf16 v[86:89], v[140:143], v[212:215], v[86:89]
	v_mfma_f32_16x16x32_bf16 v[78:81], v[156:159], v[212:215], v[78:81]
	v_mfma_f32_16x16x32_bf16 v[126:129], v[152:155], v[192:195], v[126:129]
	v_mfma_f32_16x16x32_bf16 v[122:125], v[160:163], v[192:195], v[122:125]
	v_mfma_f32_16x16x32_bf16 v[118:121], v[152:155], v[200:203], v[118:121]
	v_mfma_f32_16x16x32_bf16 v[110:113], v[160:163], v[200:203], v[110:113]
	v_mfma_f32_16x16x32_bf16 v[102:105], v[152:155], v[208:211], v[102:105]
	v_mfma_f32_16x16x32_bf16 v[94:97], v[160:163], v[208:211], v[94:97]
	v_mfma_f32_16x16x32_bf16 v[86:89], v[152:155], v[216:219], v[86:89]
	v_mfma_f32_16x16x32_bf16 v[78:81], v[160:163], v[216:219], v[78:81]
	s_setprio 0
	s_setprio 1
	v_mfma_f32_16x16x32_bf16 v[114:117], v[164:167], v[188:191], v[114:117]
	v_mfma_f32_16x16x32_bf16 v[106:109], v[172:175], v[188:191], v[106:109]
	v_mfma_f32_16x16x32_bf16 v[98:101], v[164:167], v[196:199], v[98:101]
	v_mfma_f32_16x16x32_bf16 v[90:93], v[172:175], v[196:199], v[90:93]
	v_mfma_f32_16x16x32_bf16 v[82:85], v[164:167], v[204:207], v[82:85]
	v_mfma_f32_16x16x32_bf16 v[74:77], v[172:175], v[204:207], v[74:77]
	v_mfma_f32_16x16x32_bf16 v[70:73], v[164:167], v[212:215], v[70:73]
	v_mfma_f32_16x16x32_bf16 v[66:69], v[172:175], v[212:215], v[66:69]
	v_mfma_f32_16x16x32_bf16 v[114:117], v[168:171], v[192:195], v[114:117]
	v_mfma_f32_16x16x32_bf16 v[106:109], v[184:187], v[192:195], v[106:109]
	v_mfma_f32_16x16x32_bf16 v[98:101], v[168:171], v[200:203], v[98:101]
	v_mfma_f32_16x16x32_bf16 v[90:93], v[184:187], v[200:203], v[90:93]
	v_mfma_f32_16x16x32_bf16 v[82:85], v[168:171], v[208:211], v[82:85]
	v_mfma_f32_16x16x32_bf16 v[74:77], v[184:187], v[208:211], v[74:77]
	v_mfma_f32_16x16x32_bf16 v[70:73], v[168:171], v[216:219], v[70:73]
	v_mfma_f32_16x16x32_bf16 v[66:69], v[184:187], v[216:219], v[66:69]
	s_setprio 0
	s_barrier
; #define PG8_STAGE(bufoff, gbase, voff) do { _Pragma("unroll") for (int _i = 0; _i < 2; ++_i) \
;         __builtin_amdgcn_global_load_lds((const unsigned*)((const char*)(gbase) + (voff)[_i]), (PG8_LAS unsigned*)(lds + (bufoff) + ldsw + _i * 8192), 16, 0, 0); } while (0)
; #define PG8_LDA(dst, b, h) do { _Pragma("unroll") for (int m = 0; m < 4; ++m) _Pragma("unroll") for (int k = 0; k < 2; ++k) dst[m][k] = *(const PG8_LAS bf16x8*)(lds + PG8_SA(b, h) + aoff + m * 2048 + k * 1024); } while (0)
; #define PG8_MMA(ai, bj, At, Bt) do { __builtin_amdgcn_s_setprio(1); _Pragma("unroll") for (int m = 0; m < 4; ++m) _Pragma("unroll") for (int n = 0; n < 2; ++n) _Pragma("unroll") for (int k = 0; k < 2; ++k) \
;         acc[ai][bj][m][n] = __builtin_amdgcn_mfma_f32_16x16x32_bf16(Bt[n][k], At[m][k], acc[ai][bj][m][n], 0, 0, 0); __builtin_amdgcn_s_setprio(0); } while (0)
; #define PG8_WAIT_V(n) asm volatile("s_waitcnt vmcnt(" #n ")" ::: "memory")
; #define PG8_WAIT_L(n) asm volatile("s_waitcnt lgkmcnt(" #n ")" ::: "memory")
; #define PG8_BAR __builtin_amdgcn_s_barrier()
; #define PG8_SCHED __builtin_amdgcn_sched_barrier(0)
; template <class Epi, class Sched, bool ALIGN_EPI = false, bool SP2 = false, bool GATHER = false>
; __device__ __forceinline__ void gemm_phase(PG8_LAS unsigned char* lds, const Gemm g, const Sched& S, const Epi& E, int tid_in, const int* rowsrc = nullptr, PG8_LAS int* idx_lds = nullptr) {
;     ...
;             PG8_LDA(At, 1, 1); PG8_STAGE(PG8_SB(1, 0), b3, voffB); PG8_STAGE(PG8_SB(1, 1), b3 + hstep, voffB); PG8_STAGE(PG8_SA(1, 0), a3, PG8_OS(0));
;             PG8_WAIT_V(8); PG8_WAIT_L(0); PG8_BAR; PG8_MMA(1, 0, At, B0); PG8_MMA(1, 1, At, B1); PG8_BAR; PG8_SCHED;
;     ...
;         if constexpr (ALIGN_EPI) { if (wr == 0) PG8_BAR; }
	s_add_i32 s28, s60, s49
	v_lshl_add_u64 v[176:177], v[176:177], 0, s[10:11]
	s_mov_b32 m0, s28
	ds_read_b128 v[188:191], v150 offset:49152
	ds_read_b128 v[192:195], v150 offset:50176
	ds_read_b128 v[196:199], v150 offset:51200
	ds_read_b128 v[200:203], v150 offset:52224
	ds_read_b128 v[204:207], v150 offset:53248
	ds_read_b128 v[208:211], v150 offset:54272
	ds_read_b128 v[212:215], v150 offset:55296
	ds_read_b128 v[216:219], v150 offset:56320
	global_load_lds_dwordx4 v[176:177], off
	s_add_i32 m0, s28, 0x2000
	s_add_u32 s26, s26, 0x20080
	v_lshl_add_u64 v[176:177], v[178:179], 0, s[10:11]
	s_addc_u32 s27, s27, 0
	s_add_i32 s28, s61, s49
	global_load_lds_dwordx4 v[176:177], off
	v_lshl_add_u64 v[176:177], s[26:27], 0, v[0:1]
	s_mov_b32 m0, s28
	s_nop 0
	global_load_lds_dwordx4 v[176:177], off
	v_lshl_add_u64 v[176:177], s[26:27], 0, v[130:131]
	s_add_i32 m0, s28, 0x2000
	s_nop 0
	global_load_lds_dwordx4 v[176:177], off
	v_lshl_add_u64 v[176:177], v[180:181], 0, s[10:11]
	s_mov_b32 m0, s52
	s_nop 0
	global_load_lds_dwordx4 v[176:177], off
	v_lshl_add_u64 v[176:177], v[182:183], 0, s[10:11]
	s_mov_b32 m0, s53
	s_nop 0
	global_load_lds_dwordx4 v[176:177], off
	s_waitcnt vmcnt(8)
	s_waitcnt lgkmcnt(0)
	v_mfma_f32_16x16x32_bf16 v[62:65], v[140:143], v[188:191], v[62:65]
	v_mfma_f32_16x16x32_bf16 v[58:61], v[156:159], v[188:191], v[58:61]
	v_mfma_f32_16x16x32_bf16 v[54:57], v[140:143], v[196:199], v[54:57]
	s_barrier
	s_setprio 1
	s_waitcnt lgkmcnt(0)
	v_mfma_f32_16x16x32_bf16 v[46:49], v[156:159], v[196:199], v[46:49]
	v_mfma_f32_16x16x32_bf16 v[38:41], v[140:143], v[204:207], v[38:41]
	v_mfma_f32_16x16x32_bf16 v[30:33], v[156:159], v[204:207], v[30:33]
	v_mfma_f32_16x16x32_bf16 v[22:25], v[140:143], v[212:215], v[22:25]
	v_mfma_f32_16x16x32_bf16 v[14:17], v[156:159], v[212:215], v[14:17]
	v_mfma_f32_16x16x32_bf16 v[62:65], v[152:155], v[192:195], v[62:65]
	v_mfma_f32_16x16x32_bf16 v[58:61], v[160:163], v[192:195], v[58:61]
	v_mfma_f32_16x16x32_bf16 v[54:57], v[152:155], v[200:203], v[54:57]
	v_mfma_f32_16x16x32_bf16 v[46:49], v[160:163], v[200:203], v[46:49]
	v_mfma_f32_16x16x32_bf16 v[38:41], v[152:155], v[208:211], v[38:41]
	v_mfma_f32_16x16x32_bf16 v[30:33], v[160:163], v[208:211], v[30:33]
	v_mfma_f32_16x16x32_bf16 v[22:25], v[152:155], v[216:219], v[22:25]
	v_mfma_f32_16x16x32_bf16 v[14:17], v[160:163], v[216:219], v[14:17]
	s_setprio 0
	s_setprio 1
	v_mfma_f32_16x16x32_bf16 v[50:53], v[164:167], v[188:191], v[50:53]
	v_mfma_f32_16x16x32_bf16 v[42:45], v[172:175], v[188:191], v[42:45]
	v_mfma_f32_16x16x32_bf16 v[34:37], v[164:167], v[196:199], v[34:37]
	v_mfma_f32_16x16x32_bf16 v[26:29], v[172:175], v[196:199], v[26:29]
	v_mfma_f32_16x16x32_bf16 v[18:21], v[164:167], v[204:207], v[18:21]
	v_mfma_f32_16x16x32_bf16 v[10:13], v[172:175], v[204:207], v[10:13]
	v_mfma_f32_16x16x32_bf16 v[6:9], v[164:167], v[212:215], v[6:9]
	v_mfma_f32_16x16x32_bf16 v[2:5], v[172:175], v[212:215], v[2:5]
	v_mfma_f32_16x16x32_bf16 v[50:53], v[168:171], v[192:195], v[50:53]
	v_mfma_f32_16x16x32_bf16 v[42:45], v[184:187], v[192:195], v[42:45]
	v_mfma_f32_16x16x32_bf16 v[34:37], v[168:171], v[200:203], v[34:37]
	v_mfma_f32_16x16x32_bf16 v[26:29], v[184:187], v[200:203], v[26:29]
	v_mfma_f32_16x16x32_bf16 v[18:21], v[168:171], v[208:211], v[18:21]
	v_mfma_f32_16x16x32_bf16 v[10:13], v[184:187], v[208:211], v[10:13]
	v_mfma_f32_16x16x32_bf16 v[6:9], v[168:171], v[216:219], v[6:9]
	v_mfma_f32_16x16x32_bf16 v[2:5], v[184:187], v[216:219], v[2:5]
	s_setprio 0
	s_barrier
	s_add_i32 s59, s59, 2
	s_add_u32 s24, s24, 0x100
	s_addc_u32 s25, s25, 0
	s_add_u32 s57, s57, 0x100
	s_addc_u32 s58, s58, 0
	s_cmp_gt_u32 s59, 5
	s_cbranch_scc0 .LBB0_1227
	s_mov_b32 s97, 1
	s_and_b64 vcc, exec, s[8:9]
	s_cbranch_vccz .LBB0_1230
	s_barrier

; #define PG8_WAIT_V(n) asm volatile("s_waitcnt vmcnt(" #n ")" ::: "memory")
; #define PG8_BAR __builtin_amdgcn_s_barrier()
; template <class Epi, class Sched, bool ALIGN_EPI = false, bool SP2 = false, bool GATHER = false>
; __device__ __forceinline__ void gemm_phase(PG8_LAS unsigned char* lds, const Gemm g, const Sched& S, const Epi& E, int tid_in, const int* rowsrc = nullptr, PG8_LAS int* idx_lds = nullptr) {
;     ...
;     PG8_WAIT_V(0);
;     if constexpr (!ALIGN_EPI) { if (wr == 0) PG8_BAR; }
;     PG8_BAR;
; __global__ void __launch_bounds__(NTHREADS, 2) fwd_kernel(Args args) {
;     ...
;                        { pg8::Gemm g{(const bf16*)(F.ws + R_DOWN) + 512, (const bf16*)(wb + MLA_WUKV), MROWS, 2048, 256, 1024}; pg8::StaticOrder S;
;                          const int r1_ = ((rows_out / 256) * 6) % F.G; S.init(MROWS, 2048, F.G, (F.G % 8 == 0 && r1_ % 8 == 0) ? ((int)blockIdx.x + F.G - r1_) % F.G : (int)blockIdx.x);
.LBB0_1234:
	s_and_b32 s0, s43, 7
	s_cmp_lg_u32 s0, 0
	s_mov_b32 s45, s63
	s_waitcnt vmcnt(0)
	s_barrier
	s_mov_b32 s97, 0
	s_cbranch_scc1 .LBB0_1236
	s_abs_i32 s0, s43
	v_cvt_f32_u32_e32 v0, s0
	s_sub_i32 s4, 0, s0
	s_add_i32 s1, s43, s63
	v_rcp_iflag_f32_e32 v0, v0
	s_nop 0
	v_mul_f32_e32 v0, 0x4f7ffffe, v0
	v_cvt_u32_f32_e32 v0, v0
	s_nop 0
	v_readfirstlane_b32 s5, v0
	s_mul_i32 s4, s4, s5
	s_mul_hi_u32 s4, s5, s4
	s_add_i32 s5, s5, s4
	s_mul_hi_u32 s4, s2, s5
	s_mul_i32 s4, s4, s0
	s_sub_i32 s2, s2, s4
	s_sub_i32 s4, s2, s0
	s_cmp_ge_u32 s2, s0
	s_cselect_b32 s2, s4, s2
	s_sub_i32 s4, s2, s0
	s_cmp_ge_u32 s2, s0
	s_cselect_b32 s2, s4, s2
	s_sub_i32 s1, s1, s2
	s_ashr_i32 s2, s1, 31
	s_abs_i32 s1, s1
	s_mul_hi_u32 s4, s1, s5
	s_mul_i32 s4, s4, s0
	s_sub_i32 s1, s1, s4
	s_sub_i32 s4, s1, s0
	s_cmp_ge_u32 s1, s0
	s_cselect_b32 s1, s4, s1
	s_sub_i32 s4, s1, s0
	s_cmp_ge_u32 s1, s0
	s_cselect_b32 s0, s4, s1
	s_xor_b32 s0, s0, s2
	s_sub_i32 s45, s0, s2

; #define PG8_STAGE(bufoff, gbase, voff) do { _Pragma("unroll") for (int _i = 0; _i < 2; ++_i) \
;         __builtin_amdgcn_global_load_lds((const unsigned*)((const char*)(gbase) + (voff)[_i]), (PG8_LAS unsigned*)(lds + (bufoff) + ldsw + _i * 8192), 16, 0, 0); } while (0)
; #define PG8_LDA(dst, b, h) do { _Pragma("unroll") for (int m = 0; m < 4; ++m) _Pragma("unroll") for (int k = 0; k < 2; ++k) dst[m][k] = *(const PG8_LAS bf16x8*)(lds + PG8_SA(b, h) + aoff + m * 2048 + k * 1024); } while (0)
; #define PG8_LDB(dst, b, h) do { _Pragma("unroll") for (int n = 0; n < 2; ++n) _Pragma("unroll") for (int k = 0; k < 2; ++k) dst[n][k] = *(const PG8_LAS bf16x8*)(lds + PG8_SB(b, h) + boff + n * 2048 + k * 1024); } while (0)
; #define PG8_SCHED __builtin_amdgcn_sched_barrier(0)
; template <class Epi, class Sched, bool ALIGN_EPI = false, bool SP2 = false, bool GATHER = false>
; __device__ __forceinline__ void gemm_phase(PG8_LAS unsigned char* lds, const Gemm g, const Sched& S, const Epi& E, int tid_in, const int* rowsrc = nullptr, PG8_LAS int* idx_lds = nullptr) {
;     ...
;         for (int t = 0; t < nt; t += 2) {
;             const bool last = (t == nt - 2);
;             if constexpr (GATHER) {
; #pragma unroll
;                 for (int h_ = 0; h_ < 2; ++h_) { gS[h_][0] = last ? gN[h_][0] : gA[h_][0]; gS[h_][1] = last ? gN[h_][1] : gA[h_][1]; } }
;             const char* a1 = cA + (size_t)(t + 1) * kstep;
;             const char* a2 = last ? nA : cA + (size_t)(t + 2) * kstep; const char* b2 = last ? nB : cB + (size_t)(t + 2) * kstep;
;             const char* a3 = a2 + kstep; const char* b3 = b2 + kstep;
;             if (last && has_next) S.a_ready(nxt);
;             if constexpr (SP2) {
;             PG8_LDB(B0, 0, 0); PG8_LDB(B1, 0, 1); PG8_SCHED; PG8_LDA(At, 0, 0); PG8_STAGE(PG8_SA(1, 1), a1 + hstepA, PG8_OA(1));
.LBB0_1245:
	s_add_u32 s31, s24, s30
	s_addc_u32 s38, s25, 0
	s_add_u32 s36, s31, 0x100
	s_addc_u32 s37, s38, 0
	s_and_b64 s[34:35], s[28:29], exec
	s_cselect_b32 s35, s15, s37
	s_cselect_b32 s34, s61, s36
	s_add_u32 s30, s22, s30
	s_addc_u32 s36, s23, 0
	s_add_u32 s30, s30, 0x100
	s_addc_u32 s36, s36, 0
	s_add_i32 s71, 0, 0x10000
	s_and_b64 s[28:29], s[28:29], exec
	s_cselect_b32 s37, s13, s36
	s_cselect_b32 s36, s62, s30
	s_add_i32 s29, 0, 0x14000
	s_add_u32 s40, s31, 0x40080
	s_addc_u32 s41, s38, 0
	s_add_i32 s70, s71, s2
	s_add_i32 m0, s21, 0xc000
	s_add_i32 s73, s21, 0xe000
	s_add_i32 s67, s70, 0x2000
	v_add_u32_e32 v136, s71, v139
	s_add_u32 s38, s36, 0x10000
	ds_read_b128 v[142:145], v136
	ds_read_b128 v[148:151], v136 offset:1024
	ds_read_b128 v[152:155], v136 offset:2048
	ds_read_b128 v[156:159], v136 offset:3072
	v_add_u32_e32 v136, s29, v139
	s_addc_u32 s39, s37, 0
	s_add_i32 s69, s29, s2
	ds_read_b128 v[160:163], v136
	ds_read_b128 v[164:167], v136 offset:1024
	ds_read_b128 v[168:171], v136 offset:2048
	ds_read_b128 v[172:175], v136 offset:3072
	s_add_i32 s68, s69, 0x2000
	s_add_i32 s66, 0, 0x18000
	s_add_i32 s65, 0, 0x1c000
	s_add_u32 s30, s34, 0x40000
	s_addc_u32 s31, s35, 0
	s_add_i32 s64, s66, s2
	s_add_i32 s63, s64, 0x2000
	s_add_u32 s28, s36, 0x10080
	s_addc_u32 s29, s37, 0
	s_add_i32 s72, s65, s2
	s_add_i32 s71, s72, 0x2000
	v_lshl_add_u64 v[136:137], s[40:41], 0, v[134:135]
	ds_read_b128 v[184:187], v141
	ds_read_b128 v[188:191], v141 offset:1024
	ds_read_b128 v[192:195], v141 offset:2048
	ds_read_b128 v[196:199], v141 offset:3072
	ds_read_b128 v[200:203], v141 offset:4096
	ds_read_b128 v[204:207], v141 offset:5120
	ds_read_b128 v[208:211], v141 offset:6144
	ds_read_b128 v[212:215], v141 offset:7168
	global_load_lds_dwordx4 v[136:137], off
	v_lshl_add_u64 v[136:137], s[40:41], 0, v[132:133]
	s_mov_b32 m0, s73
	s_nop 0
	global_load_lds_dwordx4 v[136:137], off
	s_cmp_eq_u32 s97, 0
	s_cbranch_scc1 .Lew13_a
	s_waitcnt vmcnt(24)
	s_branch .Lew13_b

; #define PG8_STAGE(bufoff, gbase, voff) do { _Pragma("unroll") for (int _i = 0; _i < 2; ++_i) \
;         __builtin_amdgcn_global_load_lds((const unsigned*)((const char*)(gbase) + (voff)[_i]), (PG8_LAS unsigned*)(lds + (bufoff) + ldsw + _i * 8192), 16, 0, 0); } while (0)
; #define PG8_LDA(dst, b, h) do { _Pragma("unroll") for (int m = 0; m < 4; ++m) _Pragma("unroll") for (int k = 0; k < 2; ++k) dst[m][k] = *(const PG8_LAS bf16x8*)(lds + PG8_SA(b, h) + aoff + m * 2048 + k * 1024); } while (0)
; #define PG8_LDB(dst, b, h) do { _Pragma("unroll") for (int n = 0; n < 2; ++n) _Pragma("unroll") for (int k = 0; k < 2; ++k) dst[n][k] = *(const PG8_LAS bf16x8*)(lds + PG8_SB(b, h) + boff + n * 2048 + k * 1024); } while (0)
; #define PG8_MMA(ai, bj, At, Bt) do { __builtin_amdgcn_s_setprio(1); _Pragma("unroll") for (int m = 0; m < 4; ++m) _Pragma("unroll") for (int n = 0; n < 2; ++n) _Pragma("unroll") for (int k = 0; k < 2; ++k) \
;         acc[ai][bj][m][n] = __builtin_amdgcn_mfma_f32_16x16x32_bf16(Bt[n][k], At[m][k], acc[ai][bj][m][n], 0, 0, 0); __builtin_amdgcn_s_setprio(0); } while (0)
; #define PG8_WAIT_V(n) asm volatile("s_waitcnt vmcnt(" #n ")" ::: "memory")
; #define PG8_WAIT_L(n) asm volatile("s_waitcnt lgkmcnt(" #n ")" ::: "memory")
; #define PG8_BAR __builtin_amdgcn_s_barrier()
; #define PG8_SCHED __builtin_amdgcn_sched_barrier(0)
; template <class Epi, class Sched, bool ALIGN_EPI = false, bool SP2 = false, bool GATHER = false>
; __device__ __forceinline__ void gemm_phase(PG8_LAS unsigned char* lds, const Gemm g, const Sched& S, const Epi& E, int tid_in, const int* rowsrc = nullptr, PG8_LAS int* idx_lds = nullptr) {
;     ...
;             PG8_LDB(B0, 0, 0); PG8_LDB(B1, 0, 1); PG8_SCHED; PG8_LDA(At, 0, 0); PG8_STAGE(PG8_SA(1, 1), a1 + hstepA, PG8_OA(1));
;             PG8_WAIT_V(8); PG8_WAIT_L(0); PG8_BAR; PG8_MMA(0, 0, At, B0); PG8_MMA(0, 1, At, B1); PG8_BAR; PG8_SCHED;
;             PG8_LDA(At, 0, 1); PG8_STAGE(PG8_SB(0, 0), b2, voffB); PG8_STAGE(PG8_SB(0, 1), b2 + hstep, voffB); PG8_STAGE(PG8_SA(0, 0), a2, PG8_OS(0));
.Lew13_b:
	s_waitcnt lgkmcnt(0)
	v_mfma_f32_16x16x32_bf16 v[126:129], v[142:145], v[184:187], v[126:129]
	v_mfma_f32_16x16x32_bf16 v[122:125], v[152:155], v[184:187], v[122:125]
	v_mfma_f32_16x16x32_bf16 v[118:121], v[142:145], v[192:195], v[118:121]
	s_barrier
	s_setprio 1
	s_waitcnt lgkmcnt(0)
	v_mfma_f32_16x16x32_bf16 v[110:113], v[152:155], v[192:195], v[110:113]
	v_mfma_f32_16x16x32_bf16 v[102:105], v[142:145], v[200:203], v[102:105]
	v_mfma_f32_16x16x32_bf16 v[94:97], v[152:155], v[200:203], v[94:97]
	v_mfma_f32_16x16x32_bf16 v[86:89], v[142:145], v[208:211], v[86:89]
	v_mfma_f32_16x16x32_bf16 v[78:81], v[152:155], v[208:211], v[78:81]
	v_mfma_f32_16x16x32_bf16 v[126:129], v[148:151], v[188:191], v[126:129]
	v_mfma_f32_16x16x32_bf16 v[122:125], v[156:159], v[188:191], v[122:125]
	v_mfma_f32_16x16x32_bf16 v[118:121], v[148:151], v[196:199], v[118:121]
	v_mfma_f32_16x16x32_bf16 v[110:113], v[156:159], v[196:199], v[110:113]
	v_mfma_f32_16x16x32_bf16 v[102:105], v[148:151], v[204:207], v[102:105]
	v_mfma_f32_16x16x32_bf16 v[94:97], v[156:159], v[204:207], v[94:97]
	v_mfma_f32_16x16x32_bf16 v[86:89], v[148:151], v[212:215], v[86:89]
	v_mfma_f32_16x16x32_bf16 v[78:81], v[156:159], v[212:215], v[78:81]
	s_setprio 0
	s_setprio 1
	v_mfma_f32_16x16x32_bf16 v[114:117], v[160:163], v[184:187], v[114:117]
	v_mfma_f32_16x16x32_bf16 v[106:109], v[168:171], v[184:187], v[106:109]
	v_mfma_f32_16x16x32_bf16 v[98:101], v[160:163], v[192:195], v[98:101]
	v_mfma_f32_16x16x32_bf16 v[90:93], v[168:171], v[192:195], v[90:93]
	v_mfma_f32_16x16x32_bf16 v[82:85], v[160:163], v[200:203], v[82:85]
	v_mfma_f32_16x16x32_bf16 v[74:77], v[168:171], v[200:203], v[74:77]
	v_mfma_f32_16x16x32_bf16 v[70:73], v[160:163], v[208:211], v[70:73]
	v_mfma_f32_16x16x32_bf16 v[66:69], v[168:171], v[208:211], v[66:69]
	v_mfma_f32_16x16x32_bf16 v[114:117], v[164:167], v[188:191], v[114:117]
	v_mfma_f32_16x16x32_bf16 v[106:109], v[172:175], v[188:191], v[106:109]
	v_mfma_f32_16x16x32_bf16 v[98:101], v[164:167], v[196:199], v[98:101]
	v_mfma_f32_16x16x32_bf16 v[90:93], v[172:175], v[196:199], v[90:93]
	v_mfma_f32_16x16x32_bf16 v[82:85], v[164:167], v[204:207], v[82:85]
	v_mfma_f32_16x16x32_bf16 v[74:77], v[172:175], v[204:207], v[74:77]
	v_mfma_f32_16x16x32_bf16 v[70:73], v[164:167], v[212:215], v[70:73]
	v_mfma_f32_16x16x32_bf16 v[66:69], v[172:175], v[212:215], v[66:69]
	s_setprio 0
	s_barrier
	s_mov_b32 m0, s70
	v_lshl_add_u64 v[136:137], s[36:37], 0, v[0:1]
	ds_read_b128 v[184:187], v141 offset:16384
	ds_read_b128 v[188:191], v141 offset:17408
	ds_read_b128 v[192:195], v141 offset:18432
	ds_read_b128 v[196:199], v141 offset:19456
	ds_read_b128 v[200:203], v141 offset:20480
	ds_read_b128 v[204:207], v141 offset:21504
	ds_read_b128 v[208:211], v141 offset:22528
	ds_read_b128 v[212:215], v141 offset:23552
	global_load_lds_dwordx4 v[136:137], off
	v_lshl_add_u64 v[176:177], s[36:37], 0, v[130:131]
	s_mov_b32 m0, s67
	v_lshl_add_u64 v[178:179], s[38:39], 0, v[0:1]
	global_load_lds_dwordx4 v[176:177], off
	s_mov_b32 m0, s69
	v_lshl_add_u64 v[180:181], s[34:35], 0, v[132:133]
	global_load_lds_dwordx4 v[178:179], off
	v_lshl_add_u64 v[178:179], s[38:39], 0, v[130:131]
	s_mov_b32 m0, s68
	s_nop 0
	global_load_lds_dwordx4 v[178:179], off
	v_lshl_add_u64 v[178:179], s[34:35], 0, v[134:135]
	s_mov_b32 m0, s21
	s_nop 0
	global_load_lds_dwordx4 v[178:179], off
	s_mov_b32 m0, s54
	s_nop 0
	global_load_lds_dwordx4 v[180:181], off
	s_cmp_eq_u32 s97, 0
	s_cbranch_scc1 .Lew14_a
	s_waitcnt vmcnt(24)
	s_branch .Lew14_b

; #define PG8_STAGE(bufoff, gbase, voff) do { _Pragma("unroll") for (int _i = 0; _i < 2; ++_i) \
;         __builtin_amdgcn_global_load_lds((const unsigned*)((const char*)(gbase) + (voff)[_i]), (PG8_LAS unsigned*)(lds + (bufoff) + ldsw + _i * 8192), 16, 0, 0); } while (0)
; #define PG8_LDA(dst, b, h) do { _Pragma("unroll") for (int m = 0; m < 4; ++m) _Pragma("unroll") for (int k = 0; k < 2; ++k) dst[m][k] = *(const PG8_LAS bf16x8*)(lds + PG8_SA(b, h) + aoff + m * 2048 + k * 1024); } while (0)
; #define PG8_LDB(dst, b, h) do { _Pragma("unroll") for (int n = 0; n < 2; ++n) _Pragma("unroll") for (int k = 0; k < 2; ++k) dst[n][k] = *(const PG8_LAS bf16x8*)(lds + PG8_SB(b, h) + boff + n * 2048 + k * 1024); } while (0)
; #define PG8_MMA(ai, bj, At, Bt) do { __builtin_amdgcn_s_setprio(1); _Pragma("unroll") for (int m = 0; m < 4; ++m) _Pragma("unroll") for (int n = 0; n < 2; ++n) _Pragma("unroll") for (int k = 0; k < 2; ++k) \
;         acc[ai][bj][m][n] = __builtin_amdgcn_mfma_f32_16x16x32_bf16(Bt[n][k], At[m][k], acc[ai][bj][m][n], 0, 0, 0); __builtin_amdgcn_s_setprio(0); } while (0)
; #define PG8_WAIT_V(n) asm volatile("s_waitcnt vmcnt(" #n ")" ::: "memory")
; #define PG8_WAIT_L(n) asm volatile("s_waitcnt lgkmcnt(" #n ")" ::: "memory")
; #define PG8_BAR __builtin_amdgcn_s_barrier()
; #define PG8_SCHED __builtin_amdgcn_sched_barrier(0)
; template <class Epi, class Sched, bool ALIGN_EPI = false, bool SP2 = false, bool GATHER = false>
; __device__ __forceinline__ void gemm_phase(PG8_LAS unsigned char* lds, const Gemm g, const Sched& S, const Epi& E, int tid_in, const int* rowsrc = nullptr, PG8_LAS int* idx_lds = nullptr) {
;     ...
;             PG8_WAIT_V(8); PG8_WAIT_L(0); PG8_BAR; PG8_MMA(1, 0, At, B0); PG8_MMA(1, 1, At, B1); PG8_BAR; PG8_SCHED;
;             PG8_LDB(B0, 1, 0); PG8_LDB(B1, 1, 1); PG8_SCHED; PG8_LDA(At, 1, 0); PG8_STAGE(PG8_SA(0, 1), a2 + hstepA, PG8_OS(1));
;             PG8_WAIT_V(8); PG8_WAIT_L(0); PG8_BAR; PG8_MMA(0, 0, At, B0); PG8_MMA(0, 1, At, B1); PG8_BAR; PG8_SCHED;
.Lew14_b:
	s_mov_b32 s97, 0
	s_waitcnt lgkmcnt(0)
	v_mfma_f32_16x16x32_bf16 v[62:65], v[142:145], v[184:187], v[62:65]
	v_mfma_f32_16x16x32_bf16 v[58:61], v[152:155], v[184:187], v[58:61]
	v_mfma_f32_16x16x32_bf16 v[54:57], v[142:145], v[192:195], v[54:57]
	s_barrier
	s_setprio 1
	s_waitcnt lgkmcnt(0)
	v_mfma_f32_16x16x32_bf16 v[46:49], v[152:155], v[192:195], v[46:49]
	v_mfma_f32_16x16x32_bf16 v[38:41], v[142:145], v[200:203], v[38:41]
	v_mfma_f32_16x16x32_bf16 v[30:33], v[152:155], v[200:203], v[30:33]
	v_mfma_f32_16x16x32_bf16 v[22:25], v[142:145], v[208:211], v[22:25]
	v_mfma_f32_16x16x32_bf16 v[14:17], v[152:155], v[208:211], v[14:17]
	v_mfma_f32_16x16x32_bf16 v[62:65], v[148:151], v[188:191], v[62:65]
	v_mfma_f32_16x16x32_bf16 v[58:61], v[156:159], v[188:191], v[58:61]
	v_mfma_f32_16x16x32_bf16 v[54:57], v[148:151], v[196:199], v[54:57]
	v_mfma_f32_16x16x32_bf16 v[46:49], v[156:159], v[196:199], v[46:49]
	v_mfma_f32_16x16x32_bf16 v[38:41], v[148:151], v[204:207], v[38:41]
	v_mfma_f32_16x16x32_bf16 v[30:33], v[156:159], v[204:207], v[30:33]
	v_mfma_f32_16x16x32_bf16 v[22:25], v[148:151], v[212:215], v[22:25]
	v_mfma_f32_16x16x32_bf16 v[14:17], v[156:159], v[212:215], v[14:17]
	s_setprio 0
	s_setprio 1
	v_mfma_f32_16x16x32_bf16 v[50:53], v[160:163], v[184:187], v[50:53]
	v_mfma_f32_16x16x32_bf16 v[42:45], v[168:171], v[184:187], v[42:45]
	v_mfma_f32_16x16x32_bf16 v[34:37], v[160:163], v[192:195], v[34:37]
	v_mfma_f32_16x16x32_bf16 v[26:29], v[168:171], v[192:195], v[26:29]
	v_mfma_f32_16x16x32_bf16 v[18:21], v[160:163], v[200:203], v[18:21]
	v_mfma_f32_16x16x32_bf16 v[10:13], v[168:171], v[200:203], v[10:13]
	v_mfma_f32_16x16x32_bf16 v[6:9], v[160:163], v[208:211], v[6:9]
	v_mfma_f32_16x16x32_bf16 v[2:5], v[168:171], v[208:211], v[2:5]
	v_mfma_f32_16x16x32_bf16 v[50:53], v[164:167], v[188:191], v[50:53]
	v_mfma_f32_16x16x32_bf16 v[42:45], v[172:175], v[188:191], v[42:45]
	v_mfma_f32_16x16x32_bf16 v[34:37], v[164:167], v[196:199], v[34:37]
	v_mfma_f32_16x16x32_bf16 v[26:29], v[172:175], v[196:199], v[26:29]
	v_mfma_f32_16x16x32_bf16 v[18:21], v[164:167], v[204:207], v[18:21]
	v_mfma_f32_16x16x32_bf16 v[10:13], v[172:175], v[204:207], v[10:13]
	v_mfma_f32_16x16x32_bf16 v[6:9], v[164:167], v[212:215], v[6:9]
	v_mfma_f32_16x16x32_bf16 v[2:5], v[172:175], v[212:215], v[2:5]
	s_setprio 0
	s_barrier
	v_add_u32_e32 v156, s66, v139
	v_add_u32_e32 v172, s65, v139
	ds_read_b128 v[142:145], v156
	ds_read_b128 v[148:151], v156 offset:1024
	ds_read_b128 v[152:155], v156 offset:2048
	ds_read_b128 v[156:159], v156 offset:3072
	ds_read_b128 v[160:163], v172
	ds_read_b128 v[164:167], v172 offset:1024
	ds_read_b128 v[168:171], v172 offset:2048
	ds_read_b128 v[172:175], v172 offset:3072
	s_mov_b32 m0, s55
	v_lshl_add_u64 v[182:183], s[30:31], 0, v[134:135]
	ds_read_b128 v[184:187], v141 offset:32768
	ds_read_b128 v[188:191], v141 offset:33792
	ds_read_b128 v[192:195], v141 offset:34816
	ds_read_b128 v[196:199], v141 offset:35840
	ds_read_b128 v[200:203], v141 offset:36864
	ds_read_b128 v[204:207], v141 offset:37888
	ds_read_b128 v[208:211], v141 offset:38912
	ds_read_b128 v[212:215], v141 offset:39936
	global_load_lds_dwordx4 v[182:183], off
	v_lshl_add_u64 v[182:183], s[30:31], 0, v[132:133]
	s_mov_b32 m0, s56
	s_nop 0
	global_load_lds_dwordx4 v[182:183], off
	s_waitcnt vmcnt(8)
	s_waitcnt lgkmcnt(0)
	v_mfma_f32_16x16x32_bf16 v[126:129], v[142:145], v[184:187], v[126:129]
	v_mfma_f32_16x16x32_bf16 v[122:125], v[152:155], v[184:187], v[122:125]
	v_mfma_f32_16x16x32_bf16 v[118:121], v[142:145], v[192:195], v[118:121]
	s_barrier
	s_setprio 1
	s_waitcnt lgkmcnt(0)
	v_mfma_f32_16x16x32_bf16 v[110:113], v[152:155], v[192:195], v[110:113]
	v_mfma_f32_16x16x32_bf16 v[102:105], v[142:145], v[200:203], v[102:105]
	v_mfma_f32_16x16x32_bf16 v[94:97], v[152:155], v[200:203], v[94:97]
	v_mfma_f32_16x16x32_bf16 v[86:89], v[142:145], v[208:211], v[86:89]
	v_mfma_f32_16x16x32_bf16 v[78:81], v[152:155], v[208:211], v[78:81]
	v_mfma_f32_16x16x32_bf16 v[126:129], v[148:151], v[188:191], v[126:129]
	v_mfma_f32_16x16x32_bf16 v[122:125], v[156:159], v[188:191], v[122:125]
	v_mfma_f32_16x16x32_bf16 v[118:121], v[148:151], v[196:199], v[118:121]
	v_mfma_f32_16x16x32_bf16 v[110:113], v[156:159], v[196:199], v[110:113]
	v_mfma_f32_16x16x32_bf16 v[102:105], v[148:151], v[204:207], v[102:105]
	v_mfma_f32_16x16x32_bf16 v[94:97], v[156:159], v[204:207], v[94:97]
	v_mfma_f32_16x16x32_bf16 v[86:89], v[148:151], v[212:215], v[86:89]
	v_mfma_f32_16x16x32_bf16 v[78:81], v[156:159], v[212:215], v[78:81]
	s_setprio 0
	s_setprio 1
	v_mfma_f32_16x16x32_bf16 v[114:117], v[160:163], v[184:187], v[114:117]
	v_mfma_f32_16x16x32_bf16 v[106:109], v[168:171], v[184:187], v[106:109]
	v_mfma_f32_16x16x32_bf16 v[98:101], v[160:163], v[192:195], v[98:101]
	v_mfma_f32_16x16x32_bf16 v[90:93], v[168:171], v[192:195], v[90:93]
	v_mfma_f32_16x16x32_bf16 v[82:85], v[160:163], v[200:203], v[82:85]
	v_mfma_f32_16x16x32_bf16 v[74:77], v[168:171], v[200:203], v[74:77]
	v_mfma_f32_16x16x32_bf16 v[70:73], v[160:163], v[208:211], v[70:73]
	v_mfma_f32_16x16x32_bf16 v[66:69], v[168:171], v[208:211], v[66:69]
	v_mfma_f32_16x16x32_bf16 v[114:117], v[164:167], v[188:191], v[114:117]
	v_mfma_f32_16x16x32_bf16 v[106:109], v[172:175], v[188:191], v[106:109]
	v_mfma_f32_16x16x32_bf16 v[98:101], v[164:167], v[196:199], v[98:101]
	v_mfma_f32_16x16x32_bf16 v[90:93], v[172:175], v[196:199], v[90:93]
	v_mfma_f32_16x16x32_bf16 v[82:85], v[164:167], v[204:207], v[82:85]
	v_mfma_f32_16x16x32_bf16 v[74:77], v[172:175], v[204:207], v[74:77]
	v_mfma_f32_16x16x32_bf16 v[70:73], v[164:167], v[212:215], v[70:73]
	v_mfma_f32_16x16x32_bf16 v[66:69], v[172:175], v[212:215], v[66:69]
	s_setprio 0
	s_barrier
; #define PG8_STAGE(bufoff, gbase, voff) do { _Pragma("unroll") for (int _i = 0; _i < 2; ++_i) \
;         __builtin_amdgcn_global_load_lds((const unsigned*)((const char*)(gbase) + (voff)[_i]), (PG8_LAS unsigned*)(lds + (bufoff) + ldsw + _i * 8192), 16, 0, 0); } while (0)
; #define PG8_LDA(dst, b, h) do { _Pragma("unroll") for (int m = 0; m < 4; ++m) _Pragma("unroll") for (int k = 0; k < 2; ++k) dst[m][k] = *(const PG8_LAS bf16x8*)(lds + PG8_SA(b, h) + aoff + m * 2048 + k * 1024); } while (0)
; #define PG8_MMA(ai, bj, At, Bt) do { __builtin_amdgcn_s_setprio(1); _Pragma("unroll") for (int m = 0; m < 4; ++m) _Pragma("unroll") for (int n = 0; n < 2; ++n) _Pragma("unroll") for (int k = 0; k < 2; ++k) \
;         acc[ai][bj][m][n] = __builtin_amdgcn_mfma_f32_16x16x32_bf16(Bt[n][k], At[m][k], acc[ai][bj][m][n], 0, 0, 0); __builtin_amdgcn_s_setprio(0); } while (0)
; #define PG8_WAIT_V(n) asm volatile("s_waitcnt vmcnt(" #n ")" ::: "memory")
; #define PG8_WAIT_L(n) asm volatile("s_waitcnt lgkmcnt(" #n ")" ::: "memory")
; #define PG8_BAR __builtin_amdgcn_s_barrier()
; #define PG8_SCHED __builtin_amdgcn_sched_barrier(0)
; template <class Epi, class Sched, bool ALIGN_EPI = false, bool SP2 = false, bool GATHER = false>
; __device__ __forceinline__ void gemm_phase(PG8_LAS unsigned char* lds, const Gemm g, const Sched& S, const Epi& E, int tid_in, const int* rowsrc = nullptr, PG8_LAS int* idx_lds = nullptr) {
;     ...
;             PG8_LDA(At, 1, 1); PG8_STAGE(PG8_SB(1, 0), b3, voffB); PG8_STAGE(PG8_SB(1, 1), b3 + hstep, voffB); PG8_STAGE(PG8_SA(1, 0), a3, PG8_OS(0));
;             PG8_WAIT_V(8); PG8_WAIT_L(0); PG8_BAR; PG8_MMA(1, 0, At, B0); PG8_MMA(1, 1, At, B1); PG8_BAR; PG8_SCHED;
;     ...
;         if constexpr (ALIGN_EPI) { if (wr == 0) PG8_BAR; }
	s_mov_b32 m0, s64
	v_lshl_add_u64 v[136:137], v[136:137], 0, s[10:11]
	ds_read_b128 v[184:187], v141 offset:49152
	ds_read_b128 v[188:191], v141 offset:50176
	ds_read_b128 v[192:195], v141 offset:51200
	ds_read_b128 v[196:199], v141 offset:52224
	ds_read_b128 v[200:203], v141 offset:53248
	ds_read_b128 v[204:207], v141 offset:54272
	ds_read_b128 v[208:211], v141 offset:55296
	ds_read_b128 v[212:215], v141 offset:56320
	global_load_lds_dwordx4 v[136:137], off
	v_lshl_add_u64 v[136:137], v[176:177], 0, s[10:11]
	s_mov_b32 m0, s63
	s_nop 0
	global_load_lds_dwordx4 v[136:137], off
	v_lshl_add_u64 v[136:137], s[28:29], 0, v[0:1]
	s_mov_b32 m0, s72
	s_nop 0
	global_load_lds_dwordx4 v[136:137], off
	v_lshl_add_u64 v[136:137], s[28:29], 0, v[130:131]
	s_mov_b32 m0, s71
	s_nop 0
	global_load_lds_dwordx4 v[136:137], off
	v_lshl_add_u64 v[136:137], v[178:179], 0, s[10:11]
	s_mov_b32 m0, s57
	s_nop 0
	global_load_lds_dwordx4 v[136:137], off
	v_lshl_add_u64 v[136:137], v[180:181], 0, s[10:11]
	s_mov_b32 m0, s58
	s_nop 0
	global_load_lds_dwordx4 v[136:137], off
	s_waitcnt vmcnt(8)
	s_waitcnt lgkmcnt(0)
	v_mfma_f32_16x16x32_bf16 v[62:65], v[142:145], v[184:187], v[62:65]
	v_mfma_f32_16x16x32_bf16 v[58:61], v[152:155], v[184:187], v[58:61]
	v_mfma_f32_16x16x32_bf16 v[54:57], v[142:145], v[192:195], v[54:57]
	s_barrier
	s_setprio 1
	s_waitcnt lgkmcnt(0)
	v_mfma_f32_16x16x32_bf16 v[46:49], v[152:155], v[192:195], v[46:49]
	v_mfma_f32_16x16x32_bf16 v[38:41], v[142:145], v[200:203], v[38:41]
	v_mfma_f32_16x16x32_bf16 v[30:33], v[152:155], v[200:203], v[30:33]
	v_mfma_f32_16x16x32_bf16 v[22:25], v[142:145], v[208:211], v[22:25]
	v_mfma_f32_16x16x32_bf16 v[14:17], v[152:155], v[208:211], v[14:17]
	v_mfma_f32_16x16x32_bf16 v[62:65], v[148:151], v[188:191], v[62:65]
	v_mfma_f32_16x16x32_bf16 v[58:61], v[156:159], v[188:191], v[58:61]
	v_mfma_f32_16x16x32_bf16 v[54:57], v[148:151], v[196:199], v[54:57]
	v_mfma_f32_16x16x32_bf16 v[46:49], v[156:159], v[196:199], v[46:49]
	v_mfma_f32_16x16x32_bf16 v[38:41], v[148:151], v[204:207], v[38:41]
	v_mfma_f32_16x16x32_bf16 v[30:33], v[156:159], v[204:207], v[30:33]
	v_mfma_f32_16x16x32_bf16 v[22:25], v[148:151], v[212:215], v[22:25]
	v_mfma_f32_16x16x32_bf16 v[14:17], v[156:159], v[212:215], v[14:17]
	s_setprio 0
	s_setprio 1
	v_mfma_f32_16x16x32_bf16 v[50:53], v[160:163], v[184:187], v[50:53]
	v_mfma_f32_16x16x32_bf16 v[42:45], v[168:171], v[184:187], v[42:45]
	v_mfma_f32_16x16x32_bf16 v[34:37], v[160:163], v[192:195], v[34:37]
	v_mfma_f32_16x16x32_bf16 v[26:29], v[168:171], v[192:195], v[26:29]
	v_mfma_f32_16x16x32_bf16 v[18:21], v[160:163], v[200:203], v[18:21]
	v_mfma_f32_16x16x32_bf16 v[10:13], v[168:171], v[200:203], v[10:13]
	v_mfma_f32_16x16x32_bf16 v[6:9], v[160:163], v[208:211], v[6:9]
	v_mfma_f32_16x16x32_bf16 v[2:5], v[168:171], v[208:211], v[2:5]
	v_mfma_f32_16x16x32_bf16 v[50:53], v[164:167], v[188:191], v[50:53]
	v_mfma_f32_16x16x32_bf16 v[42:45], v[172:175], v[188:191], v[42:45]
	v_mfma_f32_16x16x32_bf16 v[34:37], v[164:167], v[196:199], v[34:37]
	v_mfma_f32_16x16x32_bf16 v[26:29], v[172:175], v[196:199], v[26:29]
	v_mfma_f32_16x16x32_bf16 v[18:21], v[164:167], v[204:207], v[18:21]
	v_mfma_f32_16x16x32_bf16 v[10:13], v[172:175], v[204:207], v[10:13]
	v_mfma_f32_16x16x32_bf16 v[6:9], v[164:167], v[212:215], v[6:9]
	v_mfma_f32_16x16x32_bf16 v[2:5], v[172:175], v[212:215], v[2:5]
	s_setprio 0
	s_barrier
	s_movk_i32 s30, 0x100
	s_andn2_b64 vcc, exec, s[26:27]
	s_mov_b64 s[28:29], -1
	s_mov_b64 s[26:27], 0
	s_cbranch_vccz .LBB0_1245
	s_mov_b32 s97, 1
	s_and_b64 vcc, exec, s[8:9]
	s_cbranch_vccz .LBB0_1248
	s_barrier

; #define PG8_STAGE(bufoff, gbase, voff) do { _Pragma("unroll") for (int _i = 0; _i < 2; ++_i) \
;         __builtin_amdgcn_global_load_lds((const unsigned*)((const char*)(gbase) + (voff)[_i]), (PG8_LAS unsigned*)(lds + (bufoff) + ldsw + _i * 8192), 16, 0, 0); } while (0)
; #define PG8_LDA(dst, b, h) do { _Pragma("unroll") for (int m = 0; m < 4; ++m) _Pragma("unroll") for (int k = 0; k < 2; ++k) dst[m][k] = *(const PG8_LAS bf16x8*)(lds + PG8_SA(b, h) + aoff + m * 2048 + k * 1024); } while (0)
; #define PG8_LDB(dst, b, h) do { _Pragma("unroll") for (int n = 0; n < 2; ++n) _Pragma("unroll") for (int k = 0; k < 2; ++k) dst[n][k] = *(const PG8_LAS bf16x8*)(lds + PG8_SB(b, h) + boff + n * 2048 + k * 1024); } while (0)
; #define PG8_SCHED __builtin_amdgcn_sched_barrier(0)
; template <class Epi, class Sched, bool ALIGN_EPI = false, bool SP2 = false, bool GATHER = false>
; __device__ __forceinline__ void gemm_phase(PG8_LAS unsigned char* lds, const Gemm g, const Sched& S, const Epi& E, int tid_in, const int* rowsrc = nullptr, PG8_LAS int* idx_lds = nullptr) {
;     ...
;         for (int t = 0; t < nt; t += 2) {
;             const bool last = (t == nt - 2);
;             if constexpr (GATHER) {
; #pragma unroll
;                 for (int h_ = 0; h_ < 2; ++h_) { gS[h_][0] = last ? gN[h_][0] : gA[h_][0]; gS[h_][1] = last ? gN[h_][1] : gA[h_][1]; } }
;             const char* a1 = cA + (size_t)(t + 1) * kstep;
;             const char* a2 = last ? nA : cA + (size_t)(t + 2) * kstep; const char* b2 = last ? nB : cB + (size_t)(t + 2) * kstep;
;             const char* a3 = a2 + kstep; const char* b3 = b2 + kstep;
;             if (last && has_next) S.a_ready(nxt);
;             if constexpr (SP2) {
;             PG8_LDB(B0, 0, 0); PG8_LDB(B1, 0, 1); PG8_SCHED; PG8_LDA(At, 0, 0); PG8_STAGE(PG8_SA(1, 1), a1 + hstepA, PG8_OA(1));
.LBB0_1618:
	s_add_u32 s22, s20, 0xfffc0080
	s_addc_u32 s23, s21, -1
	s_add_i32 s57, 0, 0x10000
	s_cmp_eq_u32 s56, 12
	s_cselect_b32 s25, s9, s23
	s_cselect_b32 s24, s17, s22
	s_cselect_b32 s23, s7, s55
	s_cselect_b32 s22, s19, s54
	s_add_i32 s60, 0, 0x14000
	v_add_u32_e32 v142, s57, v184
	v_add_u32_e32 v178, s60, v184
	ds_read_b128 v[122:125], v142
	ds_read_b128 v[126:129], v142 offset:1024
	ds_read_b128 v[134:137], v142 offset:2048
	ds_read_b128 v[142:145], v142 offset:3072
	ds_read_b128 v[174:177], v178
	ds_read_b128 v[188:191], v178 offset:1024
	ds_read_b128 v[192:195], v178 offset:2048
	ds_read_b128 v[196:199], v178 offset:3072
	v_lshl_add_u64 v[178:179], s[20:21], 0, v[170:171]
	s_add_i32 m0, s39, 0xc000
	ds_read_b128 v[200:203], v186
	ds_read_b128 v[204:207], v186 offset:1024
	ds_read_b128 v[208:211], v186 offset:2048
	ds_read_b128 v[212:215], v186 offset:3072
	ds_read_b128 v[216:219], v186 offset:4096
	ds_read_b128 v[220:223], v186 offset:5120
	ds_read_b128 v[224:227], v186 offset:6144
	ds_read_b128 v[228:231], v186 offset:7168
	global_load_lds_dwordx4 v[178:179], off
	v_lshl_add_u64 v[178:179], s[20:21], 0, v[172:173]
	s_add_i32 m0, s39, 0xe000
	s_nop 0
	global_load_lds_dwordx4 v[178:179], off
	s_cmp_eq_u32 s97, 0
	s_cbranch_scc1 .Lew15_a
	s_waitcnt vmcnt(24)
	s_branch .Lew15_b

; #define PG8_STAGE(bufoff, gbase, voff) do { _Pragma("unroll") for (int _i = 0; _i < 2; ++_i) \
;         __builtin_amdgcn_global_load_lds((const unsigned*)((const char*)(gbase) + (voff)[_i]), (PG8_LAS unsigned*)(lds + (bufoff) + ldsw + _i * 8192), 16, 0, 0); } while (0)
; #define PG8_LDA(dst, b, h) do { _Pragma("unroll") for (int m = 0; m < 4; ++m) _Pragma("unroll") for (int k = 0; k < 2; ++k) dst[m][k] = *(const PG8_LAS bf16x8*)(lds + PG8_SA(b, h) + aoff + m * 2048 + k * 1024); } while (0)
; #define PG8_LDB(dst, b, h) do { _Pragma("unroll") for (int n = 0; n < 2; ++n) _Pragma("unroll") for (int k = 0; k < 2; ++k) dst[n][k] = *(const PG8_LAS bf16x8*)(lds + PG8_SB(b, h) + boff + n * 2048 + k * 1024); } while (0)
; #define PG8_MMA(ai, bj, At, Bt) do { __builtin_amdgcn_s_setprio(1); _Pragma("unroll") for (int m = 0; m < 4; ++m) _Pragma("unroll") for (int n = 0; n < 2; ++n) _Pragma("unroll") for (int k = 0; k < 2; ++k) \
;         acc[ai][bj][m][n] = __builtin_amdgcn_mfma_f32_16x16x32_bf16(Bt[n][k], At[m][k], acc[ai][bj][m][n], 0, 0, 0); __builtin_amdgcn_s_setprio(0); } while (0)
; #define PG8_WAIT_V(n) asm volatile("s_waitcnt vmcnt(" #n ")" ::: "memory")
; #define PG8_WAIT_L(n) asm volatile("s_waitcnt lgkmcnt(" #n ")" ::: "memory")
; #define PG8_BAR __builtin_amdgcn_s_barrier()
; #define PG8_SCHED __builtin_amdgcn_sched_barrier(0)
; template <class Epi, class Sched, bool ALIGN_EPI = false, bool SP2 = false, bool GATHER = false>
; __device__ __forceinline__ void gemm_phase(PG8_LAS unsigned char* lds, const Gemm g, const Sched& S, const Epi& E, int tid_in, const int* rowsrc = nullptr, PG8_LAS int* idx_lds = nullptr) {
;     ...
;             PG8_LDB(B0, 0, 0); PG8_LDB(B1, 0, 1); PG8_SCHED; PG8_LDA(At, 0, 0); PG8_STAGE(PG8_SA(1, 1), a1 + hstepA, PG8_OA(1));
;             PG8_WAIT_V(8); PG8_WAIT_L(0); PG8_BAR; PG8_MMA(0, 0, At, B0); PG8_MMA(0, 1, At, B1); PG8_BAR; PG8_SCHED;
;             PG8_LDA(At, 0, 1); PG8_STAGE(PG8_SB(0, 0), b2, voffB); PG8_STAGE(PG8_SB(0, 1), b2 + hstep, voffB); PG8_STAGE(PG8_SA(0, 0), a2, PG8_OS(0));
.Lew15_b:
	s_waitcnt lgkmcnt(0)
	v_mfma_f32_16x16x32_bf16 v[138:141], v[122:125], v[200:203], v[138:141]
	v_mfma_f32_16x16x32_bf16 v[130:133], v[134:137], v[200:203], v[130:133]
	v_mfma_f32_16x16x32_bf16 v[118:121], v[122:125], v[208:211], v[118:121]
	s_barrier
	s_setprio 1
	s_waitcnt lgkmcnt(0)
	v_mfma_f32_16x16x32_bf16 v[106:109], v[134:137], v[208:211], v[106:109]
	v_mfma_f32_16x16x32_bf16 v[102:105], v[122:125], v[216:219], v[102:105]
	v_mfma_f32_16x16x32_bf16 v[90:93], v[134:137], v[216:219], v[90:93]
	v_mfma_f32_16x16x32_bf16 v[86:89], v[122:125], v[224:227], v[86:89]
	v_mfma_f32_16x16x32_bf16 v[74:77], v[134:137], v[224:227], v[74:77]
	v_mfma_f32_16x16x32_bf16 v[138:141], v[126:129], v[204:207], v[138:141]
	v_mfma_f32_16x16x32_bf16 v[130:133], v[142:145], v[204:207], v[130:133]
	v_mfma_f32_16x16x32_bf16 v[118:121], v[126:129], v[212:215], v[118:121]
	v_mfma_f32_16x16x32_bf16 v[106:109], v[142:145], v[212:215], v[106:109]
	v_mfma_f32_16x16x32_bf16 v[102:105], v[126:129], v[220:223], v[102:105]
	v_mfma_f32_16x16x32_bf16 v[90:93], v[142:145], v[220:223], v[90:93]
	v_mfma_f32_16x16x32_bf16 v[86:89], v[126:129], v[228:231], v[86:89]
	v_mfma_f32_16x16x32_bf16 v[74:77], v[142:145], v[228:231], v[74:77]
	s_setprio 0
	s_setprio 1
	v_mfma_f32_16x16x32_bf16 v[114:117], v[174:177], v[200:203], v[114:117]
	v_mfma_f32_16x16x32_bf16 v[110:113], v[192:195], v[200:203], v[110:113]
	v_mfma_f32_16x16x32_bf16 v[98:101], v[174:177], v[208:211], v[98:101]
	v_mfma_f32_16x16x32_bf16 v[94:97], v[192:195], v[208:211], v[94:97]
	v_mfma_f32_16x16x32_bf16 v[82:85], v[174:177], v[216:219], v[82:85]
	v_mfma_f32_16x16x32_bf16 v[78:81], v[192:195], v[216:219], v[78:81]
	v_mfma_f32_16x16x32_bf16 v[70:73], v[174:177], v[224:227], v[70:73]
	v_mfma_f32_16x16x32_bf16 v[66:69], v[192:195], v[224:227], v[66:69]
	v_mfma_f32_16x16x32_bf16 v[114:117], v[188:191], v[204:207], v[114:117]
	v_mfma_f32_16x16x32_bf16 v[110:113], v[196:199], v[204:207], v[110:113]
	v_mfma_f32_16x16x32_bf16 v[98:101], v[188:191], v[212:215], v[98:101]
	v_mfma_f32_16x16x32_bf16 v[94:97], v[196:199], v[212:215], v[94:97]
	v_mfma_f32_16x16x32_bf16 v[82:85], v[188:191], v[220:223], v[82:85]
	v_mfma_f32_16x16x32_bf16 v[78:81], v[196:199], v[220:223], v[78:81]
	v_mfma_f32_16x16x32_bf16 v[70:73], v[188:191], v[228:231], v[70:73]
	v_mfma_f32_16x16x32_bf16 v[66:69], v[196:199], v[228:231], v[66:69]
	s_setprio 0
	s_barrier
	s_add_i32 s57, s57, s38
	v_lshl_add_u64 v[178:179], s[22:23], 0, v[0:1]
	s_mov_b32 m0, s57
	ds_read_b128 v[200:203], v186 offset:16384
	ds_read_b128 v[204:207], v186 offset:17408
	ds_read_b128 v[208:211], v186 offset:18432
	ds_read_b128 v[212:215], v186 offset:19456
	ds_read_b128 v[216:219], v186 offset:20480
	ds_read_b128 v[220:223], v186 offset:21504
	ds_read_b128 v[224:227], v186 offset:22528
	ds_read_b128 v[228:231], v186 offset:23552
	global_load_lds_dwordx4 v[178:179], off
	s_add_i32 m0, s57, 0x2000
	s_add_u32 s58, s22, 0x40000
	v_lshl_add_u64 v[180:181], s[22:23], 0, v[148:149]
	s_addc_u32 s59, s23, 0
	s_add_i32 s57, s60, s38
	global_load_lds_dwordx4 v[180:181], off
	v_lshl_add_u64 v[182:183], s[58:59], 0, v[0:1]
	s_mov_b32 m0, s57
	v_lshl_add_u64 v[232:233], s[24:25], 0, v[150:151]
	global_load_lds_dwordx4 v[182:183], off
	v_lshl_add_u64 v[182:183], s[58:59], 0, v[148:149]
	s_add_i32 m0, s57, 0x2000
	s_nop 0
	global_load_lds_dwordx4 v[182:183], off
	v_lshl_add_u64 v[182:183], s[24:25], 0, v[152:153]
	s_mov_b32 m0, s39
	s_nop 0
	global_load_lds_dwordx4 v[182:183], off
	s_mov_b32 m0, s40
	s_nop 0
	global_load_lds_dwordx4 v[232:233], off
	s_cmp_eq_u32 s97, 0
	s_cbranch_scc1 .Lew16_a
	s_waitcnt vmcnt(24)
	s_branch .Lew16_b

; #define PG8_STAGE(bufoff, gbase, voff) do { _Pragma("unroll") for (int _i = 0; _i < 2; ++_i) \
;         __builtin_amdgcn_global_load_lds((const unsigned*)((const char*)(gbase) + (voff)[_i]), (PG8_LAS unsigned*)(lds + (bufoff) + ldsw + _i * 8192), 16, 0, 0); } while (0)
; #define PG8_LDA(dst, b, h) do { _Pragma("unroll") for (int m = 0; m < 4; ++m) _Pragma("unroll") for (int k = 0; k < 2; ++k) dst[m][k] = *(const PG8_LAS bf16x8*)(lds + PG8_SA(b, h) + aoff + m * 2048 + k * 1024); } while (0)
; #define PG8_LDB(dst, b, h) do { _Pragma("unroll") for (int n = 0; n < 2; ++n) _Pragma("unroll") for (int k = 0; k < 2; ++k) dst[n][k] = *(const PG8_LAS bf16x8*)(lds + PG8_SB(b, h) + boff + n * 2048 + k * 1024); } while (0)
; #define PG8_MMA(ai, bj, At, Bt) do { __builtin_amdgcn_s_setprio(1); _Pragma("unroll") for (int m = 0; m < 4; ++m) _Pragma("unroll") for (int n = 0; n < 2; ++n) _Pragma("unroll") for (int k = 0; k < 2; ++k) \
;         acc[ai][bj][m][n] = __builtin_amdgcn_mfma_f32_16x16x32_bf16(Bt[n][k], At[m][k], acc[ai][bj][m][n], 0, 0, 0); __builtin_amdgcn_s_setprio(0); } while (0)
; #define PG8_WAIT_V(n) asm volatile("s_waitcnt vmcnt(" #n ")" ::: "memory")
; #define PG8_WAIT_L(n) asm volatile("s_waitcnt lgkmcnt(" #n ")" ::: "memory")
; #define PG8_BAR __builtin_amdgcn_s_barrier()
; #define PG8_SCHED __builtin_amdgcn_sched_barrier(0)
; template <class Epi, class Sched, bool ALIGN_EPI = false, bool SP2 = false, bool GATHER = false>
; __device__ __forceinline__ void gemm_phase(PG8_LAS unsigned char* lds, const Gemm g, const Sched& S, const Epi& E, int tid_in, const int* rowsrc = nullptr, PG8_LAS int* idx_lds = nullptr) {
;     ...
;             PG8_WAIT_V(8); PG8_WAIT_L(0); PG8_BAR; PG8_MMA(1, 0, At, B0); PG8_MMA(1, 1, At, B1); PG8_BAR; PG8_SCHED;
;             PG8_LDB(B0, 1, 0); PG8_LDB(B1, 1, 1); PG8_SCHED; PG8_LDA(At, 1, 0); PG8_STAGE(PG8_SA(0, 1), a2 + hstepA, PG8_OS(1));
;             PG8_WAIT_V(8); PG8_WAIT_L(0); PG8_BAR; PG8_MMA(0, 0, At, B0); PG8_MMA(0, 1, At, B1); PG8_BAR; PG8_SCHED;
.Lew16_b:
	s_mov_b32 s97, 0
	s_waitcnt lgkmcnt(0)
	v_mfma_f32_16x16x32_bf16 v[62:65], v[122:125], v[200:203], v[62:65]
	v_mfma_f32_16x16x32_bf16 v[58:61], v[134:137], v[200:203], v[58:61]
	v_mfma_f32_16x16x32_bf16 v[54:57], v[122:125], v[208:211], v[54:57]
	s_barrier
	s_setprio 1
	s_waitcnt lgkmcnt(0)
	v_mfma_f32_16x16x32_bf16 v[42:45], v[134:137], v[208:211], v[42:45]
	v_mfma_f32_16x16x32_bf16 v[38:41], v[122:125], v[216:219], v[38:41]
	v_mfma_f32_16x16x32_bf16 v[26:29], v[134:137], v[216:219], v[26:29]
	v_mfma_f32_16x16x32_bf16 v[22:25], v[122:125], v[224:227], v[22:25]
	v_mfma_f32_16x16x32_bf16 v[10:13], v[134:137], v[224:227], v[10:13]
	v_mfma_f32_16x16x32_bf16 v[62:65], v[126:129], v[204:207], v[62:65]
	v_mfma_f32_16x16x32_bf16 v[58:61], v[142:145], v[204:207], v[58:61]
	v_mfma_f32_16x16x32_bf16 v[54:57], v[126:129], v[212:215], v[54:57]
	v_mfma_f32_16x16x32_bf16 v[42:45], v[142:145], v[212:215], v[42:45]
	v_mfma_f32_16x16x32_bf16 v[38:41], v[126:129], v[220:223], v[38:41]
	v_mfma_f32_16x16x32_bf16 v[26:29], v[142:145], v[220:223], v[26:29]
	v_mfma_f32_16x16x32_bf16 v[22:25], v[126:129], v[228:231], v[22:25]
	v_mfma_f32_16x16x32_bf16 v[10:13], v[142:145], v[228:231], v[10:13]
	s_setprio 0
	s_setprio 1
	v_mfma_f32_16x16x32_bf16 v[50:53], v[174:177], v[200:203], v[50:53]
	v_mfma_f32_16x16x32_bf16 v[46:49], v[192:195], v[200:203], v[46:49]
	v_mfma_f32_16x16x32_bf16 v[34:37], v[174:177], v[208:211], v[34:37]
	v_mfma_f32_16x16x32_bf16 v[30:33], v[192:195], v[208:211], v[30:33]
	v_mfma_f32_16x16x32_bf16 v[18:21], v[174:177], v[216:219], v[18:21]
	v_mfma_f32_16x16x32_bf16 v[14:17], v[192:195], v[216:219], v[14:17]
	v_mfma_f32_16x16x32_bf16 v[6:9], v[174:177], v[224:227], v[6:9]
	v_mfma_f32_16x16x32_bf16 v[2:5], v[192:195], v[224:227], v[2:5]
	v_mfma_f32_16x16x32_bf16 v[50:53], v[188:191], v[204:207], v[50:53]
	v_mfma_f32_16x16x32_bf16 v[46:49], v[196:199], v[204:207], v[46:49]
	v_mfma_f32_16x16x32_bf16 v[34:37], v[188:191], v[212:215], v[34:37]
	v_mfma_f32_16x16x32_bf16 v[30:33], v[196:199], v[212:215], v[30:33]
	v_mfma_f32_16x16x32_bf16 v[18:21], v[188:191], v[220:223], v[18:21]
	v_mfma_f32_16x16x32_bf16 v[14:17], v[196:199], v[220:223], v[14:17]
	v_mfma_f32_16x16x32_bf16 v[6:9], v[188:191], v[228:231], v[6:9]
	v_mfma_f32_16x16x32_bf16 v[2:5], v[196:199], v[228:231], v[2:5]
	s_setprio 0
	s_barrier
	s_add_i32 s57, 0, 0x18000
	s_add_i32 s58, 0, 0x1c000
	v_add_u32_e32 v142, s57, v184
	v_add_u32_e32 v187, s58, v184
	ds_read_b128 v[122:125], v142
	ds_read_b128 v[126:129], v142 offset:1024
	ds_read_b128 v[134:137], v142 offset:2048
	ds_read_b128 v[142:145], v142 offset:3072
	ds_read_b128 v[174:177], v187
	ds_read_b128 v[188:191], v187 offset:1024
	ds_read_b128 v[192:195], v187 offset:2048
	ds_read_b128 v[196:199], v187 offset:3072
	s_add_u32 s24, s24, 0x40000
	s_addc_u32 s25, s25, 0
	s_mov_b32 m0, s41
	v_lshl_add_u64 v[234:235], s[24:25], 0, v[152:153]
	ds_read_b128 v[200:203], v186 offset:32768
	ds_read_b128 v[204:207], v186 offset:33792
	ds_read_b128 v[208:211], v186 offset:34816
	ds_read_b128 v[212:215], v186 offset:35840
	ds_read_b128 v[216:219], v186 offset:36864
	ds_read_b128 v[220:223], v186 offset:37888
	ds_read_b128 v[224:227], v186 offset:38912
	ds_read_b128 v[228:231], v186 offset:39936
	global_load_lds_dwordx4 v[234:235], off
	v_lshl_add_u64 v[234:235], s[24:25], 0, v[150:151]
	s_mov_b32 m0, s43
	s_nop 0
	global_load_lds_dwordx4 v[234:235], off
	s_waitcnt vmcnt(8)
	s_waitcnt lgkmcnt(0)
	v_mfma_f32_16x16x32_bf16 v[138:141], v[122:125], v[200:203], v[138:141]
	v_mfma_f32_16x16x32_bf16 v[130:133], v[134:137], v[200:203], v[130:133]
	v_mfma_f32_16x16x32_bf16 v[118:121], v[122:125], v[208:211], v[118:121]
	s_barrier
	s_setprio 1
	s_waitcnt lgkmcnt(0)
	v_mfma_f32_16x16x32_bf16 v[106:109], v[134:137], v[208:211], v[106:109]
	v_mfma_f32_16x16x32_bf16 v[102:105], v[122:125], v[216:219], v[102:105]
	v_mfma_f32_16x16x32_bf16 v[90:93], v[134:137], v[216:219], v[90:93]
	v_mfma_f32_16x16x32_bf16 v[86:89], v[122:125], v[224:227], v[86:89]
	v_mfma_f32_16x16x32_bf16 v[74:77], v[134:137], v[224:227], v[74:77]
	v_mfma_f32_16x16x32_bf16 v[138:141], v[126:129], v[204:207], v[138:141]
	v_mfma_f32_16x16x32_bf16 v[130:133], v[142:145], v[204:207], v[130:133]
	v_mfma_f32_16x16x32_bf16 v[118:121], v[126:129], v[212:215], v[118:121]
	v_mfma_f32_16x16x32_bf16 v[106:109], v[142:145], v[212:215], v[106:109]
	v_mfma_f32_16x16x32_bf16 v[102:105], v[126:129], v[220:223], v[102:105]
	v_mfma_f32_16x16x32_bf16 v[90:93], v[142:145], v[220:223], v[90:93]
	v_mfma_f32_16x16x32_bf16 v[86:89], v[126:129], v[228:231], v[86:89]
	v_mfma_f32_16x16x32_bf16 v[74:77], v[142:145], v[228:231], v[74:77]
	s_setprio 0
	s_setprio 1
	v_mfma_f32_16x16x32_bf16 v[114:117], v[174:177], v[200:203], v[114:117]
	v_mfma_f32_16x16x32_bf16 v[110:113], v[192:195], v[200:203], v[110:113]
	v_mfma_f32_16x16x32_bf16 v[98:101], v[174:177], v[208:211], v[98:101]
	v_mfma_f32_16x16x32_bf16 v[94:97], v[192:195], v[208:211], v[94:97]
	v_mfma_f32_16x16x32_bf16 v[82:85], v[174:177], v[216:219], v[82:85]
	v_mfma_f32_16x16x32_bf16 v[78:81], v[192:195], v[216:219], v[78:81]
	v_mfma_f32_16x16x32_bf16 v[70:73], v[174:177], v[224:227], v[70:73]
	v_mfma_f32_16x16x32_bf16 v[66:69], v[192:195], v[224:227], v[66:69]
	v_mfma_f32_16x16x32_bf16 v[114:117], v[188:191], v[204:207], v[114:117]
	v_mfma_f32_16x16x32_bf16 v[110:113], v[196:199], v[204:207], v[110:113]
	v_mfma_f32_16x16x32_bf16 v[98:101], v[188:191], v[212:215], v[98:101]
	v_mfma_f32_16x16x32_bf16 v[94:97], v[196:199], v[212:215], v[94:97]
	v_mfma_f32_16x16x32_bf16 v[82:85], v[188:191], v[220:223], v[82:85]
	v_mfma_f32_16x16x32_bf16 v[78:81], v[196:199], v[220:223], v[78:81]
	v_mfma_f32_16x16x32_bf16 v[70:73], v[188:191], v[228:231], v[70:73]
	v_mfma_f32_16x16x32_bf16 v[66:69], v[196:199], v[228:231], v[66:69]
	s_setprio 0
	s_barrier
; #define PG8_STAGE(bufoff, gbase, voff) do { _Pragma("unroll") for (int _i = 0; _i < 2; ++_i) \
;         __builtin_amdgcn_global_load_lds((const unsigned*)((const char*)(gbase) + (voff)[_i]), (PG8_LAS unsigned*)(lds + (bufoff) + ldsw + _i * 8192), 16, 0, 0); } while (0)
; #define PG8_LDA(dst, b, h) do { _Pragma("unroll") for (int m = 0; m < 4; ++m) _Pragma("unroll") for (int k = 0; k < 2; ++k) dst[m][k] = *(const PG8_LAS bf16x8*)(lds + PG8_SA(b, h) + aoff + m * 2048 + k * 1024); } while (0)
; #define PG8_MMA(ai, bj, At, Bt) do { __builtin_amdgcn_s_setprio(1); _Pragma("unroll") for (int m = 0; m < 4; ++m) _Pragma("unroll") for (int n = 0; n < 2; ++n) _Pragma("unroll") for (int k = 0; k < 2; ++k) \
;         acc[ai][bj][m][n] = __builtin_amdgcn_mfma_f32_16x16x32_bf16(Bt[n][k], At[m][k], acc[ai][bj][m][n], 0, 0, 0); __builtin_amdgcn_s_setprio(0); } while (0)
; #define PG8_WAIT_V(n) asm volatile("s_waitcnt vmcnt(" #n ")" ::: "memory")
; #define PG8_WAIT_L(n) asm volatile("s_waitcnt lgkmcnt(" #n ")" ::: "memory")
; #define PG8_BAR __builtin_amdgcn_s_barrier()
; #define PG8_SCHED __builtin_amdgcn_sched_barrier(0)
; template <class Epi, class Sched, bool ALIGN_EPI = false, bool SP2 = false, bool GATHER = false>
; __device__ __forceinline__ void gemm_phase(PG8_LAS unsigned char* lds, const Gemm g, const Sched& S, const Epi& E, int tid_in, const int* rowsrc = nullptr, PG8_LAS int* idx_lds = nullptr) {
;     ...
;             PG8_LDA(At, 1, 1); PG8_STAGE(PG8_SB(1, 0), b3, voffB); PG8_STAGE(PG8_SB(1, 1), b3 + hstep, voffB); PG8_STAGE(PG8_SA(1, 0), a3, PG8_OS(0));
;             PG8_WAIT_V(8); PG8_WAIT_L(0); PG8_BAR; PG8_MMA(1, 0, At, B0); PG8_MMA(1, 1, At, B1); PG8_BAR; PG8_SCHED;
;     ...
;         if constexpr (ALIGN_EPI) { if (wr == 0) PG8_BAR; }
	s_add_i32 s24, s57, s38
	v_lshl_add_u64 v[178:179], v[178:179], 0, s[10:11]
	s_mov_b32 m0, s24
	ds_read_b128 v[200:203], v186 offset:49152
	ds_read_b128 v[204:207], v186 offset:50176
	ds_read_b128 v[208:211], v186 offset:51200
	ds_read_b128 v[212:215], v186 offset:52224
	ds_read_b128 v[216:219], v186 offset:53248
	ds_read_b128 v[220:223], v186 offset:54272
	ds_read_b128 v[224:227], v186 offset:55296
	ds_read_b128 v[228:231], v186 offset:56320
	global_load_lds_dwordx4 v[178:179], off
	s_add_i32 m0, s24, 0x2000
	s_add_u32 s22, s22, 0x40080
	v_lshl_add_u64 v[178:179], v[180:181], 0, s[10:11]
	s_addc_u32 s23, s23, 0
	s_add_i32 s24, s58, s38
	global_load_lds_dwordx4 v[178:179], off
	v_lshl_add_u64 v[178:179], s[22:23], 0, v[0:1]
	s_mov_b32 m0, s24
	s_nop 0
	global_load_lds_dwordx4 v[178:179], off
	v_lshl_add_u64 v[178:179], s[22:23], 0, v[148:149]
	s_add_i32 m0, s24, 0x2000
	s_nop 0
	global_load_lds_dwordx4 v[178:179], off
	v_lshl_add_u64 v[178:179], v[182:183], 0, s[10:11]
	s_mov_b32 m0, s51
	s_nop 0
	global_load_lds_dwordx4 v[178:179], off
	v_lshl_add_u64 v[178:179], v[232:233], 0, s[10:11]
	s_mov_b32 m0, s52
	s_nop 0
	global_load_lds_dwordx4 v[178:179], off
	s_waitcnt vmcnt(8)
	s_waitcnt lgkmcnt(0)
	v_mfma_f32_16x16x32_bf16 v[62:65], v[122:125], v[200:203], v[62:65]
	v_mfma_f32_16x16x32_bf16 v[58:61], v[134:137], v[200:203], v[58:61]
	v_mfma_f32_16x16x32_bf16 v[54:57], v[122:125], v[208:211], v[54:57]
	s_barrier
	s_setprio 1
	s_waitcnt lgkmcnt(0)
	v_mfma_f32_16x16x32_bf16 v[42:45], v[134:137], v[208:211], v[42:45]
	v_mfma_f32_16x16x32_bf16 v[38:41], v[122:125], v[216:219], v[38:41]
	v_mfma_f32_16x16x32_bf16 v[26:29], v[134:137], v[216:219], v[26:29]
	v_mfma_f32_16x16x32_bf16 v[22:25], v[122:125], v[224:227], v[22:25]
	v_mfma_f32_16x16x32_bf16 v[10:13], v[134:137], v[224:227], v[10:13]
	v_mfma_f32_16x16x32_bf16 v[62:65], v[126:129], v[204:207], v[62:65]
	v_mfma_f32_16x16x32_bf16 v[58:61], v[142:145], v[204:207], v[58:61]
	v_mfma_f32_16x16x32_bf16 v[54:57], v[126:129], v[212:215], v[54:57]
	v_mfma_f32_16x16x32_bf16 v[42:45], v[142:145], v[212:215], v[42:45]
	v_mfma_f32_16x16x32_bf16 v[38:41], v[126:129], v[220:223], v[38:41]
	v_mfma_f32_16x16x32_bf16 v[26:29], v[142:145], v[220:223], v[26:29]
	v_mfma_f32_16x16x32_bf16 v[22:25], v[126:129], v[228:231], v[22:25]
	v_mfma_f32_16x16x32_bf16 v[10:13], v[142:145], v[228:231], v[10:13]
	s_setprio 0
	s_setprio 1
	v_mfma_f32_16x16x32_bf16 v[50:53], v[174:177], v[200:203], v[50:53]
	v_mfma_f32_16x16x32_bf16 v[46:49], v[192:195], v[200:203], v[46:49]
	v_mfma_f32_16x16x32_bf16 v[34:37], v[174:177], v[208:211], v[34:37]
	v_mfma_f32_16x16x32_bf16 v[30:33], v[192:195], v[208:211], v[30:33]
	v_mfma_f32_16x16x32_bf16 v[18:21], v[174:177], v[216:219], v[18:21]
	v_mfma_f32_16x16x32_bf16 v[14:17], v[192:195], v[216:219], v[14:17]
	v_mfma_f32_16x16x32_bf16 v[6:9], v[174:177], v[224:227], v[6:9]
	v_mfma_f32_16x16x32_bf16 v[2:5], v[192:195], v[224:227], v[2:5]
	v_mfma_f32_16x16x32_bf16 v[50:53], v[188:191], v[204:207], v[50:53]
	v_mfma_f32_16x16x32_bf16 v[46:49], v[196:199], v[204:207], v[46:49]
	v_mfma_f32_16x16x32_bf16 v[34:37], v[188:191], v[212:215], v[34:37]
	v_mfma_f32_16x16x32_bf16 v[30:33], v[196:199], v[212:215], v[30:33]
	v_mfma_f32_16x16x32_bf16 v[18:21], v[188:191], v[220:223], v[18:21]
	v_mfma_f32_16x16x32_bf16 v[14:17], v[196:199], v[220:223], v[14:17]
	v_mfma_f32_16x16x32_bf16 v[6:9], v[188:191], v[228:231], v[6:9]
	v_mfma_f32_16x16x32_bf16 v[2:5], v[196:199], v[228:231], v[2:5]
	s_setprio 0
	s_barrier
	s_add_i32 s56, s56, 2
	s_add_u32 s20, s20, 0x100
	s_addc_u32 s21, s21, 0
	s_add_u32 s54, s54, 0x100
	s_addc_u32 s55, s55, 0
	s_cmp_gt_u32 s56, 13
	s_cbranch_scc0 .LBB0_1618
	s_mov_b32 s97, 1
	s_and_b64 vcc, exec, s[4:5]
	s_cbranch_vccz .LBB0_1621
	s_barrier

.LBB0_1911:
	s_mov_b32 s97, 0
	v_readlane_b32 s4, v251, 10
	v_readlane_b32 s5, v251, 11
	s_cmp_ge_i32 s2, s4
	s_cselect_b64 s[0:1], -1, 0
	s_cmp_lt_i32 s2, s5
	s_cselect_b64 s[4:5], -1, 0
	s_and_b64 s[4:5], s[0:1], s[4:5]
	s_mov_b64 s[0:1], -1
	s_and_b64 vcc, exec, s[4:5]
	s_cbranch_vccnz .LBB0_1913
	v_readlane_b32 s0, v252, 37
	s_add_i32 s2, s0, 3
	s_mov_b64 s[0:1], 0

; #define PG8_STAGE(bufoff, gbase, voff) do { _Pragma("unroll") for (int _i = 0; _i < 2; ++_i) \
;         __builtin_amdgcn_global_load_lds((const unsigned*)((const char*)(gbase) + (voff)[_i]), (PG8_LAS unsigned*)(lds + (bufoff) + ldsw + _i * 8192), 16, 0, 0); } while (0)
; #define PG8_LDA(dst, b, h) do { _Pragma("unroll") for (int m = 0; m < 4; ++m) _Pragma("unroll") for (int k = 0; k < 2; ++k) dst[m][k] = *(const PG8_LAS bf16x8*)(lds + PG8_SA(b, h) + aoff + m * 2048 + k * 1024); } while (0)
; #define PG8_LDB(dst, b, h) do { _Pragma("unroll") for (int n = 0; n < 2; ++n) _Pragma("unroll") for (int k = 0; k < 2; ++k) dst[n][k] = *(const PG8_LAS bf16x8*)(lds + PG8_SB(b, h) + boff + n * 2048 + k * 1024); } while (0)
; #define PG8_SCHED __builtin_amdgcn_sched_barrier(0)
; template <class Epi, class Sched, bool ALIGN_EPI = false, bool SP2 = false, bool GATHER = false>
; __device__ __forceinline__ void gemm_phase(PG8_LAS unsigned char* lds, const Gemm g, const Sched& S, const Epi& E, int tid_in, const int* rowsrc = nullptr, PG8_LAS int* idx_lds = nullptr) {
;     ...
;             if constexpr (GATHER) {
; #pragma unroll
;                 for (int h_ = 0; h_ < 2; ++h_) { gS[h_][0] = last ? gN[h_][0] : gA[h_][0]; gS[h_][1] = last ? gN[h_][1] : gA[h_][1]; } }
;             const char* a1 = cA + (size_t)(t + 1) * kstep;
;             const char* a2 = last ? nA : cA + (size_t)(t + 2) * kstep; const char* b2 = last ? nB : cB + (size_t)(t + 2) * kstep;
;             const char* a3 = a2 + kstep; const char* b3 = b2 + kstep;
;             if (last && has_next) S.a_ready(nxt);
;             if constexpr (SP2) {
;             PG8_LDB(B0, 0, 0); PG8_LDB(B1, 0, 1); PG8_SCHED; PG8_LDA(At, 0, 0); PG8_STAGE(PG8_SA(1, 1), a1 + hstepA, PG8_OA(1));
.LBB0_1930:
	s_add_u32 s22, s27, s20
	s_addc_u32 s23, s28, s21
	s_add_u32 s24, s22, 0x9000100
	s_addc_u32 s25, s23, 0
	s_add_u32 s56, s53, s20
	s_addc_u32 s57, s54, s21
	s_add_i32 s58, 0, 0x10000
	s_cmpk_eq_i32 s20, 0x700
	s_cselect_b64 vcc, -1, 0
	s_and_b64 s[22:23], vcc, exec
	s_cselect_b32 s25, s1, s25
	s_cselect_b32 s24, s0, s24
	v_add_u32_e32 v141, s58, v153
	s_cselect_b32 s23, s15, s57
	s_cselect_b32 s22, s43, s56
	s_add_i32 s59, 0, 0x14000
	ds_read_b128 v[160:163], v141
	ds_read_b128 v[164:167], v141 offset:1024
	ds_read_b128 v[168:171], v141 offset:2048
	ds_read_b128 v[172:175], v141 offset:3072
	v_add_u32_e32 v141, s59, v153
	ds_read_b128 v[176:179], v141
	ds_read_b128 v[180:183], v141 offset:1024
	ds_read_b128 v[184:187], v141 offset:2048
	ds_read_b128 v[188:191], v141 offset:3072
	v_cndmask_b32_e32 v0, v134, v158, vcc
	v_cndmask_b32_e32 v224, v136, v157, vcc
	v_cndmask_b32_e32 v135, v138, v156, vcc
	v_cndmask_b32_e32 v139, v140, v155, vcc
	v_lshl_add_u64 v[226:227], v[144:145], 0, s[20:21]
	s_add_i32 m0, s45, 0xc000
	ds_read_b128 v[192:195], v154
	ds_read_b128 v[196:199], v154 offset:1024
	ds_read_b128 v[200:203], v154 offset:2048
	ds_read_b128 v[204:207], v154 offset:3072
	ds_read_b128 v[208:211], v154 offset:4096
	ds_read_b128 v[212:215], v154 offset:5120
	ds_read_b128 v[216:219], v154 offset:6144
	ds_read_b128 v[220:223], v154 offset:7168
	global_load_lds_dwordx4 v[226:227], off
	v_lshl_add_u64 v[226:227], v[142:143], 0, s[20:21]
	s_add_i32 m0, s45, 0xe000
	s_nop 0
	global_load_lds_dwordx4 v[226:227], off
	s_cmp_eq_u32 s97, 0
	s_cbranch_scc1 .Lew17_a
	s_waitcnt vmcnt(16)
	s_branch .Lew17_b

; #define PG8_STAGE(bufoff, gbase, voff) do { _Pragma("unroll") for (int _i = 0; _i < 2; ++_i) \
;         __builtin_amdgcn_global_load_lds((const unsigned*)((const char*)(gbase) + (voff)[_i]), (PG8_LAS unsigned*)(lds + (bufoff) + ldsw + _i * 8192), 16, 0, 0); } while (0)
; #define PG8_LDA(dst, b, h) do { _Pragma("unroll") for (int m = 0; m < 4; ++m) _Pragma("unroll") for (int k = 0; k < 2; ++k) dst[m][k] = *(const PG8_LAS bf16x8*)(lds + PG8_SA(b, h) + aoff + m * 2048 + k * 1024); } while (0)
; #define PG8_LDB(dst, b, h) do { _Pragma("unroll") for (int n = 0; n < 2; ++n) _Pragma("unroll") for (int k = 0; k < 2; ++k) dst[n][k] = *(const PG8_LAS bf16x8*)(lds + PG8_SB(b, h) + boff + n * 2048 + k * 1024); } while (0)
; #define PG8_MMA(ai, bj, At, Bt) do { __builtin_amdgcn_s_setprio(1); _Pragma("unroll") for (int m = 0; m < 4; ++m) _Pragma("unroll") for (int n = 0; n < 2; ++n) _Pragma("unroll") for (int k = 0; k < 2; ++k) \
;         acc[ai][bj][m][n] = __builtin_amdgcn_mfma_f32_16x16x32_bf16(Bt[n][k], At[m][k], acc[ai][bj][m][n], 0, 0, 0); __builtin_amdgcn_s_setprio(0); } while (0)
; #define PG8_WAIT_V(n) asm volatile("s_waitcnt vmcnt(" #n ")" ::: "memory")
; #define PG8_WAIT_L(n) asm volatile("s_waitcnt lgkmcnt(" #n ")" ::: "memory")
; #define PG8_BAR __builtin_amdgcn_s_barrier()
; #define PG8_SCHED __builtin_amdgcn_sched_barrier(0)
; template <class Epi, class Sched, bool ALIGN_EPI = false, bool SP2 = false, bool GATHER = false>
; __device__ __forceinline__ void gemm_phase(PG8_LAS unsigned char* lds, const Gemm g, const Sched& S, const Epi& E, int tid_in, const int* rowsrc = nullptr, PG8_LAS int* idx_lds = nullptr) {
;     ...
;             PG8_LDB(B0, 0, 0); PG8_LDB(B1, 0, 1); PG8_SCHED; PG8_LDA(At, 0, 0); PG8_STAGE(PG8_SA(1, 1), a1 + hstepA, PG8_OA(1));
;             PG8_WAIT_V(8); PG8_WAIT_L(0); PG8_BAR; PG8_MMA(0, 0, At, B0); PG8_MMA(0, 1, At, B1); PG8_BAR; PG8_SCHED;
;             PG8_LDA(At, 0, 1); PG8_STAGE(PG8_SB(0, 0), b2, voffB); PG8_STAGE(PG8_SB(0, 1), b2 + hstep, voffB); PG8_STAGE(PG8_SA(0, 0), a2, PG8_OS(0));
.Lew17_b:
	s_waitcnt lgkmcnt(0)
	v_mfma_f32_16x16x32_bf16 v[126:129], v[160:163], v[192:195], v[126:129]
	v_mfma_f32_16x16x32_bf16 v[118:121], v[168:171], v[192:195], v[118:121]
	v_mfma_f32_16x16x32_bf16 v[110:113], v[160:163], v[200:203], v[110:113]
	s_barrier
	s_setprio 1
	s_waitcnt lgkmcnt(0)
	v_mfma_f32_16x16x32_bf16 v[102:105], v[168:171], v[200:203], v[102:105]
	v_mfma_f32_16x16x32_bf16 v[94:97], v[160:163], v[208:211], v[94:97]
	v_mfma_f32_16x16x32_bf16 v[86:89], v[168:171], v[208:211], v[86:89]
	v_mfma_f32_16x16x32_bf16 v[78:81], v[160:163], v[216:219], v[78:81]
	v_mfma_f32_16x16x32_bf16 v[70:73], v[168:171], v[216:219], v[70:73]
	v_mfma_f32_16x16x32_bf16 v[126:129], v[164:167], v[196:199], v[126:129]
	v_mfma_f32_16x16x32_bf16 v[118:121], v[172:175], v[196:199], v[118:121]
	v_mfma_f32_16x16x32_bf16 v[110:113], v[164:167], v[204:207], v[110:113]
	v_mfma_f32_16x16x32_bf16 v[102:105], v[172:175], v[204:207], v[102:105]
	v_mfma_f32_16x16x32_bf16 v[94:97], v[164:167], v[212:215], v[94:97]
	v_mfma_f32_16x16x32_bf16 v[86:89], v[172:175], v[212:215], v[86:89]
	v_mfma_f32_16x16x32_bf16 v[78:81], v[164:167], v[220:223], v[78:81]
	v_mfma_f32_16x16x32_bf16 v[70:73], v[172:175], v[220:223], v[70:73]
	s_setprio 0
	s_setprio 1
	v_mfma_f32_16x16x32_bf16 v[122:125], v[176:179], v[192:195], v[122:125]
	v_mfma_f32_16x16x32_bf16 v[114:117], v[184:187], v[192:195], v[114:117]
	v_mfma_f32_16x16x32_bf16 v[106:109], v[176:179], v[200:203], v[106:109]
	v_mfma_f32_16x16x32_bf16 v[98:101], v[184:187], v[200:203], v[98:101]
	v_mfma_f32_16x16x32_bf16 v[90:93], v[176:179], v[208:211], v[90:93]
	v_mfma_f32_16x16x32_bf16 v[82:85], v[184:187], v[208:211], v[82:85]
	v_mfma_f32_16x16x32_bf16 v[74:77], v[176:179], v[216:219], v[74:77]
	v_mfma_f32_16x16x32_bf16 v[66:69], v[184:187], v[216:219], v[66:69]
	v_mfma_f32_16x16x32_bf16 v[122:125], v[180:183], v[196:199], v[122:125]
	v_mfma_f32_16x16x32_bf16 v[114:117], v[188:191], v[196:199], v[114:117]
	v_mfma_f32_16x16x32_bf16 v[106:109], v[180:183], v[204:207], v[106:109]
	v_mfma_f32_16x16x32_bf16 v[98:101], v[188:191], v[204:207], v[98:101]
	v_mfma_f32_16x16x32_bf16 v[90:93], v[180:183], v[212:215], v[90:93]
	v_mfma_f32_16x16x32_bf16 v[82:85], v[188:191], v[212:215], v[82:85]
	v_mfma_f32_16x16x32_bf16 v[74:77], v[180:183], v[220:223], v[74:77]
	v_mfma_f32_16x16x32_bf16 v[66:69], v[188:191], v[220:223], v[66:69]
	s_setprio 0
	s_barrier
	s_add_i32 s56, s58, s36
	v_lshl_add_u64 v[226:227], s[22:23], 0, v[130:131]
	s_mov_b32 m0, s56
	ds_read_b128 v[192:195], v154 offset:16384
	ds_read_b128 v[196:199], v154 offset:17408
	ds_read_b128 v[200:203], v154 offset:18432
	ds_read_b128 v[204:207], v154 offset:19456
	ds_read_b128 v[208:211], v154 offset:20480
	ds_read_b128 v[212:215], v154 offset:21504
	ds_read_b128 v[216:219], v154 offset:22528
	ds_read_b128 v[220:223], v154 offset:23552
	global_load_lds_dwordx4 v[226:227], off
	s_add_i32 m0, s56, 0x2000
	s_add_u32 s56, s22, 0x40000
	v_lshl_add_u64 v[228:229], s[22:23], 0, v[132:133]
	s_addc_u32 s57, s23, 0
	s_add_i32 s58, s59, s36
	global_load_lds_dwordx4 v[228:229], off
	v_lshl_add_u64 v[230:231], s[56:57], 0, v[130:131]
	s_mov_b32 m0, s58
	v_mov_b32_e32 v225, v1
	global_load_lds_dwordx4 v[230:231], off
	v_lshl_add_u64 v[230:231], s[56:57], 0, v[132:133]
	s_add_i32 m0, s58, 0x2000
	s_nop 0
	global_load_lds_dwordx4 v[230:231], off
	s_mov_b32 m0, s45
	v_lshl_add_u64 v[230:231], s[24:25], 0, v[0:1]
	global_load_lds_dwordx4 v0, s[24:25]
	s_mov_b32 m0, s46
	s_nop 0
	global_load_lds_dwordx4 v224, s[24:25]
	s_cmp_eq_u32 s97, 0
	s_cbranch_scc1 .Lew18_a
	s_waitcnt vmcnt(16)
	s_branch .Lew18_b

; #define PG8_STAGE(bufoff, gbase, voff) do { _Pragma("unroll") for (int _i = 0; _i < 2; ++_i) \
;         __builtin_amdgcn_global_load_lds((const unsigned*)((const char*)(gbase) + (voff)[_i]), (PG8_LAS unsigned*)(lds + (bufoff) + ldsw + _i * 8192), 16, 0, 0); } while (0)
; #define PG8_LDA(dst, b, h) do { _Pragma("unroll") for (int m = 0; m < 4; ++m) _Pragma("unroll") for (int k = 0; k < 2; ++k) dst[m][k] = *(const PG8_LAS bf16x8*)(lds + PG8_SA(b, h) + aoff + m * 2048 + k * 1024); } while (0)
; #define PG8_LDB(dst, b, h) do { _Pragma("unroll") for (int n = 0; n < 2; ++n) _Pragma("unroll") for (int k = 0; k < 2; ++k) dst[n][k] = *(const PG8_LAS bf16x8*)(lds + PG8_SB(b, h) + boff + n * 2048 + k * 1024); } while (0)
; #define PG8_MMA(ai, bj, At, Bt) do { __builtin_amdgcn_s_setprio(1); _Pragma("unroll") for (int m = 0; m < 4; ++m) _Pragma("unroll") for (int n = 0; n < 2; ++n) _Pragma("unroll") for (int k = 0; k < 2; ++k) \
;         acc[ai][bj][m][n] = __builtin_amdgcn_mfma_f32_16x16x32_bf16(Bt[n][k], At[m][k], acc[ai][bj][m][n], 0, 0, 0); __builtin_amdgcn_s_setprio(0); } while (0)
; #define PG8_WAIT_V(n) asm volatile("s_waitcnt vmcnt(" #n ")" ::: "memory")
; #define PG8_WAIT_L(n) asm volatile("s_waitcnt lgkmcnt(" #n ")" ::: "memory")
; #define PG8_BAR __builtin_amdgcn_s_barrier()
; #define PG8_SCHED __builtin_amdgcn_sched_barrier(0)
; template <class Epi, class Sched, bool ALIGN_EPI = false, bool SP2 = false, bool GATHER = false>
; __device__ __forceinline__ void gemm_phase(PG8_LAS unsigned char* lds, const Gemm g, const Sched& S, const Epi& E, int tid_in, const int* rowsrc = nullptr, PG8_LAS int* idx_lds = nullptr) {
;     ...
;             PG8_WAIT_V(8); PG8_WAIT_L(0); PG8_BAR; PG8_MMA(1, 0, At, B0); PG8_MMA(1, 1, At, B1); PG8_BAR; PG8_SCHED;
;             PG8_LDB(B0, 1, 0); PG8_LDB(B1, 1, 1); PG8_SCHED; PG8_LDA(At, 1, 0); PG8_STAGE(PG8_SA(0, 1), a2 + hstepA, PG8_OS(1));
;             PG8_WAIT_V(8); PG8_WAIT_L(0); PG8_BAR; PG8_MMA(0, 0, At, B0); PG8_MMA(0, 1, At, B1); PG8_BAR; PG8_SCHED;
.Lew18_b:
	s_mov_b32 s97, 0
	s_waitcnt lgkmcnt(0)
	v_lshl_add_u64 v[224:225], s[24:25], 0, v[224:225]
	s_barrier
	s_setprio 1
	s_waitcnt lgkmcnt(0)
	v_mfma_f32_16x16x32_bf16 v[62:65], v[160:163], v[192:195], v[62:65]
	v_mfma_f32_16x16x32_bf16 v[54:57], v[168:171], v[192:195], v[54:57]
	v_mfma_f32_16x16x32_bf16 v[46:49], v[160:163], v[200:203], v[46:49]
	v_mfma_f32_16x16x32_bf16 v[38:41], v[168:171], v[200:203], v[38:41]
	v_mfma_f32_16x16x32_bf16 v[30:33], v[160:163], v[208:211], v[30:33]
	v_mfma_f32_16x16x32_bf16 v[22:25], v[168:171], v[208:211], v[22:25]
	v_mfma_f32_16x16x32_bf16 v[14:17], v[160:163], v[216:219], v[14:17]
	v_mfma_f32_16x16x32_bf16 v[6:9], v[168:171], v[216:219], v[6:9]
	v_mfma_f32_16x16x32_bf16 v[62:65], v[164:167], v[196:199], v[62:65]
	v_mfma_f32_16x16x32_bf16 v[54:57], v[172:175], v[196:199], v[54:57]
	v_mfma_f32_16x16x32_bf16 v[46:49], v[164:167], v[204:207], v[46:49]
	v_mfma_f32_16x16x32_bf16 v[38:41], v[172:175], v[204:207], v[38:41]
	v_mfma_f32_16x16x32_bf16 v[30:33], v[164:167], v[212:215], v[30:33]
	v_mfma_f32_16x16x32_bf16 v[22:25], v[172:175], v[212:215], v[22:25]
	v_mfma_f32_16x16x32_bf16 v[14:17], v[164:167], v[220:223], v[14:17]
	v_mfma_f32_16x16x32_bf16 v[6:9], v[172:175], v[220:223], v[6:9]
	s_setprio 0
	s_setprio 1
	v_mfma_f32_16x16x32_bf16 v[58:61], v[176:179], v[192:195], v[58:61]
	v_mfma_f32_16x16x32_bf16 v[50:53], v[184:187], v[192:195], v[50:53]
	v_mfma_f32_16x16x32_bf16 v[42:45], v[176:179], v[200:203], v[42:45]
	v_mfma_f32_16x16x32_bf16 v[34:37], v[184:187], v[200:203], v[34:37]
	v_mfma_f32_16x16x32_bf16 v[26:29], v[176:179], v[208:211], v[26:29]
	v_mfma_f32_16x16x32_bf16 v[18:21], v[184:187], v[208:211], v[18:21]
	v_mfma_f32_16x16x32_bf16 v[10:13], v[176:179], v[216:219], v[10:13]
	v_mfma_f32_16x16x32_bf16 v[2:5], v[184:187], v[216:219], v[2:5]
	v_mfma_f32_16x16x32_bf16 v[58:61], v[180:183], v[196:199], v[58:61]
	v_mfma_f32_16x16x32_bf16 v[50:53], v[188:191], v[196:199], v[50:53]
	v_mfma_f32_16x16x32_bf16 v[42:45], v[180:183], v[204:207], v[42:45]
	v_mfma_f32_16x16x32_bf16 v[34:37], v[188:191], v[204:207], v[34:37]
	v_mfma_f32_16x16x32_bf16 v[26:29], v[180:183], v[212:215], v[26:29]
	v_mfma_f32_16x16x32_bf16 v[18:21], v[188:191], v[212:215], v[18:21]
	v_mfma_f32_16x16x32_bf16 v[10:13], v[180:183], v[220:223], v[10:13]
	v_mfma_f32_16x16x32_bf16 v[2:5], v[188:191], v[220:223], v[2:5]
	s_setprio 0
	s_barrier
	s_add_i32 s56, 0, 0x18000
	v_add_u32_e32 v0, s56, v153
	s_add_i32 s57, 0, 0x1c000
	ds_read_b128 v[160:163], v0
	ds_read_b128 v[164:167], v0 offset:1024
	ds_read_b128 v[168:171], v0 offset:2048
	ds_read_b128 v[172:175], v0 offset:3072
	v_add_u32_e32 v0, s57, v153
	ds_read_b128 v[176:179], v0
	ds_read_b128 v[180:183], v0 offset:1024
	ds_read_b128 v[184:187], v0 offset:2048
	ds_read_b128 v[188:191], v0 offset:3072
	s_mov_b32 m0, s47
	ds_read_b128 v[192:195], v154 offset:32768
	ds_read_b128 v[196:199], v154 offset:33792
	ds_read_b128 v[200:203], v154 offset:34816
	ds_read_b128 v[204:207], v154 offset:35840
	ds_read_b128 v[208:211], v154 offset:36864
	ds_read_b128 v[212:215], v154 offset:37888
	ds_read_b128 v[216:219], v154 offset:38912
	ds_read_b128 v[220:223], v154 offset:39936
	global_load_lds_dwordx4 v135, s[24:25]
	s_mov_b32 m0, s48
	s_nop 0
	global_load_lds_dwordx4 v139, s[24:25]
	s_waitcnt vmcnt(8)
	s_waitcnt lgkmcnt(0)
	v_mfma_f32_16x16x32_bf16 v[126:129], v[160:163], v[192:195], v[126:129]
	v_mfma_f32_16x16x32_bf16 v[118:121], v[168:171], v[192:195], v[118:121]
	v_mfma_f32_16x16x32_bf16 v[110:113], v[160:163], v[200:203], v[110:113]
	s_barrier
	s_setprio 1
	s_waitcnt lgkmcnt(0)
	v_mfma_f32_16x16x32_bf16 v[102:105], v[168:171], v[200:203], v[102:105]
	v_mfma_f32_16x16x32_bf16 v[94:97], v[160:163], v[208:211], v[94:97]
	v_mfma_f32_16x16x32_bf16 v[86:89], v[168:171], v[208:211], v[86:89]
	v_mfma_f32_16x16x32_bf16 v[78:81], v[160:163], v[216:219], v[78:81]
	v_mfma_f32_16x16x32_bf16 v[70:73], v[168:171], v[216:219], v[70:73]
	v_mfma_f32_16x16x32_bf16 v[126:129], v[164:167], v[196:199], v[126:129]
	v_mfma_f32_16x16x32_bf16 v[118:121], v[172:175], v[196:199], v[118:121]
	v_mfma_f32_16x16x32_bf16 v[110:113], v[164:167], v[204:207], v[110:113]
	v_mfma_f32_16x16x32_bf16 v[102:105], v[172:175], v[204:207], v[102:105]
	v_mfma_f32_16x16x32_bf16 v[94:97], v[164:167], v[212:215], v[94:97]
	v_mfma_f32_16x16x32_bf16 v[86:89], v[172:175], v[212:215], v[86:89]
	v_mfma_f32_16x16x32_bf16 v[78:81], v[164:167], v[220:223], v[78:81]
	v_mfma_f32_16x16x32_bf16 v[70:73], v[172:175], v[220:223], v[70:73]
	s_setprio 0
	s_setprio 1
	v_mfma_f32_16x16x32_bf16 v[122:125], v[176:179], v[192:195], v[122:125]
	v_mfma_f32_16x16x32_bf16 v[114:117], v[184:187], v[192:195], v[114:117]
	v_mfma_f32_16x16x32_bf16 v[106:109], v[176:179], v[200:203], v[106:109]
	v_mfma_f32_16x16x32_bf16 v[98:101], v[184:187], v[200:203], v[98:101]
	v_mfma_f32_16x16x32_bf16 v[90:93], v[176:179], v[208:211], v[90:93]
	v_mfma_f32_16x16x32_bf16 v[82:85], v[184:187], v[208:211], v[82:85]
	v_mfma_f32_16x16x32_bf16 v[74:77], v[176:179], v[216:219], v[74:77]
	v_mfma_f32_16x16x32_bf16 v[66:69], v[184:187], v[216:219], v[66:69]
	v_mfma_f32_16x16x32_bf16 v[122:125], v[180:183], v[196:199], v[122:125]
	v_mfma_f32_16x16x32_bf16 v[114:117], v[188:191], v[196:199], v[114:117]
	v_mfma_f32_16x16x32_bf16 v[106:109], v[180:183], v[204:207], v[106:109]
	v_mfma_f32_16x16x32_bf16 v[98:101], v[188:191], v[204:207], v[98:101]
	v_mfma_f32_16x16x32_bf16 v[90:93], v[180:183], v[212:215], v[90:93]
	v_mfma_f32_16x16x32_bf16 v[82:85], v[188:191], v[212:215], v[82:85]
	v_mfma_f32_16x16x32_bf16 v[74:77], v[180:183], v[220:223], v[74:77]
	v_mfma_f32_16x16x32_bf16 v[66:69], v[188:191], v[220:223], v[66:69]
	s_setprio 0
	s_barrier
; #define PG8_STAGE(bufoff, gbase, voff) do { _Pragma("unroll") for (int _i = 0; _i < 2; ++_i) \
;         __builtin_amdgcn_global_load_lds((const unsigned*)((const char*)(gbase) + (voff)[_i]), (PG8_LAS unsigned*)(lds + (bufoff) + ldsw + _i * 8192), 16, 0, 0); } while (0)
; #define PG8_LDA(dst, b, h) do { _Pragma("unroll") for (int m = 0; m < 4; ++m) _Pragma("unroll") for (int k = 0; k < 2; ++k) dst[m][k] = *(const PG8_LAS bf16x8*)(lds + PG8_SA(b, h) + aoff + m * 2048 + k * 1024); } while (0)
; #define PG8_MMA(ai, bj, At, Bt) do { __builtin_amdgcn_s_setprio(1); _Pragma("unroll") for (int m = 0; m < 4; ++m) _Pragma("unroll") for (int n = 0; n < 2; ++n) _Pragma("unroll") for (int k = 0; k < 2; ++k) \
;         acc[ai][bj][m][n] = __builtin_amdgcn_mfma_f32_16x16x32_bf16(Bt[n][k], At[m][k], acc[ai][bj][m][n], 0, 0, 0); __builtin_amdgcn_s_setprio(0); } while (0)
; #define PG8_WAIT_V(n) asm volatile("s_waitcnt vmcnt(" #n ")" ::: "memory")
; #define PG8_WAIT_L(n) asm volatile("s_waitcnt lgkmcnt(" #n ")" ::: "memory")
; #define PG8_BAR __builtin_amdgcn_s_barrier()
; #define PG8_SCHED __builtin_amdgcn_sched_barrier(0)
; template <class Epi, class Sched, bool ALIGN_EPI = false, bool SP2 = false, bool GATHER = false>
; __device__ __forceinline__ void gemm_phase(PG8_LAS unsigned char* lds, const Gemm g, const Sched& S, const Epi& E, int tid_in, const int* rowsrc = nullptr, PG8_LAS int* idx_lds = nullptr) {
;     ...
;             PG8_LDA(At, 1, 1); PG8_STAGE(PG8_SB(1, 0), b3, voffB); PG8_STAGE(PG8_SB(1, 1), b3 + hstep, voffB); PG8_STAGE(PG8_SA(1, 0), a3, PG8_OS(0));
;             PG8_WAIT_V(8); PG8_WAIT_L(0); PG8_BAR; PG8_MMA(1, 0, At, B0); PG8_MMA(1, 1, At, B1); PG8_BAR; PG8_SCHED;
;     ...
;         if constexpr (ALIGN_EPI) { if (wr == 0) PG8_BAR; }
	s_add_i32 s24, s56, s36
	v_lshl_add_u64 v[226:227], v[226:227], 0, s[10:11]
	s_mov_b32 m0, s24
	ds_read_b128 v[192:195], v154 offset:49152
	ds_read_b128 v[196:199], v154 offset:50176
	ds_read_b128 v[200:203], v154 offset:51200
	ds_read_b128 v[204:207], v154 offset:52224
	ds_read_b128 v[208:211], v154 offset:53248
	ds_read_b128 v[212:215], v154 offset:54272
	ds_read_b128 v[216:219], v154 offset:55296
	ds_read_b128 v[220:223], v154 offset:56320
	global_load_lds_dwordx4 v[226:227], off
	s_add_i32 m0, s24, 0x2000
	s_add_u32 s22, s22, 0x40080
	v_lshl_add_u64 v[226:227], v[228:229], 0, s[10:11]
	s_addc_u32 s23, s23, 0
	s_add_i32 s24, s57, s36
	global_load_lds_dwordx4 v[226:227], off
	v_lshl_add_u64 v[226:227], s[22:23], 0, v[130:131]
	s_mov_b32 m0, s24
	v_lshl_add_u64 v[224:225], v[224:225], 0, s[10:11]
	global_load_lds_dwordx4 v[226:227], off
	v_lshl_add_u64 v[226:227], s[22:23], 0, v[132:133]
	s_add_i32 m0, s24, 0x2000
	s_nop 0
	global_load_lds_dwordx4 v[226:227], off
	v_lshl_add_u64 v[226:227], v[230:231], 0, s[10:11]
	s_mov_b32 m0, s49
	s_nop 0
	global_load_lds_dwordx4 v[226:227], off
	s_mov_b32 m0, s50
	s_nop 0
	global_load_lds_dwordx4 v[224:225], off
	s_waitcnt vmcnt(8)
	s_waitcnt lgkmcnt(0)
	v_mfma_f32_16x16x32_bf16 v[62:65], v[160:163], v[192:195], v[62:65]
	v_mfma_f32_16x16x32_bf16 v[54:57], v[168:171], v[192:195], v[54:57]
	v_mfma_f32_16x16x32_bf16 v[46:49], v[160:163], v[200:203], v[46:49]
	s_barrier
	s_setprio 1
	s_waitcnt lgkmcnt(0)
	v_mfma_f32_16x16x32_bf16 v[38:41], v[168:171], v[200:203], v[38:41]
	v_mfma_f32_16x16x32_bf16 v[30:33], v[160:163], v[208:211], v[30:33]
	v_mfma_f32_16x16x32_bf16 v[22:25], v[168:171], v[208:211], v[22:25]
	v_mfma_f32_16x16x32_bf16 v[14:17], v[160:163], v[216:219], v[14:17]
	v_mfma_f32_16x16x32_bf16 v[6:9], v[168:171], v[216:219], v[6:9]
	v_mfma_f32_16x16x32_bf16 v[62:65], v[164:167], v[196:199], v[62:65]
	v_mfma_f32_16x16x32_bf16 v[54:57], v[172:175], v[196:199], v[54:57]
	v_mfma_f32_16x16x32_bf16 v[46:49], v[164:167], v[204:207], v[46:49]
	v_mfma_f32_16x16x32_bf16 v[38:41], v[172:175], v[204:207], v[38:41]
	v_mfma_f32_16x16x32_bf16 v[30:33], v[164:167], v[212:215], v[30:33]
	v_mfma_f32_16x16x32_bf16 v[22:25], v[172:175], v[212:215], v[22:25]
	v_mfma_f32_16x16x32_bf16 v[14:17], v[164:167], v[220:223], v[14:17]
	v_mfma_f32_16x16x32_bf16 v[6:9], v[172:175], v[220:223], v[6:9]
	s_setprio 0
	s_setprio 1
	v_mfma_f32_16x16x32_bf16 v[58:61], v[176:179], v[192:195], v[58:61]
	v_mfma_f32_16x16x32_bf16 v[50:53], v[184:187], v[192:195], v[50:53]
	v_mfma_f32_16x16x32_bf16 v[42:45], v[176:179], v[200:203], v[42:45]
	v_mfma_f32_16x16x32_bf16 v[34:37], v[184:187], v[200:203], v[34:37]
	v_mfma_f32_16x16x32_bf16 v[26:29], v[176:179], v[208:211], v[26:29]
	v_mfma_f32_16x16x32_bf16 v[18:21], v[184:187], v[208:211], v[18:21]
	v_mfma_f32_16x16x32_bf16 v[10:13], v[176:179], v[216:219], v[10:13]
	v_mfma_f32_16x16x32_bf16 v[2:5], v[184:187], v[216:219], v[2:5]
	v_mfma_f32_16x16x32_bf16 v[58:61], v[180:183], v[196:199], v[58:61]
	v_mfma_f32_16x16x32_bf16 v[50:53], v[188:191], v[196:199], v[50:53]
	v_mfma_f32_16x16x32_bf16 v[42:45], v[180:183], v[204:207], v[42:45]
	v_mfma_f32_16x16x32_bf16 v[34:37], v[188:191], v[204:207], v[34:37]
	v_mfma_f32_16x16x32_bf16 v[26:29], v[180:183], v[212:215], v[26:29]
	v_mfma_f32_16x16x32_bf16 v[18:21], v[188:191], v[212:215], v[18:21]
	v_mfma_f32_16x16x32_bf16 v[10:13], v[180:183], v[220:223], v[10:13]
	v_mfma_f32_16x16x32_bf16 v[2:5], v[188:191], v[220:223], v[2:5]
	s_setprio 0
	s_barrier
	s_add_i32 s55, s55, 2
	s_add_u32 s20, s20, 0x100
	s_addc_u32 s21, s21, 0
	s_cmp_gt_u32 s55, 13
	s_cbranch_scc0 .LBB0_1930
	s_mov_b32 s97, 1
	s_and_b64 vcc, exec, s[8:9]
	s_cbranch_vccz .LBB0_1933
	s_barrier

.LBB0_1993:
	s_mov_b32 s97, 0
	v_readlane_b32 s4, v251, 10
	v_readlane_b32 s5, v251, 11
	s_cmp_ge_i32 s2, s4
	s_cselect_b64 s[0:1], -1, 0
	s_cmp_lt_i32 s2, s5
	s_cselect_b64 s[4:5], -1, 0
	s_and_b64 s[4:5], s[0:1], s[4:5]
	s_mov_b64 s[0:1], -1
	s_and_b64 vcc, exec, s[4:5]
	s_cbranch_vccnz .LBB0_1995
	v_readlane_b32 s0, v252, 37
	s_add_i32 s44, s0, 4
	s_mov_b64 s[0:1], 0

; #define PG8_STAGE(bufoff, gbase, voff) do { _Pragma("unroll") for (int _i = 0; _i < 2; ++_i) \
;         __builtin_amdgcn_global_load_lds((const unsigned*)((const char*)(gbase) + (voff)[_i]), (PG8_LAS unsigned*)(lds + (bufoff) + ldsw + _i * 8192), 16, 0, 0); } while (0)
; #define PG8_LDA(dst, b, h) do { _Pragma("unroll") for (int m = 0; m < 4; ++m) _Pragma("unroll") for (int k = 0; k < 2; ++k) dst[m][k] = *(const PG8_LAS bf16x8*)(lds + PG8_SA(b, h) + aoff + m * 2048 + k * 1024); } while (0)
; #define PG8_LDB(dst, b, h) do { _Pragma("unroll") for (int n = 0; n < 2; ++n) _Pragma("unroll") for (int k = 0; k < 2; ++k) dst[n][k] = *(const PG8_LAS bf16x8*)(lds + PG8_SB(b, h) + boff + n * 2048 + k * 1024); } while (0)
; #define PG8_SCHED __builtin_amdgcn_sched_barrier(0)
; template <class Epi, class Sched, bool ALIGN_EPI = false, bool SP2 = false, bool GATHER = false>
; __device__ __forceinline__ void gemm_phase(PG8_LAS unsigned char* lds, const Gemm g, const Sched& S, const Epi& E, int tid_in, const int* rowsrc = nullptr, PG8_LAS int* idx_lds = nullptr) {
;     ...
;         for (int t = 0; t < nt; t += 2) {
;             const bool last = (t == nt - 2);
;             if constexpr (GATHER) {
; #pragma unroll
;                 for (int h_ = 0; h_ < 2; ++h_) { gS[h_][0] = last ? gN[h_][0] : gA[h_][0]; gS[h_][1] = last ? gN[h_][1] : gA[h_][1]; } }
;             const char* a1 = cA + (size_t)(t + 1) * kstep;
;             const char* a2 = last ? nA : cA + (size_t)(t + 2) * kstep; const char* b2 = last ? nB : cB + (size_t)(t + 2) * kstep;
;             const char* a3 = a2 + kstep; const char* b3 = b2 + kstep;
;             if (last && has_next) S.a_ready(nxt);
;             if constexpr (SP2) {
;             PG8_LDB(B0, 0, 0); PG8_LDB(B1, 0, 1); PG8_SCHED; PG8_LDA(At, 0, 0); PG8_STAGE(PG8_SA(1, 1), a1 + hstepA, PG8_OA(1));
.LBB0_2005:
	s_add_u32 s28, s26, 0xfffc0080
	s_addc_u32 s29, s27, -1
	s_add_i32 s58, 0, 0x10000
	s_cmp_eq_u32 s57, 12
	s_cselect_b32 s31, s13, s29
	s_cselect_b32 s30, s23, s28
	v_add_u32_e32 v0, s58, v151
	s_cselect_b32 s29, s15, s56
	s_cselect_b32 s28, s43, s55
	s_add_i32 s60, 0, 0x14000
	ds_read_b128 v[142:145], v0
	ds_read_b128 v[154:157], v0 offset:1024
	ds_read_b128 v[158:161], v0 offset:2048
	ds_read_b128 v[162:165], v0 offset:3072
	v_add_u32_e32 v0, s60, v151
	ds_read_b128 v[166:169], v0
	ds_read_b128 v[170:173], v0 offset:1024
	ds_read_b128 v[174:177], v0 offset:2048
	ds_read_b128 v[178:181], v0 offset:3072
	v_lshl_add_u64 v[148:149], s[26:27], 0, v[138:139]
	s_add_i32 m0, s25, 0xc000
	ds_read_b128 v[182:185], v153
	ds_read_b128 v[186:189], v153 offset:1024
	ds_read_b128 v[190:193], v153 offset:2048
	ds_read_b128 v[194:197], v153 offset:3072
	ds_read_b128 v[198:201], v153 offset:4096
	ds_read_b128 v[202:205], v153 offset:5120
	ds_read_b128 v[206:209], v153 offset:6144
	ds_read_b128 v[210:213], v153 offset:7168
	global_load_lds_dwordx4 v[148:149], off
	v_lshl_add_u64 v[148:149], s[26:27], 0, v[140:141]
	s_add_i32 m0, s25, 0xe000
	s_nop 0
	global_load_lds_dwordx4 v[148:149], off
	s_cmp_eq_u32 s97, 0
	s_cbranch_scc1 .Lew19_a
	s_waitcnt vmcnt(24)
	s_branch .Lew19_b

; #define PG8_STAGE(bufoff, gbase, voff) do { _Pragma("unroll") for (int _i = 0; _i < 2; ++_i) \
;         __builtin_amdgcn_global_load_lds((const unsigned*)((const char*)(gbase) + (voff)[_i]), (PG8_LAS unsigned*)(lds + (bufoff) + ldsw + _i * 8192), 16, 0, 0); } while (0)
; #define PG8_LDA(dst, b, h) do { _Pragma("unroll") for (int m = 0; m < 4; ++m) _Pragma("unroll") for (int k = 0; k < 2; ++k) dst[m][k] = *(const PG8_LAS bf16x8*)(lds + PG8_SA(b, h) + aoff + m * 2048 + k * 1024); } while (0)
; #define PG8_LDB(dst, b, h) do { _Pragma("unroll") for (int n = 0; n < 2; ++n) _Pragma("unroll") for (int k = 0; k < 2; ++k) dst[n][k] = *(const PG8_LAS bf16x8*)(lds + PG8_SB(b, h) + boff + n * 2048 + k * 1024); } while (0)
; #define PG8_MMA(ai, bj, At, Bt) do { __builtin_amdgcn_s_setprio(1); _Pragma("unroll") for (int m = 0; m < 4; ++m) _Pragma("unroll") for (int n = 0; n < 2; ++n) _Pragma("unroll") for (int k = 0; k < 2; ++k) \
;         acc[ai][bj][m][n] = __builtin_amdgcn_mfma_f32_16x16x32_bf16(Bt[n][k], At[m][k], acc[ai][bj][m][n], 0, 0, 0); __builtin_amdgcn_s_setprio(0); } while (0)
; #define PG8_WAIT_V(n) asm volatile("s_waitcnt vmcnt(" #n ")" ::: "memory")
; #define PG8_WAIT_L(n) asm volatile("s_waitcnt lgkmcnt(" #n ")" ::: "memory")
; #define PG8_BAR __builtin_amdgcn_s_barrier()
; #define PG8_SCHED __builtin_amdgcn_sched_barrier(0)
; template <class Epi, class Sched, bool ALIGN_EPI = false, bool SP2 = false, bool GATHER = false>
; __device__ __forceinline__ void gemm_phase(PG8_LAS unsigned char* lds, const Gemm g, const Sched& S, const Epi& E, int tid_in, const int* rowsrc = nullptr, PG8_LAS int* idx_lds = nullptr) {
;     ...
;             PG8_LDB(B0, 0, 0); PG8_LDB(B1, 0, 1); PG8_SCHED; PG8_LDA(At, 0, 0); PG8_STAGE(PG8_SA(1, 1), a1 + hstepA, PG8_OA(1));
;             PG8_WAIT_V(8); PG8_WAIT_L(0); PG8_BAR; PG8_MMA(0, 0, At, B0); PG8_MMA(0, 1, At, B1); PG8_BAR; PG8_SCHED;
;             PG8_LDA(At, 0, 1); PG8_STAGE(PG8_SB(0, 0), b2, voffB); PG8_STAGE(PG8_SB(0, 1), b2 + hstep, voffB); PG8_STAGE(PG8_SA(0, 0), a2, PG8_OS(0));
.Lew19_b:
	s_waitcnt lgkmcnt(0)
	v_mfma_f32_16x16x32_bf16 v[126:129], v[142:145], v[182:185], v[126:129]
	v_mfma_f32_16x16x32_bf16 v[122:125], v[158:161], v[182:185], v[122:125]
	v_mfma_f32_16x16x32_bf16 v[110:113], v[142:145], v[190:193], v[110:113]
	s_barrier
	s_setprio 1
	s_waitcnt lgkmcnt(0)
	v_mfma_f32_16x16x32_bf16 v[106:109], v[158:161], v[190:193], v[106:109]
	v_mfma_f32_16x16x32_bf16 v[94:97], v[142:145], v[198:201], v[94:97]
	v_mfma_f32_16x16x32_bf16 v[90:93], v[158:161], v[198:201], v[90:93]
	v_mfma_f32_16x16x32_bf16 v[78:81], v[142:145], v[206:209], v[78:81]
	v_mfma_f32_16x16x32_bf16 v[74:77], v[158:161], v[206:209], v[74:77]
	v_mfma_f32_16x16x32_bf16 v[126:129], v[154:157], v[186:189], v[126:129]
	v_mfma_f32_16x16x32_bf16 v[122:125], v[162:165], v[186:189], v[122:125]
	v_mfma_f32_16x16x32_bf16 v[110:113], v[154:157], v[194:197], v[110:113]
	v_mfma_f32_16x16x32_bf16 v[106:109], v[162:165], v[194:197], v[106:109]
	v_mfma_f32_16x16x32_bf16 v[94:97], v[154:157], v[202:205], v[94:97]
	v_mfma_f32_16x16x32_bf16 v[90:93], v[162:165], v[202:205], v[90:93]
	v_mfma_f32_16x16x32_bf16 v[78:81], v[154:157], v[210:213], v[78:81]
	v_mfma_f32_16x16x32_bf16 v[74:77], v[162:165], v[210:213], v[74:77]
	s_setprio 0
	s_setprio 1
	v_mfma_f32_16x16x32_bf16 v[118:121], v[166:169], v[182:185], v[118:121]
	v_mfma_f32_16x16x32_bf16 v[114:117], v[174:177], v[182:185], v[114:117]
	v_mfma_f32_16x16x32_bf16 v[102:105], v[166:169], v[190:193], v[102:105]
	v_mfma_f32_16x16x32_bf16 v[98:101], v[174:177], v[190:193], v[98:101]
	v_mfma_f32_16x16x32_bf16 v[86:89], v[166:169], v[198:201], v[86:89]
	v_mfma_f32_16x16x32_bf16 v[82:85], v[174:177], v[198:201], v[82:85]
	v_mfma_f32_16x16x32_bf16 v[70:73], v[166:169], v[206:209], v[70:73]
	v_mfma_f32_16x16x32_bf16 v[66:69], v[174:177], v[206:209], v[66:69]
	v_mfma_f32_16x16x32_bf16 v[118:121], v[170:173], v[186:189], v[118:121]
	v_mfma_f32_16x16x32_bf16 v[114:117], v[178:181], v[186:189], v[114:117]
	v_mfma_f32_16x16x32_bf16 v[102:105], v[170:173], v[194:197], v[102:105]
	v_mfma_f32_16x16x32_bf16 v[98:101], v[178:181], v[194:197], v[98:101]
	v_mfma_f32_16x16x32_bf16 v[86:89], v[170:173], v[202:205], v[86:89]
	v_mfma_f32_16x16x32_bf16 v[82:85], v[178:181], v[202:205], v[82:85]
	v_mfma_f32_16x16x32_bf16 v[70:73], v[170:173], v[210:213], v[70:73]
	v_mfma_f32_16x16x32_bf16 v[66:69], v[178:181], v[210:213], v[66:69]
	s_setprio 0
	s_barrier
	s_add_i32 s58, s58, s44
	v_lshl_add_u64 v[148:149], s[28:29], 0, v[134:135]
	s_mov_b32 m0, s58
	ds_read_b128 v[182:185], v153 offset:16384
	ds_read_b128 v[186:189], v153 offset:17408
	ds_read_b128 v[190:193], v153 offset:18432
	ds_read_b128 v[194:197], v153 offset:19456
	ds_read_b128 v[198:201], v153 offset:20480
	ds_read_b128 v[202:205], v153 offset:21504
	ds_read_b128 v[206:209], v153 offset:22528
	ds_read_b128 v[210:213], v153 offset:23552
	global_load_lds_dwordx4 v[148:149], off
	s_add_i32 m0, s58, 0x2000
	s_add_u32 s58, s28, 0x40000
	v_lshl_add_u64 v[214:215], s[28:29], 0, v[130:131]
	s_addc_u32 s59, s29, 0
	s_add_i32 s60, s60, s44
	global_load_lds_dwordx4 v[214:215], off
	v_lshl_add_u64 v[216:217], s[58:59], 0, v[134:135]
	s_mov_b32 m0, s60
	v_lshl_add_u64 v[218:219], s[30:31], 0, v[132:133]
	global_load_lds_dwordx4 v[216:217], off
	v_lshl_add_u64 v[216:217], s[58:59], 0, v[130:131]
	s_add_i32 m0, s60, 0x2000
	s_nop 0
	global_load_lds_dwordx4 v[216:217], off
	v_lshl_add_u64 v[216:217], s[30:31], 0, v[136:137]
	s_mov_b32 m0, s25
	s_nop 0
	global_load_lds_dwordx4 v[216:217], off
	s_mov_b32 m0, s48
	s_nop 0
	global_load_lds_dwordx4 v[218:219], off
	s_cmp_eq_u32 s97, 0
	s_cbranch_scc1 .Lew20_a
	s_waitcnt vmcnt(24)
	s_branch .Lew20_b

; #define PG8_STAGE(bufoff, gbase, voff) do { _Pragma("unroll") for (int _i = 0; _i < 2; ++_i) \
;         __builtin_amdgcn_global_load_lds((const unsigned*)((const char*)(gbase) + (voff)[_i]), (PG8_LAS unsigned*)(lds + (bufoff) + ldsw + _i * 8192), 16, 0, 0); } while (0)
; #define PG8_LDA(dst, b, h) do { _Pragma("unroll") for (int m = 0; m < 4; ++m) _Pragma("unroll") for (int k = 0; k < 2; ++k) dst[m][k] = *(const PG8_LAS bf16x8*)(lds + PG8_SA(b, h) + aoff + m * 2048 + k * 1024); } while (0)
; #define PG8_LDB(dst, b, h) do { _Pragma("unroll") for (int n = 0; n < 2; ++n) _Pragma("unroll") for (int k = 0; k < 2; ++k) dst[n][k] = *(const PG8_LAS bf16x8*)(lds + PG8_SB(b, h) + boff + n * 2048 + k * 1024); } while (0)
; #define PG8_MMA(ai, bj, At, Bt) do { __builtin_amdgcn_s_setprio(1); _Pragma("unroll") for (int m = 0; m < 4; ++m) _Pragma("unroll") for (int n = 0; n < 2; ++n) _Pragma("unroll") for (int k = 0; k < 2; ++k) \
;         acc[ai][bj][m][n] = __builtin_amdgcn_mfma_f32_16x16x32_bf16(Bt[n][k], At[m][k], acc[ai][bj][m][n], 0, 0, 0); __builtin_amdgcn_s_setprio(0); } while (0)
; #define PG8_WAIT_V(n) asm volatile("s_waitcnt vmcnt(" #n ")" ::: "memory")
; #define PG8_WAIT_L(n) asm volatile("s_waitcnt lgkmcnt(" #n ")" ::: "memory")
; #define PG8_BAR __builtin_amdgcn_s_barrier()
; #define PG8_SCHED __builtin_amdgcn_sched_barrier(0)
; template <class Epi, class Sched, bool ALIGN_EPI = false, bool SP2 = false, bool GATHER = false>
; __device__ __forceinline__ void gemm_phase(PG8_LAS unsigned char* lds, const Gemm g, const Sched& S, const Epi& E, int tid_in, const int* rowsrc = nullptr, PG8_LAS int* idx_lds = nullptr) {
;     ...
;             PG8_WAIT_V(8); PG8_WAIT_L(0); PG8_BAR; PG8_MMA(1, 0, At, B0); PG8_MMA(1, 1, At, B1); PG8_BAR; PG8_SCHED;
;             PG8_LDB(B0, 1, 0); PG8_LDB(B1, 1, 1); PG8_SCHED; PG8_LDA(At, 1, 0); PG8_STAGE(PG8_SA(0, 1), a2 + hstepA, PG8_OS(1));
;             PG8_WAIT_V(8); PG8_WAIT_L(0); PG8_BAR; PG8_MMA(0, 0, At, B0); PG8_MMA(0, 1, At, B1); PG8_BAR; PG8_SCHED;
.Lew20_b:
	s_mov_b32 s97, 0
	s_waitcnt lgkmcnt(0)
	v_mfma_f32_16x16x32_bf16 v[62:65], v[142:145], v[182:185], v[62:65]
	v_mfma_f32_16x16x32_bf16 v[58:61], v[158:161], v[182:185], v[58:61]
	v_mfma_f32_16x16x32_bf16 v[46:49], v[142:145], v[190:193], v[46:49]
	s_barrier
	s_setprio 1
	s_waitcnt lgkmcnt(0)
	v_mfma_f32_16x16x32_bf16 v[42:45], v[158:161], v[190:193], v[42:45]
	v_mfma_f32_16x16x32_bf16 v[30:33], v[142:145], v[198:201], v[30:33]
	v_mfma_f32_16x16x32_bf16 v[26:29], v[158:161], v[198:201], v[26:29]
	v_mfma_f32_16x16x32_bf16 v[14:17], v[142:145], v[206:209], v[14:17]
	v_mfma_f32_16x16x32_bf16 v[10:13], v[158:161], v[206:209], v[10:13]
	v_mfma_f32_16x16x32_bf16 v[62:65], v[154:157], v[186:189], v[62:65]
	v_mfma_f32_16x16x32_bf16 v[58:61], v[162:165], v[186:189], v[58:61]
	v_mfma_f32_16x16x32_bf16 v[46:49], v[154:157], v[194:197], v[46:49]
	v_mfma_f32_16x16x32_bf16 v[42:45], v[162:165], v[194:197], v[42:45]
	v_mfma_f32_16x16x32_bf16 v[30:33], v[154:157], v[202:205], v[30:33]
	v_mfma_f32_16x16x32_bf16 v[26:29], v[162:165], v[202:205], v[26:29]
	v_mfma_f32_16x16x32_bf16 v[14:17], v[154:157], v[210:213], v[14:17]
	v_mfma_f32_16x16x32_bf16 v[10:13], v[162:165], v[210:213], v[10:13]
	s_setprio 0
	s_setprio 1
	v_mfma_f32_16x16x32_bf16 v[54:57], v[166:169], v[182:185], v[54:57]
	v_mfma_f32_16x16x32_bf16 v[50:53], v[174:177], v[182:185], v[50:53]
	v_mfma_f32_16x16x32_bf16 v[38:41], v[166:169], v[190:193], v[38:41]
	v_mfma_f32_16x16x32_bf16 v[34:37], v[174:177], v[190:193], v[34:37]
	v_mfma_f32_16x16x32_bf16 v[22:25], v[166:169], v[198:201], v[22:25]
	v_mfma_f32_16x16x32_bf16 v[18:21], v[174:177], v[198:201], v[18:21]
	v_mfma_f32_16x16x32_bf16 v[6:9], v[166:169], v[206:209], v[6:9]
	v_mfma_f32_16x16x32_bf16 v[2:5], v[174:177], v[206:209], v[2:5]
	v_mfma_f32_16x16x32_bf16 v[54:57], v[170:173], v[186:189], v[54:57]
	v_mfma_f32_16x16x32_bf16 v[50:53], v[178:181], v[186:189], v[50:53]
	v_mfma_f32_16x16x32_bf16 v[38:41], v[170:173], v[194:197], v[38:41]
	v_mfma_f32_16x16x32_bf16 v[34:37], v[178:181], v[194:197], v[34:37]
	v_mfma_f32_16x16x32_bf16 v[22:25], v[170:173], v[202:205], v[22:25]
	v_mfma_f32_16x16x32_bf16 v[18:21], v[178:181], v[202:205], v[18:21]
	v_mfma_f32_16x16x32_bf16 v[6:9], v[170:173], v[210:213], v[6:9]
	v_mfma_f32_16x16x32_bf16 v[2:5], v[178:181], v[210:213], v[2:5]
	s_setprio 0
	s_barrier
	s_add_i32 s58, 0, 0x18000
	v_add_u32_e32 v0, s58, v151
	s_add_i32 s59, 0, 0x1c000
	ds_read_b128 v[142:145], v0
	ds_read_b128 v[154:157], v0 offset:1024
	ds_read_b128 v[158:161], v0 offset:2048
	ds_read_b128 v[162:165], v0 offset:3072
	v_add_u32_e32 v0, s59, v151
	ds_read_b128 v[166:169], v0
	ds_read_b128 v[170:173], v0 offset:1024
	ds_read_b128 v[174:177], v0 offset:2048
	ds_read_b128 v[178:181], v0 offset:3072
	s_add_u32 s30, s30, 0x40000
	s_addc_u32 s31, s31, 0
	s_mov_b32 m0, s49
	v_lshl_add_u64 v[220:221], s[30:31], 0, v[136:137]
	ds_read_b128 v[182:185], v153 offset:32768
	ds_read_b128 v[186:189], v153 offset:33792
	ds_read_b128 v[190:193], v153 offset:34816
	ds_read_b128 v[194:197], v153 offset:35840
	ds_read_b128 v[198:201], v153 offset:36864
	ds_read_b128 v[202:205], v153 offset:37888
	ds_read_b128 v[206:209], v153 offset:38912
	ds_read_b128 v[210:213], v153 offset:39936
	global_load_lds_dwordx4 v[220:221], off
	v_lshl_add_u64 v[220:221], s[30:31], 0, v[132:133]
	s_mov_b32 m0, s50
	s_nop 0
	global_load_lds_dwordx4 v[220:221], off
	s_waitcnt vmcnt(8)
	s_waitcnt lgkmcnt(0)
	v_mfma_f32_16x16x32_bf16 v[126:129], v[142:145], v[182:185], v[126:129]
	v_mfma_f32_16x16x32_bf16 v[122:125], v[158:161], v[182:185], v[122:125]
	v_mfma_f32_16x16x32_bf16 v[110:113], v[142:145], v[190:193], v[110:113]
	s_barrier
	s_setprio 1
	s_waitcnt lgkmcnt(0)
	v_mfma_f32_16x16x32_bf16 v[106:109], v[158:161], v[190:193], v[106:109]
	v_mfma_f32_16x16x32_bf16 v[94:97], v[142:145], v[198:201], v[94:97]
	v_mfma_f32_16x16x32_bf16 v[90:93], v[158:161], v[198:201], v[90:93]
	v_mfma_f32_16x16x32_bf16 v[78:81], v[142:145], v[206:209], v[78:81]
	v_mfma_f32_16x16x32_bf16 v[74:77], v[158:161], v[206:209], v[74:77]
	v_mfma_f32_16x16x32_bf16 v[126:129], v[154:157], v[186:189], v[126:129]
	v_mfma_f32_16x16x32_bf16 v[122:125], v[162:165], v[186:189], v[122:125]
	v_mfma_f32_16x16x32_bf16 v[110:113], v[154:157], v[194:197], v[110:113]
	v_mfma_f32_16x16x32_bf16 v[106:109], v[162:165], v[194:197], v[106:109]
	v_mfma_f32_16x16x32_bf16 v[94:97], v[154:157], v[202:205], v[94:97]
	v_mfma_f32_16x16x32_bf16 v[90:93], v[162:165], v[202:205], v[90:93]
	v_mfma_f32_16x16x32_bf16 v[78:81], v[154:157], v[210:213], v[78:81]
	v_mfma_f32_16x16x32_bf16 v[74:77], v[162:165], v[210:213], v[74:77]
	s_setprio 0
	s_setprio 1
	v_mfma_f32_16x16x32_bf16 v[118:121], v[166:169], v[182:185], v[118:121]
	v_mfma_f32_16x16x32_bf16 v[114:117], v[174:177], v[182:185], v[114:117]
	v_mfma_f32_16x16x32_bf16 v[102:105], v[166:169], v[190:193], v[102:105]
	v_mfma_f32_16x16x32_bf16 v[98:101], v[174:177], v[190:193], v[98:101]
	v_mfma_f32_16x16x32_bf16 v[86:89], v[166:169], v[198:201], v[86:89]
	v_mfma_f32_16x16x32_bf16 v[82:85], v[174:177], v[198:201], v[82:85]
	v_mfma_f32_16x16x32_bf16 v[70:73], v[166:169], v[206:209], v[70:73]
	v_mfma_f32_16x16x32_bf16 v[66:69], v[174:177], v[206:209], v[66:69]
	v_mfma_f32_16x16x32_bf16 v[118:121], v[170:173], v[186:189], v[118:121]
	v_mfma_f32_16x16x32_bf16 v[114:117], v[178:181], v[186:189], v[114:117]
	v_mfma_f32_16x16x32_bf16 v[102:105], v[170:173], v[194:197], v[102:105]
	v_mfma_f32_16x16x32_bf16 v[98:101], v[178:181], v[194:197], v[98:101]
	v_mfma_f32_16x16x32_bf16 v[86:89], v[170:173], v[202:205], v[86:89]
	v_mfma_f32_16x16x32_bf16 v[82:85], v[178:181], v[202:205], v[82:85]
	v_mfma_f32_16x16x32_bf16 v[70:73], v[170:173], v[210:213], v[70:73]
	v_mfma_f32_16x16x32_bf16 v[66:69], v[178:181], v[210:213], v[66:69]
	s_setprio 0
	s_barrier
; #define PG8_STAGE(bufoff, gbase, voff) do { _Pragma("unroll") for (int _i = 0; _i < 2; ++_i) \
;         __builtin_amdgcn_global_load_lds((const unsigned*)((const char*)(gbase) + (voff)[_i]), (PG8_LAS unsigned*)(lds + (bufoff) + ldsw + _i * 8192), 16, 0, 0); } while (0)
; #define PG8_LDA(dst, b, h) do { _Pragma("unroll") for (int m = 0; m < 4; ++m) _Pragma("unroll") for (int k = 0; k < 2; ++k) dst[m][k] = *(const PG8_LAS bf16x8*)(lds + PG8_SA(b, h) + aoff + m * 2048 + k * 1024); } while (0)
; #define PG8_MMA(ai, bj, At, Bt) do { __builtin_amdgcn_s_setprio(1); _Pragma("unroll") for (int m = 0; m < 4; ++m) _Pragma("unroll") for (int n = 0; n < 2; ++n) _Pragma("unroll") for (int k = 0; k < 2; ++k) \
;         acc[ai][bj][m][n] = __builtin_amdgcn_mfma_f32_16x16x32_bf16(Bt[n][k], At[m][k], acc[ai][bj][m][n], 0, 0, 0); __builtin_amdgcn_s_setprio(0); } while (0)
; #define PG8_WAIT_V(n) asm volatile("s_waitcnt vmcnt(" #n ")" ::: "memory")
; #define PG8_WAIT_L(n) asm volatile("s_waitcnt lgkmcnt(" #n ")" ::: "memory")
; #define PG8_BAR __builtin_amdgcn_s_barrier()
; #define PG8_SCHED __builtin_amdgcn_sched_barrier(0)
; template <class Epi, class Sched, bool ALIGN_EPI = false, bool SP2 = false, bool GATHER = false>
; __device__ __forceinline__ void gemm_phase(PG8_LAS unsigned char* lds, const Gemm g, const Sched& S, const Epi& E, int tid_in, const int* rowsrc = nullptr, PG8_LAS int* idx_lds = nullptr) {
;     ...
;             PG8_LDA(At, 1, 1); PG8_STAGE(PG8_SB(1, 0), b3, voffB); PG8_STAGE(PG8_SB(1, 1), b3 + hstep, voffB); PG8_STAGE(PG8_SA(1, 0), a3, PG8_OS(0));
;             PG8_WAIT_V(8); PG8_WAIT_L(0); PG8_BAR; PG8_MMA(1, 0, At, B0); PG8_MMA(1, 1, At, B1); PG8_BAR; PG8_SCHED;
;     ...
;         if constexpr (ALIGN_EPI) { if (wr == 0) PG8_BAR; }
	s_add_i32 s30, s58, s44
	v_lshl_add_u64 v[148:149], v[148:149], 0, s[10:11]
	s_mov_b32 m0, s30
	ds_read_b128 v[182:185], v153 offset:49152
	ds_read_b128 v[186:189], v153 offset:50176
	ds_read_b128 v[190:193], v153 offset:51200
	ds_read_b128 v[194:197], v153 offset:52224
	ds_read_b128 v[198:201], v153 offset:53248
	ds_read_b128 v[202:205], v153 offset:54272
	ds_read_b128 v[206:209], v153 offset:55296
	ds_read_b128 v[210:213], v153 offset:56320
	global_load_lds_dwordx4 v[148:149], off
	s_add_i32 m0, s30, 0x2000
	s_add_u32 s28, s28, 0x40080
	v_lshl_add_u64 v[148:149], v[214:215], 0, s[10:11]
	s_addc_u32 s29, s29, 0
	s_add_i32 s30, s59, s44
	global_load_lds_dwordx4 v[148:149], off
	v_lshl_add_u64 v[148:149], s[28:29], 0, v[134:135]
	s_mov_b32 m0, s30
	s_nop 0
	global_load_lds_dwordx4 v[148:149], off
	v_lshl_add_u64 v[148:149], s[28:29], 0, v[130:131]
	s_add_i32 m0, s30, 0x2000
	s_nop 0
	global_load_lds_dwordx4 v[148:149], off
	v_lshl_add_u64 v[148:149], v[216:217], 0, s[10:11]
	s_mov_b32 m0, s51
	s_nop 0
	global_load_lds_dwordx4 v[148:149], off
	v_lshl_add_u64 v[148:149], v[218:219], 0, s[10:11]
	s_mov_b32 m0, s52
	s_nop 0
	global_load_lds_dwordx4 v[148:149], off
	s_waitcnt vmcnt(8)
	s_waitcnt lgkmcnt(0)
	v_mfma_f32_16x16x32_bf16 v[62:65], v[142:145], v[182:185], v[62:65]
	v_mfma_f32_16x16x32_bf16 v[58:61], v[158:161], v[182:185], v[58:61]
	v_mfma_f32_16x16x32_bf16 v[46:49], v[142:145], v[190:193], v[46:49]
	s_barrier
	s_setprio 1
	s_waitcnt lgkmcnt(0)
	v_mfma_f32_16x16x32_bf16 v[42:45], v[158:161], v[190:193], v[42:45]
	v_mfma_f32_16x16x32_bf16 v[30:33], v[142:145], v[198:201], v[30:33]
	v_mfma_f32_16x16x32_bf16 v[26:29], v[158:161], v[198:201], v[26:29]
	v_mfma_f32_16x16x32_bf16 v[14:17], v[142:145], v[206:209], v[14:17]
	v_mfma_f32_16x16x32_bf16 v[10:13], v[158:161], v[206:209], v[10:13]
	v_mfma_f32_16x16x32_bf16 v[62:65], v[154:157], v[186:189], v[62:65]
	v_mfma_f32_16x16x32_bf16 v[58:61], v[162:165], v[186:189], v[58:61]
	v_mfma_f32_16x16x32_bf16 v[46:49], v[154:157], v[194:197], v[46:49]
	v_mfma_f32_16x16x32_bf16 v[42:45], v[162:165], v[194:197], v[42:45]
	v_mfma_f32_16x16x32_bf16 v[30:33], v[154:157], v[202:205], v[30:33]
	v_mfma_f32_16x16x32_bf16 v[26:29], v[162:165], v[202:205], v[26:29]
	v_mfma_f32_16x16x32_bf16 v[14:17], v[154:157], v[210:213], v[14:17]
	v_mfma_f32_16x16x32_bf16 v[10:13], v[162:165], v[210:213], v[10:13]
	s_setprio 0
	s_setprio 1
	v_mfma_f32_16x16x32_bf16 v[54:57], v[166:169], v[182:185], v[54:57]
	v_mfma_f32_16x16x32_bf16 v[50:53], v[174:177], v[182:185], v[50:53]
	v_mfma_f32_16x16x32_bf16 v[38:41], v[166:169], v[190:193], v[38:41]
	v_mfma_f32_16x16x32_bf16 v[34:37], v[174:177], v[190:193], v[34:37]
	v_mfma_f32_16x16x32_bf16 v[22:25], v[166:169], v[198:201], v[22:25]
	v_mfma_f32_16x16x32_bf16 v[18:21], v[174:177], v[198:201], v[18:21]
	v_mfma_f32_16x16x32_bf16 v[6:9], v[166:169], v[206:209], v[6:9]
	v_mfma_f32_16x16x32_bf16 v[2:5], v[174:177], v[206:209], v[2:5]
	v_mfma_f32_16x16x32_bf16 v[54:57], v[170:173], v[186:189], v[54:57]
	v_mfma_f32_16x16x32_bf16 v[50:53], v[178:181], v[186:189], v[50:53]
	v_mfma_f32_16x16x32_bf16 v[38:41], v[170:173], v[194:197], v[38:41]
	v_mfma_f32_16x16x32_bf16 v[34:37], v[178:181], v[194:197], v[34:37]
	v_mfma_f32_16x16x32_bf16 v[22:25], v[170:173], v[202:205], v[22:25]
	v_mfma_f32_16x16x32_bf16 v[18:21], v[178:181], v[202:205], v[18:21]
	v_mfma_f32_16x16x32_bf16 v[6:9], v[170:173], v[210:213], v[6:9]
	v_mfma_f32_16x16x32_bf16 v[2:5], v[178:181], v[210:213], v[2:5]
	s_setprio 0
	s_barrier
	s_add_i32 s57, s57, 2
	s_add_u32 s26, s26, 0x100
	s_addc_u32 s27, s27, 0
	s_add_u32 s55, s55, 0x100
	s_addc_u32 s56, s56, 0
	s_cmp_gt_u32 s57, 13
	s_cbranch_scc0 .LBB0_2005
	s_mov_b32 s97, 1
	s_and_b64 vcc, exec, s[8:9]
	s_cbranch_vccz .LBB0_2008
	s_barrier
